# v20 + nt hint on the conv phase's single-use reads of the up-projection output
# speedup vs baseline: 1.0088x; 1.0007x over previous
; #define CV_LOAD(G_, V_, r0_) do { _Pragma("unroll") for (int i_ = 0; i_ < 8; ++i_) { G_[i_] = *(const GAS v2u*)(ap + (size_t)((r0_) + i_) * F2); V_[i_] = *(const GAS v2u*)(ap + (size_t)((r0_) + i_) * F2 + 128); } } while (0)
; __device__ __forceinline__ void conv_phase(Frame& F) {
;     ...
;         CV_LOAD(GA, VA, 0); CV_LOAD(GB, VB, 8); CV_COMP(GA, VA, 0); CV_LOAD(GA, VA, 16); CV_COMP(GB, VB, 8); CV_LOAD(GB, VB, 24); CV_COMP(GA, VA, 16); CV_COMP(GB, VB, 24);
.LBB0_2568:
	s_or_b64 exec, exec, s[22:23]
	v_add_co_u32_e32 v74, vcc, s25, v72
	s_waitcnt vmcnt(14)
	v_pk_mul_f32 v[62:63], v[62:63], s[20:21] op_sel_hi:[1,0]
	v_addc_co_u32_e32 v75, vcc, 0, v73, vcc
	global_load_dwordx2 v[160:161], v[72:73], off nt
	global_load_dwordx2 v[176:177], v[72:73], off offset:128 nt
	global_load_dwordx2 v[182:183], v[74:75], off offset:1536 nt
	global_load_dwordx2 v[170:171], v[74:75], off offset:1664 nt
	v_add_co_u32_e32 v74, vcc, s26, v72
	s_waitcnt vmcnt(14)
	v_pk_mul_f32 v[50:51], v[50:51], s[20:21] op_sel_hi:[1,0]
	v_addc_co_u32_e32 v75, vcc, 0, v73, vcc
	v_add_co_u32_e32 v76, vcc, s27, v72
	s_waitcnt vmcnt(6)
	v_pk_fma_f32 v[152:153], v[62:63], v[152:153], v[14:15]
	v_addc_co_u32_e32 v77, vcc, 0, v73, vcc
	global_load_dwordx2 v[156:157], v[74:75], off offset:3072 nt
	global_load_dwordx2 v[154:155], v[74:75], off offset:3200 nt
	global_load_dwordx2 v[140:141], v[76:77], off offset:512 nt
	global_load_dwordx2 v[138:139], v[76:77], off offset:640 nt
	v_add_co_u32_e32 v74, vcc, s28, v72
	v_pk_mul_f32 v[34:35], v[34:35], s[20:21] op_sel_hi:[1,0]
	s_nop 0
	v_addc_co_u32_e32 v75, vcc, 0, v73, vcc
	v_add_co_u32_e32 v76, vcc, s29, v72
	v_pk_fma_f32 v[152:153], v[50:51], v[132:133], v[152:153]
	s_nop 0
	v_addc_co_u32_e32 v77, vcc, 0, v73, vcc
	global_load_dwordx2 v[104:105], v[74:75], off offset:2048 nt
	global_load_dwordx2 v[100:101], v[74:75], off offset:2176 nt
	global_load_dwordx2 v[96:97], v[76:77], off offset:3584 nt
	global_load_dwordx2 v[92:93], v[76:77], off offset:3712 nt
	v_add_co_u32_e32 v74, vcc, s30, v72
	v_pk_mul_f32 v[64:65], v[64:65], s[20:21] op_sel_hi:[1,0]
	s_nop 0
	v_addc_co_u32_e32 v75, vcc, 0, v73, vcc
	v_add_co_u32_e32 v76, vcc, s31, v72
	v_pk_mul_f32 v[52:53], v[52:53], s[20:21] op_sel_hi:[1,0]
	s_nop 0
	v_addc_co_u32_e32 v77, vcc, 0, v73, vcc
	global_load_dwordx2 v[88:89], v[74:75], off offset:1024 nt
	global_load_dwordx2 v[84:85], v[74:75], off offset:1152 nt
	global_load_dwordx2 v[80:81], v[76:77], off offset:2560 nt
	s_nop 0
	global_load_dwordx2 v[76:77], v[76:77], off offset:2688 nt
	v_add_co_u32_e32 v74, vcc, s33, v72
	v_pk_fma_f32 v[148:149], v[64:65], v[148:149], v[16:17]
	s_nop 0
	v_addc_co_u32_e32 v75, vcc, 0, v73, vcc
	v_add_co_u32_e32 v78, vcc, s34, v72
	v_pk_mul_f32 v[36:37], v[36:37], s[20:21] op_sel_hi:[1,0]
	s_nop 0
	v_addc_co_u32_e32 v79, vcc, 0, v73, vcc
	global_load_dwordx2 v[134:135], v[74:75], off nt
	global_load_dwordx2 v[130:131], v[74:75], off offset:128 nt
	global_load_dwordx2 v[126:127], v[78:79], off offset:1536 nt
	global_load_dwordx2 v[122:123], v[78:79], off offset:1664 nt
	v_add_co_u32_e32 v74, vcc, s35, v72
	v_pk_fma_f32 v[148:149], v[52:53], v[124:125], v[148:149]
	s_nop 0
	v_addc_co_u32_e32 v75, vcc, 0, v73, vcc
	v_add_co_u32_e32 v78, vcc, s36, v72
	v_pk_mul_f32 v[58:59], v[58:59], s[20:21] op_sel_hi:[1,0]
	s_nop 0
	v_addc_co_u32_e32 v79, vcc, 0, v73, vcc
	global_load_dwordx2 v[118:119], v[74:75], off offset:3072 nt
	global_load_dwordx2 v[114:115], v[74:75], off offset:3200 nt
	global_load_dwordx2 v[110:111], v[78:79], off offset:512 nt
	global_load_dwordx2 v[106:107], v[78:79], off offset:640 nt
	v_add_co_u32_e32 v74, vcc, s37, v72
	v_pk_mul_f32 v[42:43], v[42:43], s[20:21] op_sel_hi:[1,0]
	s_nop 0
	v_addc_co_u32_e32 v75, vcc, 0, v73, vcc
	v_add_co_u32_e32 v78, vcc, s38, v72
	s_waitcnt vmcnt(24)
	v_pk_fma_f32 v[158:159], v[58:59], v[158:159], v[10:11]
	v_addc_co_u32_e32 v79, vcc, 0, v73, vcc
	global_load_dwordx2 v[102:103], v[74:75], off offset:2048 nt
	global_load_dwordx2 v[98:99], v[74:75], off offset:2176 nt
	global_load_dwordx2 v[94:95], v[78:79], off offset:3584 nt
	global_load_dwordx2 v[90:91], v[78:79], off offset:3712 nt
	v_add_co_u32_e32 v74, vcc, s39, v72
	v_pk_mul_f32 v[26:27], v[26:27], s[20:21] op_sel_hi:[1,0]
	s_nop 0
	v_addc_co_u32_e32 v75, vcc, 0, v73, vcc
	v_add_co_u32_e32 v162, vcc, s40, v72
	v_pk_fma_f32 v[158:159], v[42:43], v[136:137], v[158:159]
	s_nop 0
	v_addc_co_u32_e32 v163, vcc, 0, v73, vcc
	s_waitcnt vmcnt(27)
	v_cvt_pk_f32_fp8_e32 v[178:179], v160
	v_cvt_pk_f32_fp8_sdwa v[168:169], v160 src0_sel:WORD_1
	s_waitcnt vmcnt(26)
	v_cvt_pk_f32_fp8_e32 v[172:173], v176
	v_cvt_pk_f32_fp8_sdwa v[166:167], v176 src0_sel:WORD_1
	v_pk_fma_f32 v[180:181], v[34:35], v[178:179], v[152:153]
	global_load_dwordx2 v[86:87], v[74:75], off offset:1024 nt
	global_load_dwordx2 v[82:83], v[74:75], off offset:1152 nt
	global_load_dwordx2 v[78:79], v[162:163], off offset:2560 nt
	s_nop 0
	global_load_dwordx2 v[74:75], v[162:163], off offset:2688 nt
	v_mul_f32_e32 v152, 0xbfb8aa3b, v180
	v_exp_f32_e32 v175, v152
	v_mul_f32_e32 v152, 0xbfb8aa3b, v181
	v_exp_f32_e32 v184, v152
	v_cvt_pk_f32_fp8_e32 v[162:163], v177
	v_add_f32_e32 v175, 1.0, v175
	v_rcp_f32_e32 v176, v175
	v_add_f32_e32 v175, 1.0, v184
	v_cvt_pk_f32_fp8_sdwa v[152:153], v177 src0_sel:WORD_1
	v_rcp_f32_e32 v177, v175
	v_pk_fma_f32 v[148:149], v[36:37], v[168:169], v[148:149]
	v_pk_fma_f32 v[158:159], v[26:27], v[172:173], v[158:159]
	v_mul_f32_e32 v175, 0xbfb8aa3b, v148
	v_pk_mul_f32 v[176:177], v[180:181], v[176:177]
	v_exp_f32_e32 v175, v175
	v_mul_f32_e32 v180, 0xbfb8aa3b, v149
	v_exp_f32_e32 v180, v180
	v_pk_mul_f32 v[158:159], v[158:159], 4.0 op_sel_hi:[1,0]
	v_add_f32_e32 v175, 1.0, v175
	v_cvt_pk_f32_fp8_e32 v[164:165], v161
	v_pk_mul_f32 v[158:159], v[158:159], v[176:177]
	v_rcp_f32_e32 v176, v175
	v_add_f32_e32 v175, 1.0, v180
	v_pk_mul_f32 v[54:55], v[54:55], s[20:21] op_sel_hi:[1,0]
	v_rcp_f32_e32 v177, v175
	v_pk_mul_f32 v[38:39], v[38:39], s[20:21] op_sel_hi:[1,0]
	v_pk_fma_f32 v[144:145], v[54:55], v[144:145], v[6:7]
	v_pk_mul_f32 v[22:23], v[22:23], s[20:21] op_sel_hi:[1,0]
; __device__ __forceinline__ void unpack8_fp8(v2u w, f32x2 (&o)[4]) {
;     o[0] = __builtin_amdgcn_cvt_pk_f32_fp8((int)w.x, false); o[1] = __builtin_amdgcn_cvt_pk_f32_fp8((int)w.x, true); o[2] = __builtin_amdgcn_cvt_pk_f32_fp8((int)w.y, false); o[3] = __builtin_amdgcn_cvt_pk_f32_fp8((int)w.y, true);
; }
	v_pk_fma_f32 v[144:145], v[38:39], v[116:117], v[144:145]
	v_pk_mul_f32 v[60:61], v[60:61], s[20:21] op_sel_hi:[1,0]
	v_pk_fma_f32 v[144:145], v[22:23], v[164:165], v[144:145]
	v_pk_mul_f32 v[148:149], v[148:149], v[176:177]
	v_mul_f32_e32 v175, 0xbfb8aa3b, v144
	v_mul_f32_e32 v176, 0xbfb8aa3b, v145
	v_pk_mul_f32 v[44:45], v[44:45], s[20:21] op_sel_hi:[1,0]
	v_pk_fma_f32 v[150:151], v[60:61], v[150:151], v[12:13]
	v_exp_f32_e32 v175, v175
	v_exp_f32_e32 v176, v176
	v_pk_mul_f32 v[28:29], v[28:29], s[20:21] op_sel_hi:[1,0]
	v_pk_fma_f32 v[150:151], v[44:45], v[128:129], v[150:151]
	v_cvt_pk_f32_fp8_sdwa v[160:161], v161 src0_sel:WORD_1
	v_pk_fma_f32 v[150:151], v[28:29], v[166:167], v[150:151]
	v_pk_mul_f32 v[56:57], v[56:57], s[20:21] op_sel_hi:[1,0]
	v_pk_mul_f32 v[150:151], v[150:151], 4.0 op_sel_hi:[1,0]
	v_pk_mul_f32 v[40:41], v[40:41], s[20:21] op_sel_hi:[1,0]
	v_pk_mul_f32 v[148:149], v[150:151], v[148:149]
	v_add_f32_e32 v150, 1.0, v175
	v_add_f32_e32 v151, 1.0, v176
	v_rcp_f32_e32 v150, v150
	v_rcp_f32_e32 v151, v151
	v_pk_fma_f32 v[70:71], v[56:57], v[70:71], v[8:9]
	v_pk_mul_f32 v[24:25], v[24:25], s[20:21] op_sel_hi:[1,0]
	v_pk_fma_f32 v[70:71], v[40:41], v[108:109], v[70:71]
	v_pk_mul_f32 v[46:47], v[46:47], s[20:21] op_sel_hi:[1,0]
	v_pk_fma_f32 v[70:71], v[24:25], v[160:161], v[70:71]
	v_pk_mul_f32 v[144:145], v[144:145], v[150:151]
	v_mul_f32_e32 v150, 0xbfb8aa3b, v70
	v_mul_f32_e32 v151, 0xbfb8aa3b, v71
	v_pk_mul_f32 v[30:31], v[30:31], s[20:21] op_sel_hi:[1,0]
	v_pk_fma_f32 v[146:147], v[46:47], v[146:147], v[2:3]
	v_exp_f32_e32 v150, v150
	v_exp_f32_e32 v151, v151
	v_pk_mul_f32 v[18:19], v[18:19], s[20:21] op_sel_hi:[1,0]
	v_pk_fma_f32 v[146:147], v[30:31], v[120:121], v[146:147]
	v_pk_mul_f32 v[48:49], v[48:49], s[20:21] op_sel_hi:[1,0]
	v_pk_fma_f32 v[146:147], v[18:19], v[162:163], v[146:147]
	v_pk_mul_f32 v[32:33], v[32:33], s[20:21] op_sel_hi:[1,0]
	v_pk_mul_f32 v[146:147], v[146:147], 4.0 op_sel_hi:[1,0]
	v_pk_fma_f32 v[142:143], v[48:49], v[142:143], v[4:5]
	v_pk_mul_f32 v[144:145], v[146:147], v[144:145]
	v_add_f32_e32 v146, 1.0, v150
	v_add_f32_e32 v147, 1.0, v151
	v_rcp_f32_e32 v146, v146
	v_rcp_f32_e32 v147, v147
	v_pk_mul_f32 v[20:21], v[20:21], s[20:21] op_sel_hi:[1,0]
	v_pk_fma_f32 v[142:143], v[32:33], v[112:113], v[142:143]
	v_med3_f32 v144, v144, s41, v1
	v_pk_fma_f32 v[142:143], v[20:21], v[152:153], v[142:143]
	v_pk_mul_f32 v[70:71], v[70:71], v[146:147]
	v_pk_mul_f32 v[142:143], v[142:143], 4.0 op_sel_hi:[1,0]
	v_med3_f32 v146, v159, s41, v1
	v_pk_mul_f32 v[70:71], v[142:143], v[70:71]
	v_med3_f32 v143, v158, s41, v1
	v_mov_b32_e32 v142, v69
	v_cvt_pk_fp8_f32 v142, v143, v146
	v_med3_f32 v145, v145, s41, v1
	v_mov_b32_e32 v143, v69
	v_cvt_pk_fp8_f32 v143, v144, v145
	s_waitcnt vmcnt(29)
	v_cvt_pk_f32_fp8_e32 v[180:181], v182
	v_med3_f32 v70, v70, s41, v1
	v_med3_f32 v71, v71, s41, v1
	v_pk_fma_f32 v[132:133], v[62:63], v[132:133], v[14:15]
	v_cvt_pk_fp8_f32 v143, v70, v71 op_sel:[0,0,1]
	v_mul_u32_u24_e32 v70, 0x56000, v174
	v_mov_b32_e32 v71, v69
	v_pk_fma_f32 v[132:133], v[50:51], v[178:179], v[132:133]
	v_med3_f32 v146, v148, s41, v1
	v_med3_f32 v147, v149, s41, v1
	v_lshl_add_u64 v[70:71], s[4:5], 0, v[70:71]
	v_pk_fma_f32 v[148:149], v[34:35], v[180:181], v[132:133]
	v_lshl_add_u64 v[70:71], v[70:71], 0, v[68:69]
	v_mul_f32_e32 v68, 0xbfb8aa3b, v148
	v_exp_f32_e32 v68, v68
	v_mul_f32_e32 v132, 0xbfb8aa3b, v149
	v_exp_f32_e32 v176, v132
	v_cvt_pk_f32_fp8_sdwa v[158:159], v182 src0_sel:WORD_1
	v_add_f32_e32 v68, 1.0, v68
	s_waitcnt vmcnt(28)
	v_cvt_pk_f32_fp8_e32 v[174:175], v170
	v_cvt_pk_f32_fp8_sdwa v[150:151], v170 src0_sel:WORD_1
	v_rcp_f32_e32 v170, v68
	v_add_f32_e32 v68, 1.0, v176
	v_cvt_pk_f32_fp8_e32 v[144:145], v171
	v_cvt_pk_f32_fp8_sdwa v[132:133], v171 src0_sel:WORD_1
	v_rcp_f32_e32 v171, v68
	v_pk_fma_f32 v[124:125], v[64:65], v[124:125], v[16:17]
	v_pk_fma_f32 v[136:137], v[58:59], v[136:137], v[10:11]
	v_pk_fma_f32 v[124:125], v[52:53], v[168:169], v[124:125]
	v_pk_mul_f32 v[148:149], v[148:149], v[170:171]
	v_pk_fma_f32 v[124:125], v[36:37], v[158:159], v[124:125]
	v_pk_fma_f32 v[136:137], v[42:43], v[172:173], v[136:137]
	v_mul_f32_e32 v68, 0xbfb8aa3b, v124
	v_exp_f32_e32 v68, v68
	v_mul_f32_e32 v170, 0xbfb8aa3b, v125
	v_exp_f32_e32 v170, v170
	v_pk_fma_f32 v[136:137], v[26:27], v[174:175], v[136:137]
	v_cvt_pk_fp8_f32 v142, v146, v147 op_sel:[0,0,1]
	v_cvt_pk_f32_fp8_e32 v[146:147], v183
	v_pk_mul_f32 v[136:137], v[136:137], 4.0 op_sel_hi:[1,0]
	v_add_f32_e32 v68, 1.0, v68
	v_pk_mul_f32 v[136:137], v[136:137], v[148:149]
	v_rcp_f32_e32 v148, v68
	v_add_f32_e32 v68, 1.0, v170
	v_rcp_f32_e32 v149, v68
	v_pk_fma_f32 v[116:117], v[54:55], v[116:117], v[6:7]
	v_pk_fma_f32 v[128:129], v[60:61], v[128:129], v[12:13]
	v_pk_fma_f32 v[116:117], v[38:39], v[164:165], v[116:117]
	v_pk_mul_f32 v[124:125], v[124:125], v[148:149]
	v_pk_fma_f32 v[116:117], v[22:23], v[146:147], v[116:117]
	v_pk_fma_f32 v[128:129], v[44:45], v[166:167], v[128:129]
	v_mul_f32_e32 v68, 0xbfb8aa3b, v116
	v_exp_f32_e32 v68, v68
	v_mul_f32_e32 v148, 0xbfb8aa3b, v117
	v_exp_f32_e32 v148, v148
	v_pk_fma_f32 v[128:129], v[28:29], v[150:151], v[128:129]
	global_store_dwordx2 v[70:71], v[142:143], off
	v_cvt_pk_f32_fp8_sdwa v[142:143], v183 src0_sel:WORD_1
	v_pk_mul_f32 v[128:129], v[128:129], 4.0 op_sel_hi:[1,0]
	v_add_f32_e32 v68, 1.0, v68
	v_pk_mul_f32 v[124:125], v[128:129], v[124:125]
	v_rcp_f32_e32 v128, v68
	v_add_f32_e32 v68, 1.0, v148
	v_rcp_f32_e32 v129, v68
	v_pk_fma_f32 v[108:109], v[56:57], v[108:109], v[8:9]
	v_pk_fma_f32 v[120:121], v[46:47], v[120:121], v[2:3]
	v_pk_fma_f32 v[108:109], v[40:41], v[160:161], v[108:109]
	v_pk_mul_f32 v[116:117], v[116:117], v[128:129]
	v_pk_fma_f32 v[108:109], v[24:25], v[142:143], v[108:109]
	v_pk_fma_f32 v[120:121], v[30:31], v[162:163], v[120:121]
	v_mul_f32_e32 v68, 0xbfb8aa3b, v108
	v_exp_f32_e32 v68, v68
	v_mul_f32_e32 v128, 0xbfb8aa3b, v109
	v_exp_f32_e32 v128, v128
	v_pk_fma_f32 v[120:121], v[18:19], v[144:145], v[120:121]
	v_add_f32_e32 v68, 1.0, v68
	v_pk_mul_f32 v[120:121], v[120:121], 4.0 op_sel_hi:[1,0]
	v_pk_fma_f32 v[112:113], v[48:49], v[112:113], v[4:5]
	v_pk_mul_f32 v[116:117], v[120:121], v[116:117]
	v_rcp_f32_e32 v120, v68
	v_add_f32_e32 v68, 1.0, v128
	v_rcp_f32_e32 v121, v68
	v_pk_fma_f32 v[112:113], v[32:33], v[152:153], v[112:113]
	v_med3_f32 v68, v136, s41, v1
	v_pk_fma_f32 v[112:113], v[20:21], v[132:133], v[112:113]
	v_pk_mul_f32 v[108:109], v[108:109], v[120:121]
	v_pk_mul_f32 v[112:113], v[112:113], 4.0 op_sel_hi:[1,0]
	v_med3_f32 v116, v116, s41, v1
	v_pk_mul_f32 v[108:109], v[112:113], v[108:109]
	v_med3_f32 v113, v137, s41, v1
	v_mov_b32_e32 v112, v69
	v_cvt_pk_fp8_f32 v112, v68, v113
	v_med3_f32 v117, v117, s41, v1
	v_mov_b32_e32 v113, v69
	v_cvt_pk_fp8_f32 v113, v116, v117
	v_med3_f32 v68, v124, s41, v1
	v_med3_f32 v120, v125, s41, v1
	v_cvt_pk_fp8_f32 v112, v68, v120 op_sel:[0,0,1]
	v_med3_f32 v68, v108, s41, v1
	v_med3_f32 v108, v109, s41, v1
	v_cvt_pk_fp8_f32 v113, v68, v108 op_sel:[0,0,1]
	v_add_co_u32_e32 v108, vcc, s43, v70
	s_waitcnt vmcnt(28)
	v_cvt_pk_f32_fp8_e32 v[182:183], v156
	v_addc_co_u32_e32 v109, vcc, 0, v71, vcc
	global_store_dwordx2 v[108:109], v[112:113], off offset:2816
	v_pk_fma_f32 v[112:113], v[62:63], v[178:179], v[14:15]
	s_waitcnt vmcnt(28)
	v_cvt_pk_f32_fp8_e32 v[176:177], v154
	v_pk_fma_f32 v[112:113], v[50:51], v[180:181], v[112:113]
	v_pk_fma_f32 v[128:129], v[58:59], v[172:173], v[10:11]
	v_pk_fma_f32 v[112:113], v[34:35], v[182:183], v[112:113]
	v_cvt_pk_f32_fp8_sdwa v[170:171], v156 src0_sel:WORD_1
	v_mul_f32_e32 v68, 0xbfb8aa3b, v112
	v_exp_f32_e32 v68, v68
	v_mul_f32_e32 v116, 0xbfb8aa3b, v113
	v_exp_f32_e32 v121, v116
	v_pk_fma_f32 v[128:129], v[42:43], v[174:175], v[128:129]
	v_add_f32_e32 v68, 1.0, v68
	v_rcp_f32_e32 v120, v68
	v_add_f32_e32 v68, 1.0, v121
	v_rcp_f32_e32 v121, v68
	v_pk_fma_f32 v[128:129], v[26:27], v[176:177], v[128:129]
	v_cvt_pk_f32_fp8_e32 v[136:137], v157
	v_cvt_pk_f32_fp8_sdwa v[108:109], v157 src0_sel:WORD_1
	v_pk_mul_f32 v[112:113], v[112:113], v[120:121]
	v_pk_mul_f32 v[120:121], v[128:129], 4.0 op_sel_hi:[1,0]
	v_pk_fma_f32 v[128:129], v[64:65], v[168:169], v[16:17]
	v_cvt_pk_f32_fp8_sdwa v[156:157], v154 src0_sel:WORD_1
	v_pk_fma_f32 v[128:129], v[52:53], v[158:159], v[128:129]
	v_pk_mul_f32 v[112:113], v[120:121], v[112:113]
	v_pk_fma_f32 v[128:129], v[36:37], v[170:171], v[128:129]
	v_cvt_pk_f32_fp8_e32 v[124:125], v155
	v_mul_f32_e32 v68, 0xbfb8aa3b, v128
	v_exp_f32_e32 v68, v68
	v_mul_f32_e32 v148, 0xbfb8aa3b, v129
	v_exp_f32_e32 v148, v148
	v_cvt_pk_f32_fp8_sdwa v[116:117], v155 src0_sel:WORD_1
	v_add_f32_e32 v68, 1.0, v68
	v_rcp_f32_e32 v120, v68
	v_add_f32_e32 v68, 1.0, v148
	v_rcp_f32_e32 v121, v68
	v_pk_fma_f32 v[148:149], v[60:61], v[166:167], v[12:13]
	v_pk_fma_f32 v[152:153], v[48:49], v[152:153], v[4:5]
	v_pk_fma_f32 v[148:149], v[44:45], v[150:151], v[148:149]
	v_pk_mul_f32 v[120:121], v[128:129], v[120:121]
	v_pk_fma_f32 v[148:149], v[28:29], v[156:157], v[148:149]
	v_med3_f32 v113, v113, s41, v1
	v_pk_mul_f32 v[128:129], v[148:149], 4.0 op_sel_hi:[1,0]
	v_pk_fma_f32 v[148:149], v[54:55], v[164:165], v[6:7]
	v_pk_mul_f32 v[120:121], v[128:129], v[120:121]
	v_pk_fma_f32 v[148:149], v[38:39], v[146:147], v[148:149]
	v_pk_fma_f32 v[152:153], v[32:33], v[132:133], v[152:153]
	v_pk_fma_f32 v[148:149], v[22:23], v[136:137], v[148:149]
	v_pk_fma_f32 v[152:153], v[20:21], v[116:117], v[152:153]
	v_mul_f32_e32 v68, 0xbfb8aa3b, v148
	v_exp_f32_e32 v68, v68
	v_mul_f32_e32 v154, 0xbfb8aa3b, v149
	v_exp_f32_e32 v154, v154
	v_pk_mul_f32 v[152:153], v[152:153], 4.0 op_sel_hi:[1,0]
	v_add_f32_e32 v68, 1.0, v68
	v_rcp_f32_e32 v128, v68
	v_add_f32_e32 v68, 1.0, v154
	v_rcp_f32_e32 v129, v68
	v_pk_fma_f32 v[154:155], v[46:47], v[162:163], v[2:3]
	s_waitcnt vmcnt(27)
	v_cvt_pk_f32_fp8_e32 v[168:169], v140
	v_pk_fma_f32 v[154:155], v[30:31], v[144:145], v[154:155]
	v_pk_mul_f32 v[128:129], v[148:149], v[128:129]
	v_pk_fma_f32 v[154:155], v[18:19], v[124:125], v[154:155]
	s_waitcnt vmcnt(26)
	v_cvt_pk_f32_fp8_e32 v[162:163], v138
	v_pk_mul_f32 v[148:149], v[154:155], 4.0 op_sel_hi:[1,0]
	v_pk_fma_f32 v[154:155], v[56:57], v[160:161], v[8:9]
	v_pk_mul_f32 v[128:129], v[148:149], v[128:129]
	v_pk_fma_f32 v[154:155], v[40:41], v[142:143], v[154:155]
	v_pk_fma_f32 v[158:159], v[64:65], v[158:159], v[16:17]
	v_pk_fma_f32 v[154:155], v[24:25], v[108:109], v[154:155]
	v_pk_fma_f32 v[158:159], v[52:53], v[170:171], v[158:159]
	v_mul_f32_e32 v68, 0xbfb8aa3b, v154
	v_exp_f32_e32 v68, v68
	v_mul_f32_e32 v160, 0xbfb8aa3b, v155
	v_exp_f32_e32 v160, v160
	v_pk_fma_f32 v[146:147], v[54:55], v[146:147], v[6:7]
	v_add_f32_e32 v68, 1.0, v68
	v_rcp_f32_e32 v148, v68
	v_add_f32_e32 v68, 1.0, v160
	v_rcp_f32_e32 v149, v68
	v_med3_f32 v68, v112, s41, v1
	v_mov_b32_e32 v112, v69
	v_cvt_pk_fp8_f32 v112, v68, v113
	v_med3_f32 v68, v120, s41, v1
	v_med3_f32 v120, v121, s41, v1
	v_med3_f32 v121, v128, s41, v1
	v_med3_f32 v128, v129, s41, v1
	v_mov_b32_e32 v113, v69
	v_cvt_pk_fp8_f32 v113, v121, v128
	v_pk_mul_f32 v[148:149], v[154:155], v[148:149]
	v_cvt_pk_fp8_f32 v112, v68, v120 op_sel:[0,0,1]
	v_pk_mul_f32 v[148:149], v[152:153], v[148:149]
	v_cvt_pk_f32_fp8_sdwa v[154:155], v140 src0_sel:WORD_1
	v_med3_f32 v68, v148, s41, v1
	v_med3_f32 v120, v149, s41, v1
	v_cvt_pk_fp8_f32 v113, v68, v120 op_sel:[0,0,1]
	v_add_co_u32_e32 v120, vcc, s25, v70
	v_cvt_pk_f32_fp8_e32 v[148:149], v141
	s_nop 0
	v_addc_co_u32_e32 v121, vcc, 0, v71, vcc
	global_store_dwordx2 v[120:121], v[112:113], off offset:1536
	v_pk_fma_f32 v[120:121], v[62:63], v[180:181], v[14:15]
	v_cvt_pk_f32_fp8_sdwa v[112:113], v141 src0_sel:WORD_1
	v_pk_fma_f32 v[120:121], v[50:51], v[182:183], v[120:121]
	v_cvt_pk_f32_fp8_sdwa v[152:153], v138 src0_sel:WORD_1
	v_pk_fma_f32 v[140:141], v[34:35], v[168:169], v[120:121]
	v_cvt_pk_f32_fp8_e32 v[128:129], v139
	v_mul_f32_e32 v68, 0xbfb8aa3b, v140
	v_exp_f32_e32 v68, v68
	v_mul_f32_e32 v120, 0xbfb8aa3b, v141
	v_exp_f32_e32 v160, v120
	v_cvt_pk_f32_fp8_sdwa v[120:121], v139 src0_sel:WORD_1
	v_add_f32_e32 v68, 1.0, v68
	v_rcp_f32_e32 v138, v68
	v_add_f32_e32 v68, 1.0, v160
	v_rcp_f32_e32 v139, v68
	v_pk_fma_f32 v[160:161], v[58:59], v[174:175], v[10:11]
	v_pk_fma_f32 v[158:159], v[36:37], v[154:155], v[158:159]
	v_pk_fma_f32 v[160:161], v[42:43], v[176:177], v[160:161]
	v_mul_f32_e32 v68, 0xbfb8aa3b, v158
	v_pk_fma_f32 v[160:161], v[26:27], v[162:163], v[160:161]
	v_pk_mul_f32 v[138:139], v[140:141], v[138:139]
	v_pk_mul_f32 v[140:141], v[160:161], 4.0 op_sel_hi:[1,0]
	v_exp_f32_e32 v68, v68
	v_mul_f32_e32 v160, 0xbfb8aa3b, v159
	v_exp_f32_e32 v160, v160
	v_pk_mul_f32 v[138:139], v[140:141], v[138:139]
	v_add_f32_e32 v68, 1.0, v68
	v_rcp_f32_e32 v140, v68
	v_add_f32_e32 v68, 1.0, v160
	v_rcp_f32_e32 v141, v68
	v_pk_fma_f32 v[146:147], v[38:39], v[136:137], v[146:147]
	v_pk_fma_f32 v[150:151], v[60:61], v[150:151], v[12:13]
	v_pk_fma_f32 v[146:147], v[22:23], v[148:149], v[146:147]
	v_pk_mul_f32 v[140:141], v[158:159], v[140:141]
	v_mul_f32_e32 v68, 0xbfb8aa3b, v146
	v_exp_f32_e32 v68, v68
	v_mul_f32_e32 v158, 0xbfb8aa3b, v147
	v_exp_f32_e32 v158, v158
	v_pk_fma_f32 v[150:151], v[44:45], v[156:157], v[150:151]
	v_add_f32_e32 v68, 1.0, v68
	v_pk_fma_f32 v[150:151], v[28:29], v[152:153], v[150:151]
	v_pk_fma_f32 v[142:143], v[56:57], v[142:143], v[8:9]
	v_pk_mul_f32 v[150:151], v[150:151], 4.0 op_sel_hi:[1,0]
	v_pk_fma_f32 v[142:143], v[40:41], v[108:109], v[142:143]
	v_pk_mul_f32 v[140:141], v[150:151], v[140:141]
	v_rcp_f32_e32 v150, v68
	v_add_f32_e32 v68, 1.0, v158
	v_rcp_f32_e32 v151, v68
	v_pk_fma_f32 v[142:143], v[24:25], v[112:113], v[142:143]
	v_pk_fma_f32 v[144:145], v[46:47], v[144:145], v[2:3]
	v_mul_f32_e32 v68, 0xbfb8aa3b, v142
	v_pk_mul_f32 v[146:147], v[146:147], v[150:151]
	v_exp_f32_e32 v68, v68
	v_mul_f32_e32 v150, 0xbfb8aa3b, v143
	v_exp_f32_e32 v150, v150
	v_pk_fma_f32 v[144:145], v[30:31], v[124:125], v[144:145]
	v_add_f32_e32 v68, 1.0, v68
	v_pk_fma_f32 v[144:145], v[18:19], v[128:129], v[144:145]
	v_pk_fma_f32 v[132:133], v[48:49], v[132:133], v[4:5]
	v_pk_mul_f32 v[144:145], v[144:145], 4.0 op_sel_hi:[1,0]
	v_pk_fma_f32 v[132:133], v[32:33], v[116:117], v[132:133]
	v_pk_mul_f32 v[144:145], v[144:145], v[146:147]
	v_rcp_f32_e32 v146, v68
	v_add_f32_e32 v68, 1.0, v150
	v_rcp_f32_e32 v147, v68
	v_pk_fma_f32 v[132:133], v[20:21], v[120:121], v[132:133]
	v_med3_f32 v68, v138, s41, v1
	v_pk_mul_f32 v[132:133], v[132:133], 4.0 op_sel_hi:[1,0]
	v_pk_mul_f32 v[142:143], v[142:143], v[146:147]
	v_med3_f32 v139, v139, s41, v1
	v_mov_b32_e32 v138, v69
	v_pk_mul_f32 v[132:133], v[132:133], v[142:143]
	v_cvt_pk_fp8_f32 v138, v68, v139
	v_med3_f32 v68, v140, s41, v1
	v_med3_f32 v140, v141, s41, v1
	v_med3_f32 v141, v144, s41, v1
	v_med3_f32 v142, v145, s41, v1
	v_mov_b32_e32 v139, v69
	v_cvt_pk_fp8_f32 v139, v141, v142
	v_cvt_pk_fp8_f32 v138, v68, v140 op_sel:[0,0,1]
	v_med3_f32 v68, v132, s41, v1
	v_med3_f32 v132, v133, s41, v1
	v_cvt_pk_fp8_f32 v139, v68, v132 op_sel:[0,0,1]
	v_add_co_u32_e32 v132, vcc, s46, v70
	s_waitcnt vmcnt(26)
	v_cvt_pk_f32_fp8_e32 v[142:143], v104
	v_addc_co_u32_e32 v133, vcc, 0, v71, vcc
	global_store_dwordx2 v[132:133], v[138:139], off offset:256
	v_pk_fma_f32 v[138:139], v[62:63], v[182:183], v[14:15]
	s_waitcnt vmcnt(26)
	v_cvt_pk_f32_fp8_e32 v[164:165], v100
	v_pk_fma_f32 v[138:139], v[50:51], v[168:169], v[138:139]
	v_cvt_pk_f32_fp8_sdwa v[144:145], v100 src0_sel:WORD_1
	v_pk_fma_f32 v[138:139], v[34:35], v[142:143], v[138:139]
	v_pk_fma_f32 v[150:151], v[58:59], v[176:177], v[10:11]
	v_mul_f32_e32 v68, 0xbfb8aa3b, v138
	v_exp_f32_e32 v68, v68
	v_mul_f32_e32 v100, 0xbfb8aa3b, v139
	v_exp_f32_e32 v147, v100
	v_cvt_pk_f32_fp8_sdwa v[160:161], v104 src0_sel:WORD_1
	v_add_f32_e32 v68, 1.0, v68
	v_rcp_f32_e32 v146, v68
	v_add_f32_e32 v68, 1.0, v147
	v_rcp_f32_e32 v147, v68
	v_pk_fma_f32 v[150:151], v[42:43], v[162:163], v[150:151]
	v_cvt_pk_f32_fp8_e32 v[140:141], v105
	v_pk_fma_f32 v[150:151], v[26:27], v[164:165], v[150:151]
	v_pk_mul_f32 v[138:139], v[138:139], v[146:147]
	v_pk_mul_f32 v[146:147], v[150:151], 4.0 op_sel_hi:[1,0]
	v_pk_fma_f32 v[150:151], v[64:65], v[170:171], v[16:17]
	v_pk_mul_f32 v[138:139], v[146:147], v[138:139]
	v_pk_fma_f32 v[150:151], v[52:53], v[154:155], v[150:151]
	v_pk_fma_f32 v[136:137], v[54:55], v[136:137], v[6:7]
	v_pk_fma_f32 v[150:151], v[36:37], v[160:161], v[150:151]
	v_pk_fma_f32 v[156:157], v[60:61], v[156:157], v[12:13]
	v_mul_f32_e32 v68, 0xbfb8aa3b, v150
	v_exp_f32_e32 v68, v68
	v_mul_f32_e32 v158, 0xbfb8aa3b, v151
	v_exp_f32_e32 v158, v158
	v_pk_fma_f32 v[136:137], v[38:39], v[148:149], v[136:137]
	v_add_f32_e32 v68, 1.0, v68
	v_rcp_f32_e32 v146, v68
	v_add_f32_e32 v68, 1.0, v158
	v_rcp_f32_e32 v147, v68
	v_pk_fma_f32 v[156:157], v[44:45], v[152:153], v[156:157]
	v_pk_fma_f32 v[136:137], v[22:23], v[140:141], v[136:137]
	v_pk_fma_f32 v[156:157], v[28:29], v[144:145], v[156:157]
	v_mul_f32_e32 v68, 0xbfb8aa3b, v136
	v_pk_mul_f32 v[146:147], v[150:151], v[146:147]
	v_pk_mul_f32 v[150:151], v[156:157], 4.0 op_sel_hi:[1,0]
	v_exp_f32_e32 v68, v68
	v_mul_f32_e32 v156, 0xbfb8aa3b, v137
	v_exp_f32_e32 v156, v156
	v_cvt_pk_f32_fp8_sdwa v[104:105], v105 src0_sel:WORD_1
	v_add_f32_e32 v68, 1.0, v68
	v_pk_mul_f32 v[146:147], v[150:151], v[146:147]
	v_rcp_f32_e32 v150, v68
	v_add_f32_e32 v68, 1.0, v156
	v_rcp_f32_e32 v151, v68
	v_pk_fma_f32 v[108:109], v[56:57], v[108:109], v[8:9]
	v_cvt_pk_f32_fp8_e32 v[132:133], v101
	v_pk_fma_f32 v[108:109], v[40:41], v[112:113], v[108:109]
	v_pk_mul_f32 v[136:137], v[136:137], v[150:151]
	v_pk_fma_f32 v[108:109], v[24:25], v[104:105], v[108:109]
	v_pk_fma_f32 v[124:125], v[46:47], v[124:125], v[2:3]
	v_mul_f32_e32 v68, 0xbfb8aa3b, v108
	v_exp_f32_e32 v68, v68
	v_mul_f32_e32 v150, 0xbfb8aa3b, v109
	v_exp_f32_e32 v150, v150
	v_pk_fma_f32 v[124:125], v[30:31], v[128:129], v[124:125]
	v_add_f32_e32 v68, 1.0, v68
	v_pk_fma_f32 v[124:125], v[18:19], v[132:133], v[124:125]
	v_cvt_pk_f32_fp8_sdwa v[100:101], v101 src0_sel:WORD_1
	v_pk_mul_f32 v[124:125], v[124:125], 4.0 op_sel_hi:[1,0]
	v_pk_fma_f32 v[116:117], v[48:49], v[116:117], v[4:5]
	v_pk_mul_f32 v[124:125], v[124:125], v[136:137]
	v_rcp_f32_e32 v136, v68
	v_add_f32_e32 v68, 1.0, v150
	v_rcp_f32_e32 v137, v68
	v_pk_fma_f32 v[116:117], v[32:33], v[120:121], v[116:117]
	v_med3_f32 v68, v138, s41, v1
	v_pk_fma_f32 v[116:117], v[20:21], v[100:101], v[116:117]
	v_pk_mul_f32 v[108:109], v[108:109], v[136:137]
	v_pk_mul_f32 v[116:117], v[116:117], 4.0 op_sel_hi:[1,0]
	v_med3_f32 v124, v124, s41, v1
	v_pk_mul_f32 v[108:109], v[116:117], v[108:109]
	v_med3_f32 v117, v139, s41, v1
	v_mov_b32_e32 v116, v69
	v_cvt_pk_fp8_f32 v116, v68, v117
	v_med3_f32 v125, v125, s41, v1
	v_mov_b32_e32 v117, v69
	s_waitcnt vmcnt(25)
	v_cvt_pk_f32_fp8_e32 v[172:173], v96
	v_cvt_pk_fp8_f32 v117, v124, v125
	v_pk_fma_f32 v[138:139], v[62:63], v[168:169], v[14:15]
	v_med3_f32 v68, v146, s41, v1
	v_med3_f32 v136, v147, s41, v1
	v_pk_fma_f32 v[138:139], v[50:51], v[142:143], v[138:139]
	v_cvt_pk_fp8_f32 v116, v68, v136 op_sel:[0,0,1]
	v_med3_f32 v68, v108, s41, v1
	v_med3_f32 v108, v109, s41, v1
	v_pk_fma_f32 v[138:139], v[34:35], v[172:173], v[138:139]
	v_cvt_pk_fp8_f32 v117, v68, v108 op_sel:[0,0,1]
	v_mul_f32_e32 v68, 0xbfb8aa3b, v138
	s_waitcnt vmcnt(24)
	v_cvt_pk_f32_fp8_e32 v[166:167], v92
	v_cvt_pk_f32_fp8_sdwa v[124:125], v92 src0_sel:WORD_1
	v_exp_f32_e32 v68, v68
	v_mul_f32_e32 v92, 0xbfb8aa3b, v139
	v_exp_f32_e32 v147, v92
	v_pk_fma_f32 v[150:151], v[58:59], v[162:163], v[10:11]
	v_add_f32_e32 v68, 1.0, v68
	v_rcp_f32_e32 v146, v68
	v_add_f32_e32 v68, 1.0, v147
	v_rcp_f32_e32 v147, v68
	v_cvt_pk_f32_fp8_sdwa v[136:137], v96 src0_sel:WORD_1
	v_pk_fma_f32 v[150:151], v[42:43], v[164:165], v[150:151]
	v_add_co_u32_e32 v108, vcc, s26, v70
	v_pk_fma_f32 v[150:151], v[26:27], v[166:167], v[150:151]
	v_pk_mul_f32 v[138:139], v[138:139], v[146:147]
	v_pk_mul_f32 v[146:147], v[150:151], 4.0 op_sel_hi:[1,0]
	v_pk_fma_f32 v[150:151], v[64:65], v[154:155], v[16:17]
	v_addc_co_u32_e32 v109, vcc, 0, v71, vcc
	v_pk_fma_f32 v[150:151], v[52:53], v[160:161], v[150:151]
	global_store_dwordx2 v[108:109], v[116:117], off offset:3072
	v_pk_fma_f32 v[150:151], v[36:37], v[136:137], v[150:151]
	v_cvt_pk_f32_fp8_e32 v[116:117], v97
	v_mul_f32_e32 v68, 0xbfb8aa3b, v150
	v_exp_f32_e32 v68, v68
	v_mul_f32_e32 v154, 0xbfb8aa3b, v151
	v_exp_f32_e32 v154, v154
	v_pk_mul_f32 v[138:139], v[146:147], v[138:139]
	v_add_f32_e32 v68, 1.0, v68
	v_rcp_f32_e32 v146, v68
	v_add_f32_e32 v68, 1.0, v154
	v_rcp_f32_e32 v147, v68
	v_pk_fma_f32 v[148:149], v[54:55], v[148:149], v[6:7]
	v_pk_fma_f32 v[152:153], v[60:61], v[152:153], v[12:13]
	v_pk_fma_f32 v[148:149], v[38:39], v[140:141], v[148:149]
	v_pk_fma_f32 v[152:153], v[44:45], v[144:145], v[152:153]
	v_pk_fma_f32 v[148:149], v[22:23], v[116:117], v[148:149]
	v_pk_fma_f32 v[152:153], v[28:29], v[124:125], v[152:153]
	v_mul_f32_e32 v68, 0xbfb8aa3b, v148
	v_pk_mul_f32 v[146:147], v[150:151], v[146:147]
	v_pk_mul_f32 v[150:151], v[152:153], 4.0 op_sel_hi:[1,0]
	v_exp_f32_e32 v68, v68
	v_mul_f32_e32 v152, 0xbfb8aa3b, v149
	v_exp_f32_e32 v152, v152
	v_cvt_pk_f32_fp8_sdwa v[96:97], v97 src0_sel:WORD_1
	v_add_f32_e32 v68, 1.0, v68
	v_pk_mul_f32 v[146:147], v[150:151], v[146:147]
	v_rcp_f32_e32 v150, v68
	v_add_f32_e32 v68, 1.0, v152
	v_rcp_f32_e32 v151, v68
	v_pk_fma_f32 v[112:113], v[56:57], v[112:113], v[8:9]
	v_cvt_pk_f32_fp8_e32 v[108:109], v93
	v_pk_fma_f32 v[112:113], v[40:41], v[104:105], v[112:113]
	v_pk_mul_f32 v[148:149], v[148:149], v[150:151]
	v_pk_fma_f32 v[112:113], v[24:25], v[96:97], v[112:113]
	v_pk_fma_f32 v[128:129], v[46:47], v[128:129], v[2:3]
	v_mul_f32_e32 v68, 0xbfb8aa3b, v112
	v_exp_f32_e32 v68, v68
	v_mul_f32_e32 v150, 0xbfb8aa3b, v113
	v_exp_f32_e32 v150, v150
	v_pk_fma_f32 v[128:129], v[30:31], v[132:133], v[128:129]
	v_add_f32_e32 v68, 1.0, v68
	v_pk_fma_f32 v[128:129], v[18:19], v[108:109], v[128:129]
	v_cvt_pk_f32_fp8_sdwa v[92:93], v93 src0_sel:WORD_1
	v_pk_mul_f32 v[128:129], v[128:129], 4.0 op_sel_hi:[1,0]
	v_pk_fma_f32 v[120:121], v[48:49], v[120:121], v[4:5]
	v_pk_mul_f32 v[128:129], v[128:129], v[148:149]
	v_rcp_f32_e32 v148, v68
	v_add_f32_e32 v68, 1.0, v150
	v_rcp_f32_e32 v149, v68
	v_pk_fma_f32 v[120:121], v[32:33], v[100:101], v[120:121]
	v_med3_f32 v68, v138, s41, v1
	v_pk_fma_f32 v[120:121], v[20:21], v[92:93], v[120:121]
	v_pk_mul_f32 v[112:113], v[112:113], v[148:149]
	v_pk_mul_f32 v[120:121], v[120:121], 4.0 op_sel_hi:[1,0]
	v_med3_f32 v128, v128, s41, v1
	v_pk_mul_f32 v[112:113], v[120:121], v[112:113]
	v_med3_f32 v121, v139, s41, v1
	v_mov_b32_e32 v120, v69
	v_cvt_pk_fp8_f32 v120, v68, v121
	v_med3_f32 v129, v129, s41, v1
	v_mov_b32_e32 v121, v69
	v_cvt_pk_fp8_f32 v121, v128, v129
	s_waitcnt vmcnt(24)
	v_cvt_pk_f32_fp8_e32 v[168:169], v88
	v_med3_f32 v68, v146, s41, v1
	v_med3_f32 v138, v147, s41, v1
	v_cvt_pk_fp8_f32 v120, v68, v138 op_sel:[0,0,1]
	v_med3_f32 v68, v112, s41, v1
	v_med3_f32 v112, v113, s41, v1
	v_cvt_pk_f32_fp8_sdwa v[158:159], v88 src0_sel:WORD_1
	v_cvt_pk_f32_fp8_e32 v[150:151], v89
	v_cvt_pk_f32_fp8_sdwa v[138:139], v89 src0_sel:WORD_1
	v_pk_fma_f32 v[88:89], v[62:63], v[142:143], v[14:15]
	v_cvt_pk_fp8_f32 v121, v68, v112 op_sel:[0,0,1]
	v_pk_fma_f32 v[88:89], v[50:51], v[172:173], v[88:89]
	v_add_co_u32_e32 v112, vcc, s47, v70
	v_pk_fma_f32 v[88:89], v[34:35], v[168:169], v[88:89]
	s_nop 0
	v_addc_co_u32_e32 v113, vcc, 0, v71, vcc
	v_mul_f32_e32 v68, 0xbfb8aa3b, v88
	s_waitcnt vmcnt(23)
	v_cvt_pk_f32_fp8_e32 v[162:163], v84
	v_cvt_pk_f32_fp8_sdwa v[154:155], v84 src0_sel:WORD_1
	v_exp_f32_e32 v68, v68
	v_mul_f32_e32 v84, 0xbfb8aa3b, v89
	global_store_dwordx2 v[112:113], v[120:121], off offset:1792
	v_exp_f32_e32 v112, v84
	v_add_f32_e32 v68, 1.0, v68
	v_rcp_f32_e32 v84, v68
	v_cvt_pk_f32_fp8_e32 v[146:147], v85
	v_add_f32_e32 v68, 1.0, v112
	v_cvt_pk_f32_fp8_sdwa v[142:143], v85 src0_sel:WORD_1
	v_rcp_f32_e32 v85, v68
	v_pk_fma_f32 v[112:113], v[58:59], v[164:165], v[10:11]
	v_pk_fma_f32 v[104:105], v[56:57], v[104:105], v[8:9]
	v_pk_fma_f32 v[112:113], v[42:43], v[166:167], v[112:113]
	v_pk_mul_f32 v[84:85], v[88:89], v[84:85]
	v_pk_fma_f32 v[112:113], v[26:27], v[162:163], v[112:113]
	v_pk_fma_f32 v[104:105], v[40:41], v[96:97], v[104:105]
	v_pk_mul_f32 v[88:89], v[112:113], 4.0 op_sel_hi:[1,0]
	v_pk_fma_f32 v[112:113], v[64:65], v[160:161], v[16:17]
	v_pk_mul_f32 v[84:85], v[88:89], v[84:85]
	v_pk_fma_f32 v[112:113], v[52:53], v[136:137], v[112:113]
	v_pk_fma_f32 v[104:105], v[24:25], v[138:139], v[104:105]
	v_pk_fma_f32 v[112:113], v[36:37], v[158:159], v[112:113]
	v_pk_fma_f32 v[100:101], v[48:49], v[100:101], v[4:5]
	v_mul_f32_e32 v68, 0xbfb8aa3b, v112
	v_exp_f32_e32 v68, v68
	v_mul_f32_e32 v120, 0xbfb8aa3b, v113
	v_exp_f32_e32 v120, v120
	v_pk_fma_f32 v[100:101], v[32:33], v[92:93], v[100:101]
	v_add_f32_e32 v68, 1.0, v68
	v_rcp_f32_e32 v88, v68
	v_add_f32_e32 v68, 1.0, v120
	v_rcp_f32_e32 v89, v68
	v_pk_fma_f32 v[120:121], v[60:61], v[144:145], v[12:13]
	v_pk_fma_f32 v[100:101], v[20:21], v[142:143], v[100:101]
	v_pk_fma_f32 v[120:121], v[44:45], v[124:125], v[120:121]
	v_pk_mul_f32 v[88:89], v[112:113], v[88:89]
	v_pk_fma_f32 v[120:121], v[28:29], v[154:155], v[120:121]
	v_pk_mul_f32 v[100:101], v[100:101], 4.0 op_sel_hi:[1,0]
	v_pk_mul_f32 v[112:113], v[120:121], 4.0 op_sel_hi:[1,0]
	v_pk_fma_f32 v[120:121], v[54:55], v[140:141], v[6:7]
	v_pk_mul_f32 v[88:89], v[112:113], v[88:89]
	v_pk_fma_f32 v[120:121], v[38:39], v[116:117], v[120:121]
	v_med3_f32 v85, v85, s41, v1
	v_pk_fma_f32 v[120:121], v[22:23], v[150:151], v[120:121]
	s_waitcnt vmcnt(23)
	v_cvt_pk_f32_fp8_e32 v[170:171], v80
	v_mul_f32_e32 v68, 0xbfb8aa3b, v120
	v_exp_f32_e32 v68, v68
	v_mul_f32_e32 v128, 0xbfb8aa3b, v121
	v_exp_f32_e32 v128, v128
	v_cvt_pk_f32_fp8_sdwa v[160:161], v80 src0_sel:WORD_1
	v_add_f32_e32 v68, 1.0, v68
	v_rcp_f32_e32 v112, v68
	v_add_f32_e32 v68, 1.0, v128
	v_rcp_f32_e32 v113, v68
	v_pk_fma_f32 v[128:129], v[46:47], v[132:133], v[2:3]
	v_mul_f32_e32 v68, 0xbfb8aa3b, v104
	v_pk_fma_f32 v[128:129], v[30:31], v[108:109], v[128:129]
	v_pk_mul_f32 v[112:113], v[120:121], v[112:113]
	v_pk_fma_f32 v[128:129], v[18:19], v[146:147], v[128:129]
	v_exp_f32_e32 v68, v68
	v_pk_mul_f32 v[120:121], v[128:129], 4.0 op_sel_hi:[1,0]
	v_mul_f32_e32 v128, 0xbfb8aa3b, v105
	v_exp_f32_e32 v128, v128
	v_add_f32_e32 v68, 1.0, v68
	v_pk_mul_f32 v[112:113], v[120:121], v[112:113]
	v_rcp_f32_e32 v120, v68
	v_add_f32_e32 v68, 1.0, v128
	v_rcp_f32_e32 v121, v68
	v_med3_f32 v68, v84, s41, v1
	v_mov_b32_e32 v84, v69
	v_cvt_pk_fp8_f32 v84, v68, v85
	v_pk_mul_f32 v[104:105], v[104:105], v[120:121]
	v_med3_f32 v68, v88, s41, v1
	v_pk_mul_f32 v[100:101], v[100:101], v[104:105]
	v_med3_f32 v88, v89, s41, v1
	v_med3_f32 v89, v112, s41, v1
	v_med3_f32 v104, v113, s41, v1
	v_mov_b32_e32 v85, v69
	v_cvt_pk_fp8_f32 v85, v89, v104
	v_cvt_pk_fp8_f32 v84, v68, v88 op_sel:[0,0,1]
	v_med3_f32 v68, v100, s41, v1
	v_med3_f32 v88, v101, s41, v1
	v_cvt_pk_f32_fp8_e32 v[152:153], v81
	v_cvt_pk_f32_fp8_sdwa v[140:141], v81 src0_sel:WORD_1
	v_pk_fma_f32 v[80:81], v[62:63], v[172:173], v[14:15]
	v_cvt_pk_fp8_f32 v85, v68, v88 op_sel:[0,0,1]
	v_pk_fma_f32 v[80:81], v[50:51], v[168:169], v[80:81]
	v_add_co_u32_e32 v88, vcc, s27, v70
	v_pk_fma_f32 v[80:81], v[34:35], v[170:171], v[80:81]
	s_nop 0
	v_addc_co_u32_e32 v89, vcc, 0, v71, vcc
	v_mul_f32_e32 v68, 0xbfb8aa3b, v80
	s_waitcnt vmcnt(22)
	v_cvt_pk_f32_fp8_e32 v[164:165], v76
	v_cvt_pk_f32_fp8_sdwa v[156:157], v76 src0_sel:WORD_1
	v_exp_f32_e32 v68, v68
	v_mul_f32_e32 v76, 0xbfb8aa3b, v81
	global_store_dwordx2 v[88:89], v[84:85], off offset:512
	v_exp_f32_e32 v84, v76
	v_add_f32_e32 v68, 1.0, v68
	v_rcp_f32_e32 v76, v68
	v_cvt_pk_f32_fp8_e32 v[148:149], v77
	v_add_f32_e32 v68, 1.0, v84
	v_cvt_pk_f32_fp8_sdwa v[144:145], v77 src0_sel:WORD_1
	v_rcp_f32_e32 v77, v68
	v_pk_fma_f32 v[84:85], v[58:59], v[166:167], v[10:11]
	v_pk_fma_f32 v[96:97], v[56:57], v[96:97], v[8:9]
	v_pk_fma_f32 v[84:85], v[42:43], v[162:163], v[84:85]
	v_pk_mul_f32 v[76:77], v[80:81], v[76:77]
	v_pk_fma_f32 v[84:85], v[26:27], v[164:165], v[84:85]
	v_pk_fma_f32 v[96:97], v[40:41], v[138:139], v[96:97]
	v_pk_mul_f32 v[80:81], v[84:85], 4.0 op_sel_hi:[1,0]
	v_pk_fma_f32 v[84:85], v[64:65], v[136:137], v[16:17]
	v_pk_mul_f32 v[76:77], v[80:81], v[76:77]
	v_pk_fma_f32 v[84:85], v[52:53], v[158:159], v[84:85]
	v_pk_fma_f32 v[96:97], v[24:25], v[140:141], v[96:97]
	v_pk_fma_f32 v[84:85], v[36:37], v[160:161], v[84:85]
	v_pk_fma_f32 v[92:93], v[48:49], v[92:93], v[4:5]
	v_mul_f32_e32 v68, 0xbfb8aa3b, v84
	v_exp_f32_e32 v68, v68
	v_mul_f32_e32 v88, 0xbfb8aa3b, v85
	v_exp_f32_e32 v88, v88
	v_med3_f32 v77, v77, s41, v1
	v_add_f32_e32 v68, 1.0, v68
	v_rcp_f32_e32 v80, v68
	v_add_f32_e32 v68, 1.0, v88
	v_rcp_f32_e32 v81, v68
	v_pk_fma_f32 v[88:89], v[60:61], v[124:125], v[12:13]
	v_pk_fma_f32 v[92:93], v[32:33], v[142:143], v[92:93]
	v_pk_fma_f32 v[88:89], v[44:45], v[154:155], v[88:89]
	v_pk_mul_f32 v[80:81], v[84:85], v[80:81]
	v_pk_fma_f32 v[88:89], v[28:29], v[156:157], v[88:89]
	s_waitcnt vmcnt(22)
	v_cvt_pk_f32_fp8_e32 v[180:181], v134
	v_pk_mul_f32 v[84:85], v[88:89], 4.0 op_sel_hi:[1,0]
	v_pk_fma_f32 v[88:89], v[54:55], v[116:117], v[6:7]
	v_pk_mul_f32 v[80:81], v[84:85], v[80:81]
	v_pk_fma_f32 v[88:89], v[38:39], v[150:151], v[88:89]
	v_pk_fma_f32 v[92:93], v[20:21], v[144:145], v[92:93]
	v_pk_fma_f32 v[88:89], v[22:23], v[152:153], v[88:89]
	v_pk_mul_f32 v[92:93], v[92:93], 4.0 op_sel_hi:[1,0]
	v_mul_f32_e32 v68, 0xbfb8aa3b, v88
	v_exp_f32_e32 v68, v68
	v_mul_f32_e32 v100, 0xbfb8aa3b, v89
	v_exp_f32_e32 v100, v100
	v_pk_fma_f32 v[168:169], v[62:63], v[168:169], v[14:15]
	v_add_f32_e32 v68, 1.0, v68
	v_rcp_f32_e32 v84, v68
	v_add_f32_e32 v68, 1.0, v100
	v_rcp_f32_e32 v85, v68
	v_pk_fma_f32 v[100:101], v[46:47], v[108:109], v[2:3]
	v_mul_f32_e32 v68, 0xbfb8aa3b, v96
	v_pk_fma_f32 v[100:101], v[30:31], v[146:147], v[100:101]
	v_pk_mul_f32 v[84:85], v[88:89], v[84:85]
	v_pk_fma_f32 v[100:101], v[18:19], v[148:149], v[100:101]
	v_exp_f32_e32 v68, v68
	v_pk_mul_f32 v[88:89], v[100:101], 4.0 op_sel_hi:[1,0]
	v_mul_f32_e32 v100, 0xbfb8aa3b, v97
	v_exp_f32_e32 v100, v100
	v_add_f32_e32 v68, 1.0, v68
	v_pk_mul_f32 v[84:85], v[88:89], v[84:85]
	v_rcp_f32_e32 v88, v68
	v_add_f32_e32 v68, 1.0, v100
	v_rcp_f32_e32 v89, v68
	v_med3_f32 v68, v76, s41, v1
	v_mov_b32_e32 v76, v69
	v_cvt_pk_fp8_f32 v76, v68, v77
	v_med3_f32 v68, v80, s41, v1
	v_med3_f32 v80, v81, s41, v1
	v_med3_f32 v81, v84, s41, v1
	v_med3_f32 v84, v85, s41, v1
	v_mov_b32_e32 v77, v69
	v_cvt_pk_fp8_f32 v77, v81, v84
	v_pk_mul_f32 v[88:89], v[96:97], v[88:89]
	v_pk_fma_f32 v[168:169], v[50:51], v[170:171], v[168:169]
	v_pk_mul_f32 v[88:89], v[92:93], v[88:89]
	v_cvt_pk_fp8_f32 v76, v68, v80 op_sel:[0,0,1]
	v_med3_f32 v68, v88, s41, v1
	v_med3_f32 v80, v89, s41, v1
	v_pk_fma_f32 v[168:169], v[34:35], v[180:181], v[168:169]
	v_cvt_pk_fp8_f32 v77, v68, v80 op_sel:[0,0,1]
	v_mul_f32_e32 v68, 0xbfb8aa3b, v168
	s_waitcnt vmcnt(21)
	v_cvt_pk_f32_fp8_e32 v[178:179], v130
	v_cvt_pk_f32_fp8_sdwa v[174:175], v130 src0_sel:WORD_1
	v_exp_f32_e32 v68, v68
	v_mul_f32_e32 v130, 0xbfb8aa3b, v169
	v_exp_f32_e32 v183, v130
	v_cvt_pk_f32_fp8_sdwa v[176:177], v134 src0_sel:WORD_1
	v_add_f32_e32 v68, 1.0, v68
	v_rcp_f32_e32 v182, v68
	v_add_f32_e32 v68, 1.0, v183
	v_rcp_f32_e32 v183, v68
	v_pk_fma_f32 v[158:159], v[64:65], v[158:159], v[16:17]
	v_add_co_u32_e32 v80, vcc, s48, v70
	v_pk_fma_f32 v[158:159], v[52:53], v[160:161], v[158:159]
	v_pk_mul_f32 v[168:169], v[168:169], v[182:183]
	v_pk_fma_f32 v[158:159], v[36:37], v[176:177], v[158:159]
	v_pk_fma_f32 v[162:163], v[58:59], v[162:163], v[10:11]
	v_mul_f32_e32 v68, 0xbfb8aa3b, v158
	v_exp_f32_e32 v68, v68
	v_mul_f32_e32 v182, 0xbfb8aa3b, v159
	v_exp_f32_e32 v182, v182
	v_addc_co_u32_e32 v81, vcc, 0, v71, vcc
	v_pk_fma_f32 v[162:163], v[42:43], v[164:165], v[162:163]
	global_store_dwordx2 v[80:81], v[76:77], off offset:3328
	v_add_co_u32_e32 v76, vcc, s42, v72
	v_pk_fma_f32 v[162:163], v[26:27], v[178:179], v[162:163]
	s_nop 0
	v_addc_co_u32_e32 v77, vcc, 0, v73, vcc
	v_cvt_pk_f32_fp8_e32 v[172:173], v135
	v_pk_mul_f32 v[162:163], v[162:163], 4.0 op_sel_hi:[1,0]
	v_add_f32_e32 v68, 1.0, v68
	v_add_co_u32_e32 v80, vcc, s49, v72
	v_pk_mul_f32 v[162:163], v[162:163], v[168:169]
	v_rcp_f32_e32 v168, v68
	v_add_f32_e32 v68, 1.0, v182
	v_addc_co_u32_e32 v81, vcc, 0, v73, vcc
	v_rcp_f32_e32 v169, v68
	v_pk_fma_f32 v[150:151], v[54:55], v[150:151], v[6:7]
	global_load_dwordx2 v[136:137], v[76:77], off nt
	global_load_dwordx2 v[132:133], v[76:77], off offset:128 nt
	global_load_dwordx2 v[128:129], v[80:81], off offset:1536 nt
	global_load_dwordx2 v[124:125], v[80:81], off offset:1664 nt
	v_add_co_u32_e32 v76, vcc, s50, v72
	v_pk_fma_f32 v[150:151], v[38:39], v[152:153], v[150:151]
	s_nop 0
	v_addc_co_u32_e32 v77, vcc, 0, v73, vcc
	v_pk_fma_f32 v[150:151], v[22:23], v[172:173], v[150:151]
	v_add_co_u32_e32 v80, vcc, s51, v72
	v_mul_f32_e32 v68, 0xbfb8aa3b, v150
	s_nop 0
	v_addc_co_u32_e32 v81, vcc, 0, v73, vcc
	v_pk_mul_f32 v[158:159], v[158:159], v[168:169]
	v_exp_f32_e32 v68, v68
	v_mul_f32_e32 v168, 0xbfb8aa3b, v151
	global_load_dwordx2 v[120:121], v[76:77], off offset:3072 nt
	global_load_dwordx2 v[116:117], v[76:77], off offset:3200 nt
	global_load_dwordx2 v[112:113], v[80:81], off offset:512 nt
	global_load_dwordx2 v[108:109], v[80:81], off offset:640 nt
	v_add_co_u32_e32 v76, vcc, s52, v72
	v_pk_fma_f32 v[154:155], v[60:61], v[154:155], v[12:13]
	v_exp_f32_e32 v168, v168
	v_addc_co_u32_e32 v77, vcc, 0, v73, vcc
	v_pk_fma_f32 v[154:155], v[44:45], v[156:157], v[154:155]
	v_add_co_u32_e32 v80, vcc, s53, v72
	v_pk_fma_f32 v[154:155], v[28:29], v[174:175], v[154:155]
	s_nop 0
	v_addc_co_u32_e32 v81, vcc, 0, v73, vcc
	v_cvt_pk_f32_fp8_sdwa v[134:135], v135 src0_sel:WORD_1
	v_pk_mul_f32 v[154:155], v[154:155], 4.0 op_sel_hi:[1,0]
	v_add_f32_e32 v68, 1.0, v68
	global_load_dwordx2 v[104:105], v[76:77], off offset:2048 nt
	global_load_dwordx2 v[100:101], v[76:77], off offset:2176 nt
	global_load_dwordx2 v[96:97], v[80:81], off offset:3584 nt
	global_load_dwordx2 v[92:93], v[80:81], off offset:3712 nt
	v_add_co_u32_e32 v76, vcc, s54, v72
	v_pk_mul_f32 v[154:155], v[154:155], v[158:159]
	v_rcp_f32_e32 v158, v68
	v_add_f32_e32 v68, 1.0, v168
	v_addc_co_u32_e32 v77, vcc, 0, v73, vcc
	v_rcp_f32_e32 v159, v68
	v_pk_fma_f32 v[138:139], v[56:57], v[138:139], v[8:9]
	v_add_co_u32_e32 v166, vcc, s55, v72
	v_pk_fma_f32 v[138:139], v[40:41], v[140:141], v[138:139]
	s_nop 0
	v_addc_co_u32_e32 v167, vcc, 0, v73, vcc
	v_pk_fma_f32 v[138:139], v[24:25], v[134:135], v[138:139]
	global_load_dwordx2 v[88:89], v[76:77], off offset:1024 nt
	global_load_dwordx2 v[84:85], v[76:77], off offset:1152 nt
	global_load_dwordx2 v[80:81], v[166:167], off offset:2560 nt
	s_nop 0
	global_load_dwordx2 v[76:77], v[166:167], off offset:2688 nt
	v_cvt_pk_f32_fp8_e32 v[166:167], v131
	v_mul_f32_e32 v68, 0xbfb8aa3b, v138
	v_pk_mul_f32 v[150:151], v[150:151], v[158:159]
	v_exp_f32_e32 v68, v68
	v_mul_f32_e32 v158, 0xbfb8aa3b, v139
	v_pk_fma_f32 v[146:147], v[46:47], v[146:147], v[2:3]
	v_exp_f32_e32 v158, v158
	v_pk_fma_f32 v[146:147], v[30:31], v[148:149], v[146:147]
	v_add_f32_e32 v68, 1.0, v68
	v_pk_fma_f32 v[146:147], v[18:19], v[166:167], v[146:147]
	v_cvt_pk_f32_fp8_sdwa v[130:131], v131 src0_sel:WORD_1
	v_pk_mul_f32 v[146:147], v[146:147], 4.0 op_sel_hi:[1,0]
	v_pk_fma_f32 v[142:143], v[48:49], v[142:143], v[4:5]
	v_pk_mul_f32 v[146:147], v[146:147], v[150:151]
	v_rcp_f32_e32 v150, v68
	v_add_f32_e32 v68, 1.0, v158
	v_rcp_f32_e32 v151, v68
	v_pk_fma_f32 v[142:143], v[32:33], v[144:145], v[142:143]
	v_med3_f32 v68, v162, s41, v1
	v_pk_fma_f32 v[142:143], v[20:21], v[130:131], v[142:143]
	v_pk_mul_f32 v[138:139], v[138:139], v[150:151]
	v_pk_mul_f32 v[142:143], v[142:143], 4.0 op_sel_hi:[1,0]
	v_med3_f32 v146, v146, s41, v1
	v_pk_mul_f32 v[138:139], v[142:143], v[138:139]
	v_med3_f32 v143, v163, s41, v1
	v_mov_b32_e32 v142, v69
	v_cvt_pk_fp8_f32 v142, v68, v143
	v_med3_f32 v147, v147, s41, v1
	v_mov_b32_e32 v143, v69
	s_waitcnt vmcnt(37)
	v_cvt_pk_f32_fp8_e32 v[168:169], v126
	v_med3_f32 v68, v154, s41, v1
	v_med3_f32 v150, v155, s41, v1
	v_cvt_pk_fp8_f32 v143, v146, v147
	v_cvt_pk_fp8_f32 v142, v68, v150 op_sel:[0,0,1]
	v_pk_fma_f32 v[150:151], v[62:63], v[170:171], v[14:15]
	v_med3_f32 v68, v138, s41, v1
	v_pk_fma_f32 v[150:151], v[50:51], v[180:181], v[150:151]
	v_med3_f32 v138, v139, s41, v1
	v_pk_fma_f32 v[150:151], v[34:35], v[168:169], v[150:151]
	v_cvt_pk_fp8_f32 v143, v68, v138 op_sel:[0,0,1]
	v_mul_f32_e32 v68, 0xbfb8aa3b, v150
	s_waitcnt vmcnt(36)
	v_cvt_pk_f32_fp8_e32 v[158:159], v122
	v_cvt_pk_f32_fp8_sdwa v[146:147], v122 src0_sel:WORD_1
	v_exp_f32_e32 v68, v68
	v_mul_f32_e32 v122, 0xbfb8aa3b, v151
	v_exp_f32_e32 v163, v122
	v_cvt_pk_f32_fp8_sdwa v[154:155], v126 src0_sel:WORD_1
	v_add_f32_e32 v68, 1.0, v68
	v_rcp_f32_e32 v162, v68
	v_add_f32_e32 v68, 1.0, v163
	v_rcp_f32_e32 v163, v68
	v_pk_fma_f32 v[160:161], v[64:65], v[160:161], v[16:17]
	v_pk_fma_f32 v[164:165], v[58:59], v[164:165], v[10:11]
	v_pk_fma_f32 v[160:161], v[52:53], v[176:177], v[160:161]
	v_pk_fma_f32 v[164:165], v[42:43], v[178:179], v[164:165]
	v_pk_fma_f32 v[160:161], v[36:37], v[154:155], v[160:161]
	v_pk_fma_f32 v[164:165], v[26:27], v[158:159], v[164:165]
	v_mul_f32_e32 v68, 0xbfb8aa3b, v160
	v_pk_mul_f32 v[150:151], v[150:151], v[162:163]
	v_pk_mul_f32 v[162:163], v[164:165], 4.0 op_sel_hi:[1,0]
	v_exp_f32_e32 v68, v68
	v_mul_f32_e32 v164, 0xbfb8aa3b, v161
	v_exp_f32_e32 v164, v164
	v_add_co_u32_e32 v138, vcc, s28, v70
	v_add_f32_e32 v68, 1.0, v68
	s_nop 0
	v_addc_co_u32_e32 v139, vcc, 0, v71, vcc
	global_store_dwordx2 v[138:139], v[142:143], off offset:2048
	v_cvt_pk_f32_fp8_e32 v[142:143], v127
	v_pk_mul_f32 v[150:151], v[162:163], v[150:151]
	v_rcp_f32_e32 v162, v68
	v_add_f32_e32 v68, 1.0, v164
	v_rcp_f32_e32 v163, v68
	v_pk_fma_f32 v[152:153], v[54:55], v[152:153], v[6:7]
	v_pk_fma_f32 v[156:157], v[60:61], v[156:157], v[12:13]
	v_pk_fma_f32 v[152:153], v[38:39], v[172:173], v[152:153]
	v_pk_mul_f32 v[160:161], v[160:161], v[162:163]
	v_pk_fma_f32 v[152:153], v[22:23], v[142:143], v[152:153]
	v_pk_fma_f32 v[156:157], v[44:45], v[174:175], v[156:157]
	v_mul_f32_e32 v68, 0xbfb8aa3b, v152
	v_exp_f32_e32 v68, v68
	v_mul_f32_e32 v162, 0xbfb8aa3b, v153
	v_exp_f32_e32 v162, v162
	v_pk_fma_f32 v[156:157], v[28:29], v[146:147], v[156:157]
	v_cvt_pk_f32_fp8_sdwa v[126:127], v127 src0_sel:WORD_1
	v_pk_mul_f32 v[156:157], v[156:157], 4.0 op_sel_hi:[1,0]
	v_add_f32_e32 v68, 1.0, v68
	v_pk_mul_f32 v[156:157], v[156:157], v[160:161]
	v_rcp_f32_e32 v160, v68
	v_add_f32_e32 v68, 1.0, v162
	v_rcp_f32_e32 v161, v68
	v_pk_fma_f32 v[140:141], v[56:57], v[140:141], v[8:9]
	v_cvt_pk_f32_fp8_e32 v[138:139], v123
	v_pk_fma_f32 v[140:141], v[40:41], v[134:135], v[140:141]
	v_pk_mul_f32 v[152:153], v[152:153], v[160:161]
	v_pk_fma_f32 v[140:141], v[24:25], v[126:127], v[140:141]
	v_pk_fma_f32 v[148:149], v[46:47], v[148:149], v[2:3]
	v_mul_f32_e32 v68, 0xbfb8aa3b, v140
	v_exp_f32_e32 v68, v68
	v_mul_f32_e32 v160, 0xbfb8aa3b, v141
	v_exp_f32_e32 v160, v160
	v_pk_fma_f32 v[148:149], v[30:31], v[166:167], v[148:149]
	v_add_f32_e32 v68, 1.0, v68
	v_pk_fma_f32 v[148:149], v[18:19], v[138:139], v[148:149]
	v_cvt_pk_f32_fp8_sdwa v[122:123], v123 src0_sel:WORD_1
	v_pk_mul_f32 v[148:149], v[148:149], 4.0 op_sel_hi:[1,0]
	v_pk_fma_f32 v[144:145], v[48:49], v[144:145], v[4:5]
	v_pk_mul_f32 v[148:149], v[148:149], v[152:153]
	v_rcp_f32_e32 v152, v68
	v_add_f32_e32 v68, 1.0, v160
	v_rcp_f32_e32 v153, v68
	v_pk_fma_f32 v[144:145], v[32:33], v[130:131], v[144:145]
	v_med3_f32 v68, v150, s41, v1
	v_pk_fma_f32 v[144:145], v[20:21], v[122:123], v[144:145]
	v_pk_mul_f32 v[140:141], v[140:141], v[152:153]
	v_pk_mul_f32 v[144:145], v[144:145], 4.0 op_sel_hi:[1,0]
	v_med3_f32 v148, v148, s41, v1
	v_pk_mul_f32 v[140:141], v[144:145], v[140:141]
	v_med3_f32 v145, v151, s41, v1
	v_mov_b32_e32 v144, v69
	v_cvt_pk_fp8_f32 v144, v68, v145
	v_med3_f32 v149, v149, s41, v1
	v_mov_b32_e32 v145, v69
	s_waitcnt vmcnt(36)
	v_cvt_pk_f32_fp8_e32 v[164:165], v118
	v_med3_f32 v68, v156, s41, v1
	v_med3_f32 v150, v157, s41, v1
	v_cvt_pk_fp8_f32 v145, v148, v149
	v_cvt_pk_fp8_f32 v144, v68, v150 op_sel:[0,0,1]
	v_pk_fma_f32 v[150:151], v[62:63], v[180:181], v[14:15]
	v_med3_f32 v68, v140, s41, v1
	v_pk_fma_f32 v[150:151], v[50:51], v[168:169], v[150:151]
	v_med3_f32 v140, v141, s41, v1
	v_pk_fma_f32 v[150:151], v[34:35], v[164:165], v[150:151]
	v_cvt_pk_fp8_f32 v145, v68, v140 op_sel:[0,0,1]
	v_mul_f32_e32 v68, 0xbfb8aa3b, v150
	s_waitcnt vmcnt(35)
	v_cvt_pk_f32_fp8_e32 v[160:161], v114
	v_cvt_pk_f32_fp8_sdwa v[148:149], v114 src0_sel:WORD_1
	v_exp_f32_e32 v68, v68
	v_mul_f32_e32 v114, 0xbfb8aa3b, v151
	v_exp_f32_e32 v157, v114
	v_pk_fma_f32 v[162:163], v[58:59], v[178:179], v[10:11]
	v_add_f32_e32 v68, 1.0, v68
	v_rcp_f32_e32 v156, v68
	v_add_f32_e32 v68, 1.0, v157
	v_rcp_f32_e32 v157, v68
	v_cvt_pk_f32_fp8_sdwa v[152:153], v118 src0_sel:WORD_1
	v_pk_fma_f32 v[162:163], v[42:43], v[158:159], v[162:163]
	v_add_co_u32_e32 v140, vcc, s56, v70
	v_pk_fma_f32 v[162:163], v[26:27], v[160:161], v[162:163]
	v_pk_mul_f32 v[150:151], v[150:151], v[156:157]
	v_pk_mul_f32 v[156:157], v[162:163], 4.0 op_sel_hi:[1,0]
	v_pk_fma_f32 v[162:163], v[64:65], v[176:177], v[16:17]
	v_pk_mul_f32 v[150:151], v[156:157], v[150:151]
	v_pk_fma_f32 v[162:163], v[52:53], v[154:155], v[162:163]
	v_addc_co_u32_e32 v141, vcc, 0, v71, vcc
	v_pk_fma_f32 v[162:163], v[36:37], v[152:153], v[162:163]
	global_store_dwordx2 v[140:141], v[144:145], off offset:768
	v_mul_f32_e32 v68, 0xbfb8aa3b, v162
	v_exp_f32_e32 v68, v68
	v_mul_f32_e32 v170, 0xbfb8aa3b, v163
	v_exp_f32_e32 v170, v170
	v_cvt_pk_f32_fp8_e32 v[144:145], v119
	v_add_f32_e32 v68, 1.0, v68
	v_rcp_f32_e32 v156, v68
	v_add_f32_e32 v68, 1.0, v170
	v_rcp_f32_e32 v157, v68
	v_pk_fma_f32 v[170:171], v[60:61], v[174:175], v[12:13]
	v_cvt_pk_f32_fp8_sdwa v[118:119], v119 src0_sel:WORD_1
	v_pk_fma_f32 v[170:171], v[44:45], v[146:147], v[170:171]
	v_pk_mul_f32 v[156:157], v[162:163], v[156:157]
	v_pk_fma_f32 v[170:171], v[28:29], v[148:149], v[170:171]
	v_pk_fma_f32 v[134:135], v[56:57], v[134:135], v[8:9]
	v_pk_mul_f32 v[162:163], v[170:171], 4.0 op_sel_hi:[1,0]
	v_pk_fma_f32 v[170:171], v[54:55], v[172:173], v[6:7]
	v_pk_mul_f32 v[156:157], v[162:163], v[156:157]
	v_pk_fma_f32 v[170:171], v[38:39], v[142:143], v[170:171]
	v_pk_fma_f32 v[134:135], v[40:41], v[126:127], v[134:135]
	v_pk_fma_f32 v[170:171], v[22:23], v[144:145], v[170:171]
	v_pk_fma_f32 v[134:135], v[24:25], v[118:119], v[134:135]
	v_mul_f32_e32 v68, 0xbfb8aa3b, v170
	v_exp_f32_e32 v68, v68
	v_mul_f32_e32 v172, 0xbfb8aa3b, v171
	v_exp_f32_e32 v172, v172
	v_cvt_pk_f32_fp8_e32 v[140:141], v115
	v_add_f32_e32 v68, 1.0, v68
	v_rcp_f32_e32 v162, v68
	v_add_f32_e32 v68, 1.0, v172
	v_rcp_f32_e32 v163, v68
	v_mul_f32_e32 v68, 0xbfb8aa3b, v134
	v_exp_f32_e32 v68, v68
	v_pk_fma_f32 v[166:167], v[46:47], v[166:167], v[2:3]
	v_pk_mul_f32 v[162:163], v[170:171], v[162:163]
	v_mul_f32_e32 v170, 0xbfb8aa3b, v135
	v_exp_f32_e32 v170, v170
	v_pk_fma_f32 v[166:167], v[30:31], v[138:139], v[166:167]
	v_add_f32_e32 v68, 1.0, v68
	v_pk_fma_f32 v[166:167], v[18:19], v[140:141], v[166:167]
	v_cvt_pk_f32_fp8_sdwa v[114:115], v115 src0_sel:WORD_1
	v_pk_mul_f32 v[166:167], v[166:167], 4.0 op_sel_hi:[1,0]
	v_pk_fma_f32 v[130:131], v[48:49], v[130:131], v[4:5]
	v_pk_mul_f32 v[162:163], v[166:167], v[162:163]
	v_rcp_f32_e32 v166, v68
	v_add_f32_e32 v68, 1.0, v170
	v_rcp_f32_e32 v167, v68
	v_pk_fma_f32 v[130:131], v[32:33], v[122:123], v[130:131]
	v_med3_f32 v68, v150, s41, v1
	v_pk_fma_f32 v[130:131], v[20:21], v[114:115], v[130:131]
	v_pk_mul_f32 v[134:135], v[134:135], v[166:167]
	v_pk_mul_f32 v[130:131], v[130:131], 4.0 op_sel_hi:[1,0]
	s_waitcnt vmcnt(35)
	v_cvt_pk_f32_fp8_e32 v[166:167], v110
	v_pk_mul_f32 v[130:131], v[130:131], v[134:135]
	v_med3_f32 v135, v151, s41, v1
	v_mov_b32_e32 v134, v69
	v_cvt_pk_fp8_f32 v134, v68, v135
	v_med3_f32 v68, v156, s41, v1
	v_med3_f32 v151, v162, s41, v1
	v_med3_f32 v156, v163, s41, v1
	v_mov_b32_e32 v135, v69
	v_cvt_pk_fp8_f32 v135, v151, v156
	v_pk_fma_f32 v[168:169], v[62:63], v[168:169], v[14:15]
	v_med3_f32 v150, v157, s41, v1
	v_pk_fma_f32 v[168:169], v[50:51], v[164:165], v[168:169]
	v_cvt_pk_fp8_f32 v134, v68, v150 op_sel:[0,0,1]
	v_med3_f32 v68, v130, s41, v1
	v_med3_f32 v130, v131, s41, v1
	v_pk_fma_f32 v[168:169], v[34:35], v[166:167], v[168:169]
	v_cvt_pk_fp8_f32 v135, v68, v130 op_sel:[0,0,1]
	v_mul_f32_e32 v68, 0xbfb8aa3b, v168
	s_waitcnt vmcnt(34)
	v_cvt_pk_f32_fp8_e32 v[162:163], v106
	v_cvt_pk_f32_fp8_sdwa v[150:151], v106 src0_sel:WORD_1
	v_exp_f32_e32 v68, v68
	v_mul_f32_e32 v106, 0xbfb8aa3b, v169
	v_exp_f32_e32 v171, v106
	v_cvt_pk_f32_fp8_sdwa v[156:157], v110 src0_sel:WORD_1
	v_add_f32_e32 v68, 1.0, v68
	v_rcp_f32_e32 v170, v68
	v_add_f32_e32 v68, 1.0, v171
	v_rcp_f32_e32 v171, v68
	v_pk_fma_f32 v[154:155], v[64:65], v[154:155], v[16:17]
	v_pk_fma_f32 v[158:159], v[58:59], v[158:159], v[10:11]
	v_pk_fma_f32 v[154:155], v[52:53], v[152:153], v[154:155]
	v_pk_mul_f32 v[168:169], v[168:169], v[170:171]
	v_pk_fma_f32 v[154:155], v[36:37], v[156:157], v[154:155]
	v_add_co_u32_e32 v130, vcc, s29, v70
	v_mul_f32_e32 v68, 0xbfb8aa3b, v154
	v_exp_f32_e32 v68, v68
	v_mul_f32_e32 v170, 0xbfb8aa3b, v155
	v_exp_f32_e32 v170, v170
	v_pk_fma_f32 v[158:159], v[42:43], v[160:161], v[158:159]
	v_addc_co_u32_e32 v131, vcc, 0, v71, vcc
	v_pk_fma_f32 v[158:159], v[26:27], v[162:163], v[158:159]
	global_store_dwordx2 v[130:131], v[134:135], off offset:3584
	v_cvt_pk_f32_fp8_e32 v[134:135], v111
	v_pk_mul_f32 v[158:159], v[158:159], 4.0 op_sel_hi:[1,0]
	v_add_f32_e32 v68, 1.0, v68
	v_pk_mul_f32 v[158:159], v[158:159], v[168:169]
	v_rcp_f32_e32 v168, v68
	v_add_f32_e32 v68, 1.0, v170
	v_rcp_f32_e32 v169, v68
	v_pk_fma_f32 v[142:143], v[54:55], v[142:143], v[6:7]
	v_pk_fma_f32 v[146:147], v[60:61], v[146:147], v[12:13]
	v_pk_fma_f32 v[142:143], v[38:39], v[144:145], v[142:143]
	v_pk_mul_f32 v[154:155], v[154:155], v[168:169]
	v_pk_fma_f32 v[142:143], v[22:23], v[134:135], v[142:143]
	v_pk_fma_f32 v[146:147], v[44:45], v[148:149], v[146:147]
	v_mul_f32_e32 v68, 0xbfb8aa3b, v142
	v_exp_f32_e32 v68, v68
	v_mul_f32_e32 v168, 0xbfb8aa3b, v143
	v_exp_f32_e32 v168, v168
	v_pk_fma_f32 v[146:147], v[28:29], v[150:151], v[146:147]
	v_cvt_pk_f32_fp8_sdwa v[110:111], v111 src0_sel:WORD_1
	v_pk_mul_f32 v[146:147], v[146:147], 4.0 op_sel_hi:[1,0]
	v_add_f32_e32 v68, 1.0, v68
	v_pk_mul_f32 v[146:147], v[146:147], v[154:155]
	v_rcp_f32_e32 v154, v68
	v_add_f32_e32 v68, 1.0, v168
	v_rcp_f32_e32 v155, v68
	v_pk_fma_f32 v[126:127], v[56:57], v[126:127], v[8:9]
	v_cvt_pk_f32_fp8_e32 v[130:131], v107
	v_pk_fma_f32 v[126:127], v[40:41], v[118:119], v[126:127]
	v_pk_mul_f32 v[142:143], v[142:143], v[154:155]
	v_pk_fma_f32 v[126:127], v[24:25], v[110:111], v[126:127]
	v_pk_fma_f32 v[138:139], v[46:47], v[138:139], v[2:3]
	v_mul_f32_e32 v68, 0xbfb8aa3b, v126
	v_exp_f32_e32 v68, v68
	v_mul_f32_e32 v154, 0xbfb8aa3b, v127
	v_exp_f32_e32 v154, v154
	v_pk_fma_f32 v[138:139], v[30:31], v[140:141], v[138:139]
	v_add_f32_e32 v68, 1.0, v68
	v_pk_fma_f32 v[138:139], v[18:19], v[130:131], v[138:139]
	v_cvt_pk_f32_fp8_sdwa v[106:107], v107 src0_sel:WORD_1
	v_pk_mul_f32 v[138:139], v[138:139], 4.0 op_sel_hi:[1,0]
	v_pk_fma_f32 v[122:123], v[48:49], v[122:123], v[4:5]
	v_pk_mul_f32 v[138:139], v[138:139], v[142:143]
	v_rcp_f32_e32 v142, v68
	v_add_f32_e32 v68, 1.0, v154
	v_rcp_f32_e32 v143, v68
	v_pk_fma_f32 v[122:123], v[32:33], v[114:115], v[122:123]
	v_med3_f32 v68, v158, s41, v1
	v_pk_fma_f32 v[122:123], v[20:21], v[106:107], v[122:123]
	v_pk_mul_f32 v[126:127], v[126:127], v[142:143]
	v_pk_mul_f32 v[122:123], v[122:123], 4.0 op_sel_hi:[1,0]
	v_med3_f32 v138, v138, s41, v1
	v_pk_mul_f32 v[122:123], v[122:123], v[126:127]
	v_med3_f32 v127, v159, s41, v1
	v_mov_b32_e32 v126, v69
	v_cvt_pk_fp8_f32 v126, v68, v127
	v_med3_f32 v139, v139, s41, v1
	v_mov_b32_e32 v127, v69
	s_waitcnt vmcnt(34)
	v_cvt_pk_f32_fp8_e32 v[154:155], v102
	v_cvt_pk_fp8_f32 v127, v138, v139
	v_pk_fma_f32 v[158:159], v[62:63], v[164:165], v[14:15]
	v_med3_f32 v68, v146, s41, v1
	v_med3_f32 v142, v147, s41, v1
	v_pk_fma_f32 v[158:159], v[50:51], v[166:167], v[158:159]
	v_cvt_pk_fp8_f32 v126, v68, v142 op_sel:[0,0,1]
	v_med3_f32 v68, v122, s41, v1
	v_med3_f32 v122, v123, s41, v1
	v_pk_fma_f32 v[158:159], v[34:35], v[154:155], v[158:159]
	v_cvt_pk_fp8_f32 v127, v68, v122 op_sel:[0,0,1]
	v_mul_f32_e32 v68, 0xbfb8aa3b, v158
	s_waitcnt vmcnt(33)
	v_cvt_pk_f32_fp8_e32 v[146:147], v98
	v_cvt_pk_f32_fp8_sdwa v[138:139], v98 src0_sel:WORD_1
	v_exp_f32_e32 v68, v68
	v_mul_f32_e32 v98, 0xbfb8aa3b, v159
	v_exp_f32_e32 v165, v98
	v_cvt_pk_f32_fp8_sdwa v[142:143], v102 src0_sel:WORD_1
	v_add_f32_e32 v68, 1.0, v68
	v_rcp_f32_e32 v164, v68
	v_add_f32_e32 v68, 1.0, v165
	v_rcp_f32_e32 v165, v68
	v_pk_fma_f32 v[152:153], v[64:65], v[152:153], v[16:17]
	v_pk_fma_f32 v[160:161], v[58:59], v[160:161], v[10:11]
	v_pk_fma_f32 v[152:153], v[52:53], v[156:157], v[152:153]
	v_pk_mul_f32 v[158:159], v[158:159], v[164:165]
	v_pk_fma_f32 v[152:153], v[36:37], v[142:143], v[152:153]
	v_add_co_u32_e32 v122, vcc, s57, v70
	v_mul_f32_e32 v68, 0xbfb8aa3b, v152
	v_exp_f32_e32 v68, v68
	v_mul_f32_e32 v164, 0xbfb8aa3b, v153
	v_exp_f32_e32 v164, v164
	v_pk_fma_f32 v[160:161], v[42:43], v[162:163], v[160:161]
	v_addc_co_u32_e32 v123, vcc, 0, v71, vcc
	v_pk_fma_f32 v[160:161], v[26:27], v[146:147], v[160:161]
	global_store_dwordx2 v[122:123], v[126:127], off offset:2304
	v_cvt_pk_f32_fp8_e32 v[126:127], v103
	v_pk_mul_f32 v[160:161], v[160:161], 4.0 op_sel_hi:[1,0]
	v_add_f32_e32 v68, 1.0, v68
	v_pk_mul_f32 v[158:159], v[160:161], v[158:159]
	v_rcp_f32_e32 v160, v68
	v_add_f32_e32 v68, 1.0, v164
	v_rcp_f32_e32 v161, v68
	v_pk_fma_f32 v[144:145], v[54:55], v[144:145], v[6:7]
	v_pk_fma_f32 v[148:149], v[60:61], v[148:149], v[12:13]
	v_pk_fma_f32 v[144:145], v[38:39], v[134:135], v[144:145]
	v_pk_mul_f32 v[152:153], v[152:153], v[160:161]
	v_pk_fma_f32 v[144:145], v[22:23], v[126:127], v[144:145]
	v_pk_fma_f32 v[148:149], v[44:45], v[150:151], v[148:149]
	v_mul_f32_e32 v68, 0xbfb8aa3b, v144
	v_exp_f32_e32 v68, v68
	v_mul_f32_e32 v160, 0xbfb8aa3b, v145
	v_exp_f32_e32 v160, v160
	v_pk_fma_f32 v[148:149], v[28:29], v[138:139], v[148:149]
	v_cvt_pk_f32_fp8_sdwa v[102:103], v103 src0_sel:WORD_1
	v_pk_mul_f32 v[148:149], v[148:149], 4.0 op_sel_hi:[1,0]
	v_add_f32_e32 v68, 1.0, v68
	v_pk_mul_f32 v[148:149], v[148:149], v[152:153]
	v_rcp_f32_e32 v152, v68
	v_add_f32_e32 v68, 1.0, v160
	v_rcp_f32_e32 v153, v68
	v_pk_fma_f32 v[118:119], v[56:57], v[118:119], v[8:9]
	v_cvt_pk_f32_fp8_e32 v[122:123], v99
	v_pk_fma_f32 v[118:119], v[40:41], v[110:111], v[118:119]
	v_pk_mul_f32 v[144:145], v[144:145], v[152:153]
	v_pk_fma_f32 v[118:119], v[24:25], v[102:103], v[118:119]
	v_pk_fma_f32 v[140:141], v[46:47], v[140:141], v[2:3]
	v_mul_f32_e32 v68, 0xbfb8aa3b, v118
	v_exp_f32_e32 v68, v68
	v_mul_f32_e32 v152, 0xbfb8aa3b, v119
	v_exp_f32_e32 v152, v152
	v_pk_fma_f32 v[140:141], v[30:31], v[130:131], v[140:141]
	v_add_f32_e32 v68, 1.0, v68
	v_pk_fma_f32 v[140:141], v[18:19], v[122:123], v[140:141]
	v_cvt_pk_f32_fp8_sdwa v[98:99], v99 src0_sel:WORD_1
	v_pk_mul_f32 v[140:141], v[140:141], 4.0 op_sel_hi:[1,0]
	v_pk_fma_f32 v[114:115], v[48:49], v[114:115], v[4:5]
	v_pk_mul_f32 v[140:141], v[140:141], v[144:145]
	v_rcp_f32_e32 v144, v68
	v_add_f32_e32 v68, 1.0, v152
	v_rcp_f32_e32 v145, v68
	v_pk_fma_f32 v[114:115], v[32:33], v[106:107], v[114:115]
	v_med3_f32 v68, v158, s41, v1
	v_pk_fma_f32 v[114:115], v[20:21], v[98:99], v[114:115]
	v_pk_mul_f32 v[118:119], v[118:119], v[144:145]
	v_pk_mul_f32 v[114:115], v[114:115], 4.0 op_sel_hi:[1,0]
	v_med3_f32 v140, v140, s41, v1
	v_pk_mul_f32 v[114:115], v[114:115], v[118:119]
	v_med3_f32 v119, v159, s41, v1
	v_mov_b32_e32 v118, v69
	v_cvt_pk_fp8_f32 v118, v68, v119
	v_med3_f32 v141, v141, s41, v1
	v_mov_b32_e32 v119, v69
	s_waitcnt vmcnt(33)
	v_cvt_pk_f32_fp8_e32 v[174:175], v94
	v_cvt_pk_fp8_f32 v119, v140, v141
	v_pk_fma_f32 v[140:141], v[62:63], v[166:167], v[14:15]
	v_med3_f32 v68, v148, s41, v1
	v_med3_f32 v144, v149, s41, v1
	v_pk_fma_f32 v[140:141], v[50:51], v[154:155], v[140:141]
	v_cvt_pk_fp8_f32 v118, v68, v144 op_sel:[0,0,1]
	v_med3_f32 v68, v114, s41, v1
	v_med3_f32 v114, v115, s41, v1
	v_pk_fma_f32 v[140:141], v[34:35], v[174:175], v[140:141]
	v_cvt_pk_fp8_f32 v119, v68, v114 op_sel:[0,0,1]
	v_mul_f32_e32 v68, 0xbfb8aa3b, v140
	s_waitcnt vmcnt(32)
	v_cvt_pk_f32_fp8_e32 v[172:173], v90
	v_cvt_pk_f32_fp8_sdwa v[164:165], v90 src0_sel:WORD_1
	v_exp_f32_e32 v68, v68
	v_mul_f32_e32 v90, 0xbfb8aa3b, v141
	v_exp_f32_e32 v145, v90
	v_pk_fma_f32 v[148:149], v[58:59], v[162:163], v[10:11]
	v_add_f32_e32 v68, 1.0, v68
	v_rcp_f32_e32 v144, v68
	v_add_f32_e32 v68, 1.0, v145
	v_rcp_f32_e32 v145, v68
	v_cvt_pk_f32_fp8_sdwa v[170:171], v94 src0_sel:WORD_1
	v_pk_fma_f32 v[148:149], v[42:43], v[146:147], v[148:149]
	v_add_co_u32_e32 v114, vcc, s30, v70
	v_pk_fma_f32 v[148:149], v[26:27], v[172:173], v[148:149]
	v_pk_mul_f32 v[140:141], v[140:141], v[144:145]
	v_pk_mul_f32 v[144:145], v[148:149], 4.0 op_sel_hi:[1,0]
	v_pk_fma_f32 v[148:149], v[64:65], v[156:157], v[16:17]
	v_addc_co_u32_e32 v115, vcc, 0, v71, vcc
	v_pk_fma_f32 v[148:149], v[52:53], v[142:143], v[148:149]
	global_store_dwordx2 v[114:115], v[118:119], off offset:1024
	v_pk_fma_f32 v[148:149], v[36:37], v[170:171], v[148:149]
	v_cvt_pk_f32_fp8_e32 v[118:119], v95
	v_mul_f32_e32 v68, 0xbfb8aa3b, v148
	v_exp_f32_e32 v68, v68
	v_mul_f32_e32 v152, 0xbfb8aa3b, v149
	v_exp_f32_e32 v152, v152
	v_pk_mul_f32 v[140:141], v[144:145], v[140:141]
	v_add_f32_e32 v68, 1.0, v68
	v_rcp_f32_e32 v144, v68
	v_add_f32_e32 v68, 1.0, v152
	v_rcp_f32_e32 v145, v68
	v_pk_fma_f32 v[134:135], v[54:55], v[134:135], v[6:7]
	v_pk_fma_f32 v[150:151], v[60:61], v[150:151], v[12:13]
	v_pk_fma_f32 v[134:135], v[38:39], v[126:127], v[134:135]
	v_pk_fma_f32 v[150:151], v[44:45], v[138:139], v[150:151]
	v_pk_fma_f32 v[134:135], v[22:23], v[118:119], v[134:135]
	v_pk_fma_f32 v[150:151], v[28:29], v[164:165], v[150:151]
	v_mul_f32_e32 v68, 0xbfb8aa3b, v134
	v_pk_mul_f32 v[144:145], v[148:149], v[144:145]
	v_pk_mul_f32 v[148:149], v[150:151], 4.0 op_sel_hi:[1,0]
	v_exp_f32_e32 v68, v68
	v_mul_f32_e32 v150, 0xbfb8aa3b, v135
	v_exp_f32_e32 v150, v150
	v_cvt_pk_f32_fp8_sdwa v[94:95], v95 src0_sel:WORD_1
	v_add_f32_e32 v68, 1.0, v68
	v_pk_mul_f32 v[144:145], v[148:149], v[144:145]
	v_rcp_f32_e32 v148, v68
	v_add_f32_e32 v68, 1.0, v150
	v_rcp_f32_e32 v149, v68
	v_pk_fma_f32 v[110:111], v[56:57], v[110:111], v[8:9]
	v_cvt_pk_f32_fp8_e32 v[114:115], v91
	v_pk_fma_f32 v[110:111], v[40:41], v[102:103], v[110:111]
	v_pk_mul_f32 v[134:135], v[134:135], v[148:149]
	v_pk_fma_f32 v[110:111], v[24:25], v[94:95], v[110:111]
	v_pk_fma_f32 v[130:131], v[46:47], v[130:131], v[2:3]
	v_mul_f32_e32 v68, 0xbfb8aa3b, v110
	v_exp_f32_e32 v68, v68
	v_mul_f32_e32 v148, 0xbfb8aa3b, v111
	v_exp_f32_e32 v148, v148
	v_pk_fma_f32 v[130:131], v[30:31], v[122:123], v[130:131]
	v_add_f32_e32 v68, 1.0, v68
	v_pk_fma_f32 v[130:131], v[18:19], v[114:115], v[130:131]
	v_cvt_pk_f32_fp8_sdwa v[90:91], v91 src0_sel:WORD_1
	v_pk_mul_f32 v[130:131], v[130:131], 4.0 op_sel_hi:[1,0]
	v_pk_fma_f32 v[106:107], v[48:49], v[106:107], v[4:5]
	v_pk_mul_f32 v[130:131], v[130:131], v[134:135]
	v_rcp_f32_e32 v134, v68
	v_add_f32_e32 v68, 1.0, v148
	v_rcp_f32_e32 v135, v68
	v_pk_fma_f32 v[106:107], v[32:33], v[98:99], v[106:107]
	v_med3_f32 v68, v140, s41, v1
	v_pk_fma_f32 v[106:107], v[20:21], v[90:91], v[106:107]
	v_pk_mul_f32 v[110:111], v[110:111], v[134:135]
	v_pk_mul_f32 v[106:107], v[106:107], 4.0 op_sel_hi:[1,0]
	v_med3_f32 v130, v130, s41, v1
	v_pk_mul_f32 v[106:107], v[106:107], v[110:111]
	v_med3_f32 v111, v141, s41, v1
	v_mov_b32_e32 v110, v69
	v_cvt_pk_fp8_f32 v110, v68, v111
	v_med3_f32 v131, v131, s41, v1
	v_mov_b32_e32 v111, v69
	v_cvt_pk_fp8_f32 v111, v130, v131
	s_waitcnt vmcnt(32)
	v_cvt_pk_f32_fp8_e32 v[166:167], v86
	v_med3_f32 v68, v144, s41, v1
	v_med3_f32 v134, v145, s41, v1
	v_cvt_pk_fp8_f32 v110, v68, v134 op_sel:[0,0,1]
	v_med3_f32 v68, v106, s41, v1
	v_med3_f32 v106, v107, s41, v1
	v_cvt_pk_f32_fp8_sdwa v[156:157], v86 src0_sel:WORD_1
	v_cvt_pk_f32_fp8_e32 v[148:149], v87
	v_cvt_pk_f32_fp8_sdwa v[134:135], v87 src0_sel:WORD_1
	v_pk_fma_f32 v[86:87], v[62:63], v[154:155], v[14:15]
	v_cvt_pk_fp8_f32 v111, v68, v106 op_sel:[0,0,1]
	v_pk_fma_f32 v[86:87], v[50:51], v[174:175], v[86:87]
	v_add_co_u32_e32 v106, vcc, s58, v70
	v_pk_fma_f32 v[86:87], v[34:35], v[166:167], v[86:87]
	s_nop 0
	v_addc_co_u32_e32 v107, vcc, 0, v71, vcc
	v_mul_f32_e32 v68, 0xbfb8aa3b, v86
	s_waitcnt vmcnt(31)
	v_cvt_pk_f32_fp8_e32 v[160:161], v82
	v_cvt_pk_f32_fp8_sdwa v[152:153], v82 src0_sel:WORD_1
	v_exp_f32_e32 v68, v68
	v_mul_f32_e32 v82, 0xbfb8aa3b, v87
	global_store_dwordx2 v[106:107], v[110:111], off offset:3840
	v_exp_f32_e32 v106, v82
	v_add_f32_e32 v68, 1.0, v68
	v_rcp_f32_e32 v82, v68
	v_cvt_pk_f32_fp8_e32 v[144:145], v83
	v_add_f32_e32 v68, 1.0, v106
	v_cvt_pk_f32_fp8_sdwa v[140:141], v83 src0_sel:WORD_1
	v_rcp_f32_e32 v83, v68
	v_pk_fma_f32 v[106:107], v[58:59], v[146:147], v[10:11]
	v_pk_fma_f32 v[102:103], v[56:57], v[102:103], v[8:9]
	v_pk_fma_f32 v[106:107], v[42:43], v[172:173], v[106:107]
	v_pk_mul_f32 v[82:83], v[86:87], v[82:83]
	v_pk_fma_f32 v[106:107], v[26:27], v[160:161], v[106:107]
	v_pk_fma_f32 v[122:123], v[46:47], v[122:123], v[2:3]
	v_pk_mul_f32 v[86:87], v[106:107], 4.0 op_sel_hi:[1,0]
	v_pk_fma_f32 v[106:107], v[64:65], v[142:143], v[16:17]
	v_pk_mul_f32 v[82:83], v[86:87], v[82:83]
	v_pk_fma_f32 v[106:107], v[52:53], v[170:171], v[106:107]
	v_pk_fma_f32 v[102:103], v[40:41], v[94:95], v[102:103]
	v_pk_fma_f32 v[106:107], v[36:37], v[156:157], v[106:107]
	v_pk_fma_f32 v[122:123], v[30:31], v[114:115], v[122:123]
	v_mul_f32_e32 v68, 0xbfb8aa3b, v106
	v_exp_f32_e32 v68, v68
	v_mul_f32_e32 v110, 0xbfb8aa3b, v107
	v_exp_f32_e32 v110, v110
	v_pk_fma_f32 v[102:103], v[24:25], v[134:135], v[102:103]
	v_add_f32_e32 v68, 1.0, v68
	v_rcp_f32_e32 v86, v68
	v_add_f32_e32 v68, 1.0, v110
	v_rcp_f32_e32 v87, v68
	v_pk_fma_f32 v[110:111], v[60:61], v[138:139], v[12:13]
	v_pk_fma_f32 v[122:123], v[18:19], v[144:145], v[122:123]
	v_pk_fma_f32 v[110:111], v[44:45], v[164:165], v[110:111]
	v_pk_mul_f32 v[86:87], v[106:107], v[86:87]
	v_pk_fma_f32 v[110:111], v[28:29], v[152:153], v[110:111]
	v_pk_fma_f32 v[98:99], v[48:49], v[98:99], v[4:5]
	v_pk_mul_f32 v[106:107], v[110:111], 4.0 op_sel_hi:[1,0]
	v_pk_fma_f32 v[110:111], v[54:55], v[126:127], v[6:7]
	v_pk_mul_f32 v[86:87], v[106:107], v[86:87]
	v_pk_fma_f32 v[110:111], v[38:39], v[118:119], v[110:111]
	v_pk_fma_f32 v[98:99], v[32:33], v[90:91], v[98:99]
	v_pk_fma_f32 v[110:111], v[22:23], v[148:149], v[110:111]
	v_pk_fma_f32 v[98:99], v[20:21], v[140:141], v[98:99]
	v_mul_f32_e32 v68, 0xbfb8aa3b, v110
	v_exp_f32_e32 v68, v68
	v_mul_f32_e32 v126, 0xbfb8aa3b, v111
	v_exp_f32_e32 v126, v126
	v_pk_mul_f32 v[98:99], v[98:99], 4.0 op_sel_hi:[1,0]
	v_add_f32_e32 v68, 1.0, v68
	v_rcp_f32_e32 v106, v68
	v_add_f32_e32 v68, 1.0, v126
	v_rcp_f32_e32 v107, v68
	v_mul_f32_e32 v68, 0xbfb8aa3b, v102
	v_exp_f32_e32 v68, v68
	v_med3_f32 v83, v83, s41, v1
	v_pk_mul_f32 v[106:107], v[110:111], v[106:107]
	v_pk_mul_f32 v[110:111], v[122:123], 4.0 op_sel_hi:[1,0]
	v_mul_f32_e32 v122, 0xbfb8aa3b, v103
	v_exp_f32_e32 v122, v122
	v_add_f32_e32 v68, 1.0, v68
	v_pk_mul_f32 v[106:107], v[110:111], v[106:107]
	v_rcp_f32_e32 v110, v68
	v_add_f32_e32 v68, 1.0, v122
	v_rcp_f32_e32 v111, v68
	v_med3_f32 v68, v82, s41, v1
	v_mov_b32_e32 v82, v69
	v_cvt_pk_fp8_f32 v82, v68, v83
	v_pk_mul_f32 v[102:103], v[102:103], v[110:111]
	v_med3_f32 v68, v86, s41, v1
	v_pk_mul_f32 v[98:99], v[98:99], v[102:103]
	v_med3_f32 v86, v87, s41, v1
	v_med3_f32 v87, v106, s41, v1
	v_med3_f32 v102, v107, s41, v1
	v_mov_b32_e32 v83, v69
	v_cvt_pk_fp8_f32 v83, v87, v102
	s_waitcnt vmcnt(31)
	v_cvt_pk_f32_fp8_e32 v[168:169], v78
	v_cvt_pk_fp8_f32 v82, v68, v86 op_sel:[0,0,1]
	v_med3_f32 v68, v98, s41, v1
	v_med3_f32 v86, v99, s41, v1
	v_cvt_pk_f32_fp8_sdwa v[158:159], v78 src0_sel:WORD_1
	v_cvt_pk_f32_fp8_e32 v[150:151], v79
	v_cvt_pk_f32_fp8_sdwa v[138:139], v79 src0_sel:WORD_1
	v_pk_fma_f32 v[78:79], v[62:63], v[174:175], v[14:15]
	v_cvt_pk_fp8_f32 v83, v68, v86 op_sel:[0,0,1]
	v_pk_fma_f32 v[78:79], v[50:51], v[166:167], v[78:79]
	v_add_co_u32_e32 v86, vcc, s31, v70
	v_pk_fma_f32 v[78:79], v[34:35], v[168:169], v[78:79]
	s_nop 0
	v_addc_co_u32_e32 v87, vcc, 0, v71, vcc
	v_mul_f32_e32 v68, 0xbfb8aa3b, v78
	s_waitcnt vmcnt(30)
	v_cvt_pk_f32_fp8_e32 v[162:163], v74
	v_cvt_pk_f32_fp8_sdwa v[154:155], v74 src0_sel:WORD_1
	v_exp_f32_e32 v68, v68
	v_mul_f32_e32 v74, 0xbfb8aa3b, v79
	global_store_dwordx2 v[86:87], v[82:83], off offset:2560
	v_exp_f32_e32 v82, v74
	v_add_f32_e32 v68, 1.0, v68
	v_rcp_f32_e32 v74, v68
	v_cvt_pk_f32_fp8_e32 v[146:147], v75
	v_add_f32_e32 v68, 1.0, v82
	v_cvt_pk_f32_fp8_sdwa v[142:143], v75 src0_sel:WORD_1
	v_rcp_f32_e32 v75, v68
	v_pk_fma_f32 v[82:83], v[58:59], v[172:173], v[10:11]
	v_pk_fma_f32 v[94:95], v[56:57], v[94:95], v[8:9]
	v_pk_fma_f32 v[82:83], v[42:43], v[160:161], v[82:83]
	v_pk_mul_f32 v[74:75], v[78:79], v[74:75]
	v_pk_fma_f32 v[82:83], v[26:27], v[162:163], v[82:83]
	v_pk_fma_f32 v[94:95], v[40:41], v[134:135], v[94:95]
	v_pk_mul_f32 v[78:79], v[82:83], 4.0 op_sel_hi:[1,0]
	v_pk_fma_f32 v[82:83], v[64:65], v[170:171], v[16:17]
	v_pk_mul_f32 v[74:75], v[78:79], v[74:75]
	v_pk_fma_f32 v[82:83], v[52:53], v[156:157], v[82:83]
	v_pk_fma_f32 v[94:95], v[24:25], v[138:139], v[94:95]
	v_pk_fma_f32 v[82:83], v[36:37], v[158:159], v[82:83]
	v_pk_fma_f32 v[90:91], v[48:49], v[90:91], v[4:5]
	v_mul_f32_e32 v68, 0xbfb8aa3b, v82
	v_exp_f32_e32 v68, v68
	v_mul_f32_e32 v86, 0xbfb8aa3b, v83
	v_exp_f32_e32 v86, v86
	v_med3_f32 v75, v75, s41, v1
	v_add_f32_e32 v68, 1.0, v68
	v_rcp_f32_e32 v78, v68
	v_add_f32_e32 v68, 1.0, v86
	v_rcp_f32_e32 v79, v68
	v_pk_fma_f32 v[86:87], v[60:61], v[164:165], v[12:13]
	v_pk_fma_f32 v[90:91], v[32:33], v[140:141], v[90:91]
	v_pk_fma_f32 v[86:87], v[44:45], v[152:153], v[86:87]
	v_pk_mul_f32 v[78:79], v[82:83], v[78:79]
	v_pk_fma_f32 v[86:87], v[28:29], v[154:155], v[86:87]
	s_waitcnt vmcnt(22)
	v_cvt_pk_f32_fp8_e32 v[178:179], v136
	v_pk_mul_f32 v[82:83], v[86:87], 4.0 op_sel_hi:[1,0]
	v_pk_fma_f32 v[86:87], v[54:55], v[118:119], v[6:7]
	v_pk_mul_f32 v[78:79], v[82:83], v[78:79]
	v_pk_fma_f32 v[86:87], v[38:39], v[148:149], v[86:87]
	v_pk_fma_f32 v[90:91], v[20:21], v[142:143], v[90:91]
	v_pk_fma_f32 v[86:87], v[22:23], v[150:151], v[86:87]
	v_pk_mul_f32 v[90:91], v[90:91], 4.0 op_sel_hi:[1,0]
	v_mul_f32_e32 v68, 0xbfb8aa3b, v86
	v_exp_f32_e32 v68, v68
	v_mul_f32_e32 v98, 0xbfb8aa3b, v87
	v_exp_f32_e32 v98, v98
	v_pk_fma_f32 v[166:167], v[62:63], v[166:167], v[14:15]
	v_add_f32_e32 v68, 1.0, v68
	v_rcp_f32_e32 v82, v68
	v_add_f32_e32 v68, 1.0, v98
	v_rcp_f32_e32 v83, v68
	v_pk_fma_f32 v[98:99], v[46:47], v[114:115], v[2:3]
	v_mul_f32_e32 v68, 0xbfb8aa3b, v94
	v_pk_fma_f32 v[98:99], v[30:31], v[144:145], v[98:99]
	v_pk_mul_f32 v[82:83], v[86:87], v[82:83]
	v_pk_fma_f32 v[98:99], v[18:19], v[146:147], v[98:99]
	v_exp_f32_e32 v68, v68
	v_pk_mul_f32 v[86:87], v[98:99], 4.0 op_sel_hi:[1,0]
	v_mul_f32_e32 v98, 0xbfb8aa3b, v95
	v_exp_f32_e32 v98, v98
	v_add_f32_e32 v68, 1.0, v68
	v_pk_mul_f32 v[82:83], v[86:87], v[82:83]
	v_rcp_f32_e32 v86, v68
	v_add_f32_e32 v68, 1.0, v98
	v_rcp_f32_e32 v87, v68
	v_med3_f32 v68, v74, s41, v1
	v_mov_b32_e32 v74, v69
	v_cvt_pk_fp8_f32 v74, v68, v75
	v_med3_f32 v68, v78, s41, v1
	v_med3_f32 v78, v79, s41, v1
	v_med3_f32 v79, v82, s41, v1
	v_med3_f32 v82, v83, s41, v1
	v_mov_b32_e32 v75, v69
	v_cvt_pk_fp8_f32 v75, v79, v82
	v_pk_mul_f32 v[86:87], v[94:95], v[86:87]
	v_pk_fma_f32 v[166:167], v[50:51], v[168:169], v[166:167]
	v_pk_mul_f32 v[86:87], v[90:91], v[86:87]
	v_cvt_pk_fp8_f32 v74, v68, v78 op_sel:[0,0,1]
	v_med3_f32 v68, v86, s41, v1
	v_med3_f32 v78, v87, s41, v1
	v_pk_fma_f32 v[166:167], v[34:35], v[178:179], v[166:167]
	v_cvt_pk_fp8_f32 v75, v68, v78 op_sel:[0,0,1]
	v_mul_f32_e32 v68, 0xbfb8aa3b, v166
	s_waitcnt vmcnt(21)
	v_cvt_pk_f32_fp8_e32 v[176:177], v132
	v_cvt_pk_f32_fp8_sdwa v[172:173], v132 src0_sel:WORD_1
	v_exp_f32_e32 v68, v68
	v_mul_f32_e32 v132, 0xbfb8aa3b, v167
	v_exp_f32_e32 v181, v132
	v_cvt_pk_f32_fp8_sdwa v[174:175], v136 src0_sel:WORD_1
	v_add_f32_e32 v68, 1.0, v68
	v_rcp_f32_e32 v180, v68
	v_add_f32_e32 v68, 1.0, v181
	v_rcp_f32_e32 v181, v68
	v_pk_fma_f32 v[156:157], v[64:65], v[156:157], v[16:17]
	v_pk_fma_f32 v[160:161], v[58:59], v[160:161], v[10:11]
	v_pk_fma_f32 v[156:157], v[52:53], v[158:159], v[156:157]
	v_pk_mul_f32 v[166:167], v[166:167], v[180:181]
	v_pk_fma_f32 v[156:157], v[36:37], v[174:175], v[156:157]
	v_pk_fma_f32 v[160:161], v[42:43], v[162:163], v[160:161]
	v_mul_f32_e32 v68, 0xbfb8aa3b, v156
	v_exp_f32_e32 v68, v68
	v_mul_f32_e32 v180, 0xbfb8aa3b, v157
	v_exp_f32_e32 v180, v180
	v_pk_fma_f32 v[160:161], v[26:27], v[176:177], v[160:161]
	v_cvt_pk_f32_fp8_e32 v[170:171], v137
	v_pk_mul_f32 v[160:161], v[160:161], 4.0 op_sel_hi:[1,0]
	v_add_f32_e32 v68, 1.0, v68
	v_pk_mul_f32 v[160:161], v[160:161], v[166:167]
	v_rcp_f32_e32 v166, v68
	v_add_f32_e32 v68, 1.0, v180
	v_rcp_f32_e32 v167, v68
	v_pk_fma_f32 v[148:149], v[54:55], v[148:149], v[6:7]
	v_pk_fma_f32 v[152:153], v[60:61], v[152:153], v[12:13]
	v_pk_fma_f32 v[148:149], v[38:39], v[150:151], v[148:149]
	v_pk_mul_f32 v[156:157], v[156:157], v[166:167]
	v_pk_fma_f32 v[148:149], v[22:23], v[170:171], v[148:149]
	v_pk_fma_f32 v[152:153], v[44:45], v[154:155], v[152:153]
	v_mul_f32_e32 v68, 0xbfb8aa3b, v148
	v_exp_f32_e32 v68, v68
	v_mul_f32_e32 v166, 0xbfb8aa3b, v149
	v_exp_f32_e32 v166, v166
	v_pk_fma_f32 v[152:153], v[28:29], v[172:173], v[152:153]
	v_cvt_pk_f32_fp8_sdwa v[136:137], v137 src0_sel:WORD_1
	v_pk_mul_f32 v[152:153], v[152:153], 4.0 op_sel_hi:[1,0]
	v_add_f32_e32 v68, 1.0, v68
	v_pk_mul_f32 v[152:153], v[152:153], v[156:157]
	v_rcp_f32_e32 v156, v68
	v_add_f32_e32 v68, 1.0, v166
	v_rcp_f32_e32 v157, v68
	v_pk_fma_f32 v[134:135], v[56:57], v[134:135], v[8:9]
	v_cvt_pk_f32_fp8_e32 v[164:165], v133
	v_pk_fma_f32 v[134:135], v[40:41], v[138:139], v[134:135]
	v_pk_mul_f32 v[148:149], v[148:149], v[156:157]
	v_pk_fma_f32 v[134:135], v[24:25], v[136:137], v[134:135]
	v_pk_fma_f32 v[144:145], v[46:47], v[144:145], v[2:3]
	v_mul_f32_e32 v68, 0xbfb8aa3b, v134
	v_exp_f32_e32 v68, v68
	v_mul_f32_e32 v156, 0xbfb8aa3b, v135
	v_exp_f32_e32 v156, v156
	v_pk_fma_f32 v[144:145], v[30:31], v[146:147], v[144:145]
	v_add_f32_e32 v68, 1.0, v68
	v_pk_fma_f32 v[144:145], v[18:19], v[164:165], v[144:145]
	v_cvt_pk_f32_fp8_sdwa v[132:133], v133 src0_sel:WORD_1
	v_pk_mul_f32 v[144:145], v[144:145], 4.0 op_sel_hi:[1,0]
	v_pk_fma_f32 v[140:141], v[48:49], v[140:141], v[4:5]
	v_pk_mul_f32 v[144:145], v[144:145], v[148:149]
	v_rcp_f32_e32 v148, v68
	v_add_f32_e32 v68, 1.0, v156
	v_rcp_f32_e32 v149, v68
	v_pk_fma_f32 v[140:141], v[32:33], v[142:143], v[140:141]
	v_med3_f32 v68, v160, s41, v1
	v_pk_fma_f32 v[140:141], v[20:21], v[132:133], v[140:141]
	v_pk_mul_f32 v[134:135], v[134:135], v[148:149]
	v_pk_mul_f32 v[140:141], v[140:141], 4.0 op_sel_hi:[1,0]
	v_add_co_u32_e32 v78, vcc, s59, v70
	v_pk_mul_f32 v[134:135], v[140:141], v[134:135]
	v_med3_f32 v141, v161, s41, v1
	v_mov_b32_e32 v140, v69
	v_cvt_pk_fp8_f32 v140, v68, v141
	v_med3_f32 v144, v144, s41, v1
	v_med3_f32 v145, v145, s41, v1
	v_mov_b32_e32 v141, v69
	s_waitcnt vmcnt(20)
	v_cvt_pk_f32_fp8_e32 v[166:167], v128
	v_addc_co_u32_e32 v79, vcc, 0, v71, vcc
	v_med3_f32 v68, v152, s41, v1
	v_med3_f32 v148, v153, s41, v1
	v_cvt_pk_fp8_f32 v141, v144, v145
	global_store_dwordx2 v[78:79], v[74:75], off offset:1280
	v_add_co_u32_e32 v74, vcc, s60, v72
	v_cvt_pk_fp8_f32 v140, v68, v148 op_sel:[0,0,1]
	v_pk_fma_f32 v[148:149], v[62:63], v[168:169], v[14:15]
	v_addc_co_u32_e32 v75, vcc, 0, v73, vcc
	v_pk_fma_f32 v[148:149], v[50:51], v[178:179], v[148:149]
	v_add_co_u32_e32 v78, vcc, s61, v72
	v_med3_f32 v68, v134, s41, v1
	v_med3_f32 v134, v135, s41, v1
	v_pk_fma_f32 v[148:149], v[34:35], v[166:167], v[148:149]
	v_addc_co_u32_e32 v79, vcc, 0, v73, vcc
	v_cvt_pk_fp8_f32 v141, v68, v134 op_sel:[0,0,1]
	v_mul_f32_e32 v68, 0xbfb8aa3b, v148
	global_load_dwordx2 v[130:131], v[74:75], off nt
	global_load_dwordx2 v[126:127], v[74:75], off offset:128 nt
	global_load_dwordx2 v[122:123], v[78:79], off offset:1536 nt
	global_load_dwordx2 v[118:119], v[78:79], off offset:1664 nt
	v_add_co_u32_e32 v74, vcc, s62, v72
	s_waitcnt vmcnt(24)
	v_cvt_pk_f32_fp8_e32 v[156:157], v124
	v_cvt_pk_f32_fp8_sdwa v[144:145], v124 src0_sel:WORD_1
	v_exp_f32_e32 v68, v68
	v_mul_f32_e32 v124, 0xbfb8aa3b, v149
	v_addc_co_u32_e32 v75, vcc, 0, v73, vcc
	v_exp_f32_e32 v161, v124
	v_add_co_u32_e32 v78, vcc, s63, v72
	v_cvt_pk_f32_fp8_sdwa v[152:153], v128 src0_sel:WORD_1
	s_nop 0
	v_addc_co_u32_e32 v79, vcc, 0, v73, vcc
	global_load_dwordx2 v[114:115], v[74:75], off offset:3072 nt
	global_load_dwordx2 v[110:111], v[74:75], off offset:3200 nt
	global_load_dwordx2 v[106:107], v[78:79], off offset:512 nt
	global_load_dwordx2 v[102:103], v[78:79], off offset:640 nt
	v_add_co_u32_e32 v74, vcc, s64, v72
	v_add_f32_e32 v68, 1.0, v68
	s_nop 0
	v_addc_co_u32_e32 v75, vcc, 0, v73, vcc
	v_rcp_f32_e32 v160, v68
	v_add_f32_e32 v68, 1.0, v161
	v_add_co_u32_e32 v78, vcc, s65, v72
	v_rcp_f32_e32 v161, v68
	v_pk_fma_f32 v[158:159], v[64:65], v[158:159], v[16:17]
	v_addc_co_u32_e32 v79, vcc, 0, v73, vcc
	v_pk_fma_f32 v[162:163], v[58:59], v[162:163], v[10:11]
	v_pk_fma_f32 v[158:159], v[52:53], v[174:175], v[158:159]
	global_load_dwordx2 v[98:99], v[74:75], off offset:2048 nt
	global_load_dwordx2 v[94:95], v[74:75], off offset:2176 nt
	global_load_dwordx2 v[90:91], v[78:79], off offset:3584 nt
	global_load_dwordx2 v[86:87], v[78:79], off offset:3712 nt
	v_add_co_u32_e32 v74, vcc, s66, v72
	v_pk_fma_f32 v[162:163], v[42:43], v[176:177], v[162:163]
	v_pk_fma_f32 v[158:159], v[36:37], v[152:153], v[158:159]
	v_addc_co_u32_e32 v75, vcc, 0, v73, vcc
	v_pk_fma_f32 v[162:163], v[26:27], v[156:157], v[162:163]
	v_mul_f32_e32 v68, 0xbfb8aa3b, v158
	v_add_co_u32_e32 v72, vcc, s67, v72
	v_pk_mul_f32 v[148:149], v[148:149], v[160:161]
	v_pk_mul_f32 v[160:161], v[162:163], 4.0 op_sel_hi:[1,0]
	v_exp_f32_e32 v68, v68
	v_mul_f32_e32 v162, 0xbfb8aa3b, v159
	v_addc_co_u32_e32 v73, vcc, 0, v73, vcc
	v_exp_f32_e32 v162, v162
	v_add_co_u32_e32 v134, vcc, s33, v70
	global_load_dwordx2 v[82:83], v[74:75], off offset:1024 nt
	global_load_dwordx2 v[78:79], v[74:75], off offset:1152 nt
	s_nop 0
	global_load_dwordx2 v[74:75], v[72:73], off offset:2560 nt
	s_nop 0
	global_load_dwordx2 v[72:73], v[72:73], off offset:2688 nt
	v_addc_co_u32_e32 v135, vcc, 0, v71, vcc
	global_store_dwordx2 v[134:135], v[140:141], off
	v_cvt_pk_f32_fp8_e32 v[140:141], v129
	v_add_f32_e32 v68, 1.0, v68
	v_pk_mul_f32 v[148:149], v[160:161], v[148:149]
	v_rcp_f32_e32 v160, v68
	v_add_f32_e32 v68, 1.0, v162
	v_rcp_f32_e32 v161, v68
	v_pk_fma_f32 v[150:151], v[54:55], v[150:151], v[6:7]
	v_pk_fma_f32 v[154:155], v[60:61], v[154:155], v[12:13]
	v_pk_fma_f32 v[150:151], v[38:39], v[170:171], v[150:151]
	v_pk_mul_f32 v[158:159], v[158:159], v[160:161]
	v_pk_fma_f32 v[150:151], v[22:23], v[140:141], v[150:151]
	v_pk_fma_f32 v[154:155], v[44:45], v[172:173], v[154:155]
	v_mul_f32_e32 v68, 0xbfb8aa3b, v150
	v_exp_f32_e32 v68, v68
	v_mul_f32_e32 v160, 0xbfb8aa3b, v151
	v_exp_f32_e32 v160, v160
	v_pk_fma_f32 v[154:155], v[28:29], v[144:145], v[154:155]
	v_cvt_pk_f32_fp8_sdwa v[128:129], v129 src0_sel:WORD_1
	v_pk_mul_f32 v[154:155], v[154:155], 4.0 op_sel_hi:[1,0]
	v_add_f32_e32 v68, 1.0, v68
	v_pk_mul_f32 v[154:155], v[154:155], v[158:159]
	v_rcp_f32_e32 v158, v68
	v_add_f32_e32 v68, 1.0, v160
	v_rcp_f32_e32 v159, v68
	v_pk_fma_f32 v[138:139], v[56:57], v[138:139], v[8:9]
	v_cvt_pk_f32_fp8_e32 v[134:135], v125
	v_pk_fma_f32 v[138:139], v[40:41], v[136:137], v[138:139]
	v_pk_mul_f32 v[150:151], v[150:151], v[158:159]
	v_pk_fma_f32 v[138:139], v[24:25], v[128:129], v[138:139]
	v_pk_fma_f32 v[146:147], v[46:47], v[146:147], v[2:3]
	v_mul_f32_e32 v68, 0xbfb8aa3b, v138
	v_exp_f32_e32 v68, v68
	v_mul_f32_e32 v158, 0xbfb8aa3b, v139
	v_exp_f32_e32 v158, v158
	v_pk_fma_f32 v[146:147], v[30:31], v[164:165], v[146:147]
	v_add_f32_e32 v68, 1.0, v68
	v_pk_fma_f32 v[146:147], v[18:19], v[134:135], v[146:147]
	v_cvt_pk_f32_fp8_sdwa v[124:125], v125 src0_sel:WORD_1
	v_pk_mul_f32 v[146:147], v[146:147], 4.0 op_sel_hi:[1,0]
	v_pk_fma_f32 v[142:143], v[48:49], v[142:143], v[4:5]
	v_pk_mul_f32 v[146:147], v[146:147], v[150:151]
	v_rcp_f32_e32 v150, v68
	v_add_f32_e32 v68, 1.0, v158
	v_rcp_f32_e32 v151, v68
	v_pk_fma_f32 v[142:143], v[32:33], v[132:133], v[142:143]
	v_med3_f32 v68, v148, s41, v1
	v_pk_fma_f32 v[142:143], v[20:21], v[124:125], v[142:143]
	v_pk_mul_f32 v[138:139], v[138:139], v[150:151]
	v_pk_mul_f32 v[142:143], v[142:143], 4.0 op_sel_hi:[1,0]
	v_med3_f32 v146, v146, s41, v1
	v_pk_mul_f32 v[138:139], v[142:143], v[138:139]
	v_med3_f32 v143, v149, s41, v1
	v_mov_b32_e32 v142, v69
	v_cvt_pk_fp8_f32 v142, v68, v143
	v_med3_f32 v147, v147, s41, v1
	v_mov_b32_e32 v143, v69
	s_waitcnt vmcnt(36)
	v_cvt_pk_f32_fp8_e32 v[162:163], v120
	v_med3_f32 v68, v154, s41, v1
	v_med3_f32 v148, v155, s41, v1
	v_cvt_pk_fp8_f32 v143, v146, v147
	v_cvt_pk_fp8_f32 v142, v68, v148 op_sel:[0,0,1]
	v_pk_fma_f32 v[148:149], v[62:63], v[178:179], v[14:15]
	v_med3_f32 v68, v138, s41, v1
	v_pk_fma_f32 v[148:149], v[50:51], v[166:167], v[148:149]
	v_med3_f32 v138, v139, s41, v1
	v_pk_fma_f32 v[148:149], v[34:35], v[162:163], v[148:149]
	v_cvt_pk_fp8_f32 v143, v68, v138 op_sel:[0,0,1]
	v_mul_f32_e32 v68, 0xbfb8aa3b, v148
	s_waitcnt vmcnt(35)
	v_cvt_pk_f32_fp8_e32 v[158:159], v116
	v_cvt_pk_f32_fp8_sdwa v[146:147], v116 src0_sel:WORD_1
	v_exp_f32_e32 v68, v68
	v_mul_f32_e32 v116, 0xbfb8aa3b, v149
	v_exp_f32_e32 v155, v116
	v_pk_fma_f32 v[160:161], v[58:59], v[176:177], v[10:11]
	v_add_f32_e32 v68, 1.0, v68
	v_rcp_f32_e32 v154, v68
	v_add_f32_e32 v68, 1.0, v155
	v_rcp_f32_e32 v155, v68
	v_cvt_pk_f32_fp8_sdwa v[150:151], v120 src0_sel:WORD_1
	v_pk_fma_f32 v[160:161], v[42:43], v[156:157], v[160:161]
	v_add_co_u32_e32 v138, vcc, s68, v70
	v_pk_fma_f32 v[160:161], v[26:27], v[158:159], v[160:161]
	v_pk_mul_f32 v[148:149], v[148:149], v[154:155]
	v_pk_mul_f32 v[154:155], v[160:161], 4.0 op_sel_hi:[1,0]
	v_pk_fma_f32 v[160:161], v[64:65], v[174:175], v[16:17]
	v_pk_mul_f32 v[148:149], v[154:155], v[148:149]
	v_pk_fma_f32 v[160:161], v[52:53], v[152:153], v[160:161]
	v_addc_co_u32_e32 v139, vcc, 0, v71, vcc
	v_pk_fma_f32 v[160:161], v[36:37], v[150:151], v[160:161]
	global_store_dwordx2 v[138:139], v[142:143], off offset:2816
	v_mul_f32_e32 v68, 0xbfb8aa3b, v160
	v_exp_f32_e32 v68, v68
	v_mul_f32_e32 v168, 0xbfb8aa3b, v161
	v_exp_f32_e32 v168, v168
	v_cvt_pk_f32_fp8_e32 v[142:143], v121
	v_add_f32_e32 v68, 1.0, v68
	v_rcp_f32_e32 v154, v68
	v_add_f32_e32 v68, 1.0, v168
	v_rcp_f32_e32 v155, v68
	v_pk_fma_f32 v[168:169], v[60:61], v[172:173], v[12:13]
	v_cvt_pk_f32_fp8_sdwa v[120:121], v121 src0_sel:WORD_1
	v_pk_fma_f32 v[168:169], v[44:45], v[144:145], v[168:169]
	v_pk_mul_f32 v[154:155], v[160:161], v[154:155]
	v_pk_fma_f32 v[168:169], v[28:29], v[146:147], v[168:169]
	v_pk_fma_f32 v[136:137], v[56:57], v[136:137], v[8:9]
	v_pk_mul_f32 v[160:161], v[168:169], 4.0 op_sel_hi:[1,0]
	v_pk_fma_f32 v[168:169], v[54:55], v[170:171], v[6:7]
	v_pk_mul_f32 v[154:155], v[160:161], v[154:155]
	v_pk_fma_f32 v[168:169], v[38:39], v[140:141], v[168:169]
	v_pk_fma_f32 v[136:137], v[40:41], v[128:129], v[136:137]
	v_pk_fma_f32 v[168:169], v[22:23], v[142:143], v[168:169]
	v_pk_fma_f32 v[136:137], v[24:25], v[120:121], v[136:137]
	v_mul_f32_e32 v68, 0xbfb8aa3b, v168
	v_exp_f32_e32 v68, v68
	v_mul_f32_e32 v170, 0xbfb8aa3b, v169
	v_exp_f32_e32 v170, v170
	v_cvt_pk_f32_fp8_e32 v[138:139], v117
	v_add_f32_e32 v68, 1.0, v68
	v_rcp_f32_e32 v160, v68
	v_add_f32_e32 v68, 1.0, v170
	v_rcp_f32_e32 v161, v68
	v_mul_f32_e32 v68, 0xbfb8aa3b, v136
	v_exp_f32_e32 v68, v68
	v_pk_fma_f32 v[164:165], v[46:47], v[164:165], v[2:3]
	v_pk_mul_f32 v[160:161], v[168:169], v[160:161]
	v_mul_f32_e32 v168, 0xbfb8aa3b, v137
	v_exp_f32_e32 v168, v168
	v_pk_fma_f32 v[164:165], v[30:31], v[134:135], v[164:165]
	v_add_f32_e32 v68, 1.0, v68
	v_pk_fma_f32 v[164:165], v[18:19], v[138:139], v[164:165]
	v_cvt_pk_f32_fp8_sdwa v[116:117], v117 src0_sel:WORD_1
	v_pk_mul_f32 v[164:165], v[164:165], 4.0 op_sel_hi:[1,0]
	v_pk_fma_f32 v[132:133], v[48:49], v[132:133], v[4:5]
	v_pk_mul_f32 v[160:161], v[164:165], v[160:161]
	v_rcp_f32_e32 v164, v68
	v_add_f32_e32 v68, 1.0, v168
	v_rcp_f32_e32 v165, v68
	v_pk_fma_f32 v[132:133], v[32:33], v[124:125], v[132:133]
	v_med3_f32 v68, v148, s41, v1
	v_pk_fma_f32 v[132:133], v[20:21], v[116:117], v[132:133]
	v_pk_mul_f32 v[136:137], v[136:137], v[164:165]
	v_pk_mul_f32 v[132:133], v[132:133], 4.0 op_sel_hi:[1,0]
	s_waitcnt vmcnt(35)
	v_cvt_pk_f32_fp8_e32 v[164:165], v112
	v_pk_mul_f32 v[132:133], v[132:133], v[136:137]
	v_med3_f32 v137, v149, s41, v1
	v_mov_b32_e32 v136, v69
	v_cvt_pk_fp8_f32 v136, v68, v137
	v_med3_f32 v68, v154, s41, v1
	v_med3_f32 v149, v160, s41, v1
	v_med3_f32 v154, v161, s41, v1
	v_mov_b32_e32 v137, v69
	v_cvt_pk_fp8_f32 v137, v149, v154
	v_pk_fma_f32 v[166:167], v[62:63], v[166:167], v[14:15]
	v_med3_f32 v148, v155, s41, v1
	v_pk_fma_f32 v[166:167], v[50:51], v[162:163], v[166:167]
	v_cvt_pk_fp8_f32 v136, v68, v148 op_sel:[0,0,1]
	v_med3_f32 v68, v132, s41, v1
	v_med3_f32 v132, v133, s41, v1
	v_pk_fma_f32 v[166:167], v[34:35], v[164:165], v[166:167]
	v_cvt_pk_fp8_f32 v137, v68, v132 op_sel:[0,0,1]
	v_mul_f32_e32 v68, 0xbfb8aa3b, v166
	s_waitcnt vmcnt(34)
	v_cvt_pk_f32_fp8_e32 v[160:161], v108
	v_cvt_pk_f32_fp8_sdwa v[148:149], v108 src0_sel:WORD_1
	v_exp_f32_e32 v68, v68
	v_mul_f32_e32 v108, 0xbfb8aa3b, v167
	v_exp_f32_e32 v169, v108
	v_cvt_pk_f32_fp8_sdwa v[154:155], v112 src0_sel:WORD_1
	v_add_f32_e32 v68, 1.0, v68
	v_rcp_f32_e32 v168, v68
	v_add_f32_e32 v68, 1.0, v169
	v_rcp_f32_e32 v169, v68
	v_pk_fma_f32 v[152:153], v[64:65], v[152:153], v[16:17]
	v_pk_fma_f32 v[156:157], v[58:59], v[156:157], v[10:11]
	v_pk_fma_f32 v[152:153], v[52:53], v[150:151], v[152:153]
	v_pk_mul_f32 v[166:167], v[166:167], v[168:169]
	v_pk_fma_f32 v[152:153], v[36:37], v[154:155], v[152:153]
	v_add_co_u32_e32 v132, vcc, s34, v70
	v_mul_f32_e32 v68, 0xbfb8aa3b, v152
	v_exp_f32_e32 v68, v68
	v_mul_f32_e32 v168, 0xbfb8aa3b, v153
	v_exp_f32_e32 v168, v168
	v_pk_fma_f32 v[156:157], v[42:43], v[158:159], v[156:157]
	v_addc_co_u32_e32 v133, vcc, 0, v71, vcc
	v_pk_fma_f32 v[156:157], v[26:27], v[160:161], v[156:157]
	global_store_dwordx2 v[132:133], v[136:137], off offset:1536
	v_cvt_pk_f32_fp8_e32 v[136:137], v113
	v_pk_mul_f32 v[156:157], v[156:157], 4.0 op_sel_hi:[1,0]
	v_add_f32_e32 v68, 1.0, v68
	v_pk_mul_f32 v[156:157], v[156:157], v[166:167]
	v_rcp_f32_e32 v166, v68
	v_add_f32_e32 v68, 1.0, v168
	v_rcp_f32_e32 v167, v68
	v_pk_fma_f32 v[140:141], v[54:55], v[140:141], v[6:7]
	v_pk_fma_f32 v[144:145], v[60:61], v[144:145], v[12:13]
	v_pk_fma_f32 v[140:141], v[38:39], v[142:143], v[140:141]
	v_pk_mul_f32 v[152:153], v[152:153], v[166:167]
	v_pk_fma_f32 v[140:141], v[22:23], v[136:137], v[140:141]
	v_pk_fma_f32 v[144:145], v[44:45], v[146:147], v[144:145]
	v_mul_f32_e32 v68, 0xbfb8aa3b, v140
	v_exp_f32_e32 v68, v68
	v_mul_f32_e32 v166, 0xbfb8aa3b, v141
	v_exp_f32_e32 v166, v166
	v_pk_fma_f32 v[144:145], v[28:29], v[148:149], v[144:145]
	v_cvt_pk_f32_fp8_sdwa v[112:113], v113 src0_sel:WORD_1
	v_pk_mul_f32 v[144:145], v[144:145], 4.0 op_sel_hi:[1,0]
	v_add_f32_e32 v68, 1.0, v68
	v_pk_mul_f32 v[144:145], v[144:145], v[152:153]
	v_rcp_f32_e32 v152, v68
	v_add_f32_e32 v68, 1.0, v166
	v_rcp_f32_e32 v153, v68
	v_pk_fma_f32 v[128:129], v[56:57], v[128:129], v[8:9]
	v_cvt_pk_f32_fp8_e32 v[132:133], v109
	v_pk_fma_f32 v[128:129], v[40:41], v[120:121], v[128:129]
	v_pk_mul_f32 v[140:141], v[140:141], v[152:153]
	v_pk_fma_f32 v[128:129], v[24:25], v[112:113], v[128:129]
	v_pk_fma_f32 v[134:135], v[46:47], v[134:135], v[2:3]
	v_mul_f32_e32 v68, 0xbfb8aa3b, v128
	v_exp_f32_e32 v68, v68
	v_mul_f32_e32 v152, 0xbfb8aa3b, v129
	v_exp_f32_e32 v152, v152
	v_pk_fma_f32 v[134:135], v[30:31], v[138:139], v[134:135]
	v_add_f32_e32 v68, 1.0, v68
	v_pk_fma_f32 v[134:135], v[18:19], v[132:133], v[134:135]
	v_cvt_pk_f32_fp8_sdwa v[108:109], v109 src0_sel:WORD_1
	v_pk_mul_f32 v[134:135], v[134:135], 4.0 op_sel_hi:[1,0]
	v_pk_fma_f32 v[124:125], v[48:49], v[124:125], v[4:5]
	v_pk_mul_f32 v[134:135], v[134:135], v[140:141]
	v_rcp_f32_e32 v140, v68
	v_add_f32_e32 v68, 1.0, v152
	v_rcp_f32_e32 v141, v68
	v_pk_fma_f32 v[124:125], v[32:33], v[116:117], v[124:125]
	v_med3_f32 v68, v156, s41, v1
	v_pk_fma_f32 v[124:125], v[20:21], v[108:109], v[124:125]
	v_pk_mul_f32 v[128:129], v[128:129], v[140:141]
	v_pk_mul_f32 v[124:125], v[124:125], 4.0 op_sel_hi:[1,0]
	v_med3_f32 v134, v134, s41, v1
	v_pk_mul_f32 v[124:125], v[124:125], v[128:129]
	v_med3_f32 v129, v157, s41, v1
	v_mov_b32_e32 v128, v69
	v_cvt_pk_fp8_f32 v128, v68, v129
	v_med3_f32 v135, v135, s41, v1
	v_mov_b32_e32 v129, v69
	s_waitcnt vmcnt(34)
	v_cvt_pk_f32_fp8_e32 v[156:157], v104
	v_cvt_pk_fp8_f32 v129, v134, v135
	v_pk_fma_f32 v[134:135], v[62:63], v[162:163], v[14:15]
	v_med3_f32 v68, v144, s41, v1
	v_med3_f32 v140, v145, s41, v1
	v_pk_fma_f32 v[134:135], v[50:51], v[164:165], v[134:135]
	v_cvt_pk_fp8_f32 v128, v68, v140 op_sel:[0,0,1]
	v_med3_f32 v68, v124, s41, v1
	v_med3_f32 v124, v125, s41, v1
	v_pk_fma_f32 v[134:135], v[34:35], v[156:157], v[134:135]
	v_cvt_pk_fp8_f32 v129, v68, v124 op_sel:[0,0,1]
	v_mul_f32_e32 v68, 0xbfb8aa3b, v134
	s_waitcnt vmcnt(33)
	v_cvt_pk_f32_fp8_e32 v[152:153], v100
	v_cvt_pk_f32_fp8_sdwa v[140:141], v100 src0_sel:WORD_1
	v_exp_f32_e32 v68, v68
	v_mul_f32_e32 v100, 0xbfb8aa3b, v135
	v_exp_f32_e32 v163, v100
	v_cvt_pk_f32_fp8_sdwa v[144:145], v104 src0_sel:WORD_1
	v_add_f32_e32 v68, 1.0, v68
	v_rcp_f32_e32 v162, v68
	v_add_f32_e32 v68, 1.0, v163
	v_rcp_f32_e32 v163, v68
	v_pk_fma_f32 v[150:151], v[64:65], v[150:151], v[16:17]
	v_pk_fma_f32 v[158:159], v[58:59], v[158:159], v[10:11]
	v_pk_fma_f32 v[150:151], v[52:53], v[154:155], v[150:151]
	v_pk_mul_f32 v[134:135], v[134:135], v[162:163]
	v_pk_fma_f32 v[150:151], v[36:37], v[144:145], v[150:151]
	v_add_co_u32_e32 v124, vcc, s69, v70
	v_mul_f32_e32 v68, 0xbfb8aa3b, v150
	v_exp_f32_e32 v68, v68
	v_mul_f32_e32 v162, 0xbfb8aa3b, v151
	v_exp_f32_e32 v162, v162
	v_pk_fma_f32 v[158:159], v[42:43], v[160:161], v[158:159]
	v_addc_co_u32_e32 v125, vcc, 0, v71, vcc
	v_pk_fma_f32 v[158:159], v[26:27], v[152:153], v[158:159]
	global_store_dwordx2 v[124:125], v[128:129], off offset:256
	v_cvt_pk_f32_fp8_e32 v[128:129], v105
	v_pk_mul_f32 v[158:159], v[158:159], 4.0 op_sel_hi:[1,0]
	v_add_f32_e32 v68, 1.0, v68
	v_pk_mul_f32 v[134:135], v[158:159], v[134:135]
	v_rcp_f32_e32 v158, v68
	v_add_f32_e32 v68, 1.0, v162
	v_rcp_f32_e32 v159, v68
	v_pk_fma_f32 v[142:143], v[54:55], v[142:143], v[6:7]
	v_pk_fma_f32 v[146:147], v[60:61], v[146:147], v[12:13]
	v_pk_fma_f32 v[142:143], v[38:39], v[136:137], v[142:143]
	v_pk_mul_f32 v[150:151], v[150:151], v[158:159]
	v_pk_fma_f32 v[142:143], v[22:23], v[128:129], v[142:143]
	v_pk_fma_f32 v[146:147], v[44:45], v[148:149], v[146:147]
	v_mul_f32_e32 v68, 0xbfb8aa3b, v142
	v_exp_f32_e32 v68, v68
	v_mul_f32_e32 v158, 0xbfb8aa3b, v143
	v_exp_f32_e32 v158, v158
	v_pk_fma_f32 v[146:147], v[28:29], v[140:141], v[146:147]
	v_cvt_pk_f32_fp8_sdwa v[104:105], v105 src0_sel:WORD_1
	v_pk_mul_f32 v[146:147], v[146:147], 4.0 op_sel_hi:[1,0]
	v_add_f32_e32 v68, 1.0, v68
	v_pk_mul_f32 v[146:147], v[146:147], v[150:151]
	v_rcp_f32_e32 v150, v68
	v_add_f32_e32 v68, 1.0, v158
	v_rcp_f32_e32 v151, v68
	v_pk_fma_f32 v[120:121], v[56:57], v[120:121], v[8:9]
	v_cvt_pk_f32_fp8_e32 v[124:125], v101
	v_pk_fma_f32 v[120:121], v[40:41], v[112:113], v[120:121]
	v_pk_mul_f32 v[142:143], v[142:143], v[150:151]
	v_pk_fma_f32 v[120:121], v[24:25], v[104:105], v[120:121]
	v_pk_fma_f32 v[138:139], v[46:47], v[138:139], v[2:3]
	v_mul_f32_e32 v68, 0xbfb8aa3b, v120
	v_exp_f32_e32 v68, v68
	v_mul_f32_e32 v150, 0xbfb8aa3b, v121
	v_exp_f32_e32 v150, v150
	v_pk_fma_f32 v[138:139], v[30:31], v[132:133], v[138:139]
	v_add_f32_e32 v68, 1.0, v68
	v_pk_fma_f32 v[138:139], v[18:19], v[124:125], v[138:139]
	v_cvt_pk_f32_fp8_sdwa v[100:101], v101 src0_sel:WORD_1
	v_pk_mul_f32 v[138:139], v[138:139], 4.0 op_sel_hi:[1,0]
	v_pk_fma_f32 v[116:117], v[48:49], v[116:117], v[4:5]
	v_pk_mul_f32 v[138:139], v[138:139], v[142:143]
	v_rcp_f32_e32 v142, v68
	v_add_f32_e32 v68, 1.0, v150
	v_rcp_f32_e32 v143, v68
	v_pk_fma_f32 v[116:117], v[32:33], v[108:109], v[116:117]
	v_med3_f32 v68, v134, s41, v1
	v_pk_fma_f32 v[116:117], v[20:21], v[100:101], v[116:117]
	v_pk_mul_f32 v[120:121], v[120:121], v[142:143]
	v_pk_mul_f32 v[116:117], v[116:117], 4.0 op_sel_hi:[1,0]
	v_med3_f32 v134, v147, s41, v1
	v_pk_mul_f32 v[116:117], v[116:117], v[120:121]
	v_med3_f32 v121, v135, s41, v1
	v_mov_b32_e32 v120, v69
	v_cvt_pk_fp8_f32 v120, v68, v121
	v_med3_f32 v135, v138, s41, v1
	v_med3_f32 v138, v139, s41, v1
	v_mov_b32_e32 v121, v69
	v_cvt_pk_fp8_f32 v121, v135, v138
	v_med3_f32 v68, v146, s41, v1
	v_cvt_pk_fp8_f32 v120, v68, v134 op_sel:[0,0,1]
	v_med3_f32 v68, v116, s41, v1
	v_med3_f32 v116, v117, s41, v1
	v_cvt_pk_fp8_f32 v121, v68, v116 op_sel:[0,0,1]
	v_add_co_u32_e32 v116, vcc, s35, v70
	s_waitcnt vmcnt(33)
	v_cvt_pk_f32_fp8_e32 v[158:159], v96
	v_addc_co_u32_e32 v117, vcc, 0, v71, vcc
	global_store_dwordx2 v[116:117], v[120:121], off offset:3072
	v_pk_fma_f32 v[116:117], v[62:63], v[164:165], v[14:15]
	s_waitcnt vmcnt(33)
	v_cvt_pk_f32_fp8_e32 v[150:151], v92
	v_pk_fma_f32 v[116:117], v[50:51], v[156:157], v[116:117]
	v_cvt_pk_f32_fp8_sdwa v[138:139], v92 src0_sel:WORD_1
	v_pk_fma_f32 v[146:147], v[34:35], v[158:159], v[116:117]
	v_cvt_pk_f32_fp8_sdwa v[142:143], v96 src0_sel:WORD_1
	v_mul_f32_e32 v68, 0xbfb8aa3b, v146
	v_exp_f32_e32 v68, v68
	v_mul_f32_e32 v92, 0xbfb8aa3b, v147
	v_exp_f32_e32 v162, v92
	v_cvt_pk_f32_fp8_e32 v[120:121], v93
	v_add_f32_e32 v68, 1.0, v68
	v_rcp_f32_e32 v92, v68
	v_add_f32_e32 v68, 1.0, v162
	v_cvt_pk_f32_fp8_sdwa v[116:117], v93 src0_sel:WORD_1
	v_rcp_f32_e32 v93, v68
	v_pk_fma_f32 v[154:155], v[64:65], v[154:155], v[16:17]
	v_pk_fma_f32 v[160:161], v[58:59], v[160:161], v[10:11]
	v_pk_fma_f32 v[154:155], v[52:53], v[144:145], v[154:155]
	v_pk_fma_f32 v[160:161], v[42:43], v[152:153], v[160:161]
	v_pk_fma_f32 v[154:155], v[36:37], v[142:143], v[154:155]
	v_pk_fma_f32 v[160:161], v[26:27], v[150:151], v[160:161]
	v_mul_f32_e32 v68, 0xbfb8aa3b, v154
	v_pk_mul_f32 v[92:93], v[146:147], v[92:93]
	v_pk_mul_f32 v[146:147], v[160:161], 4.0 op_sel_hi:[1,0]
	v_exp_f32_e32 v68, v68
	v_mul_f32_e32 v160, 0xbfb8aa3b, v155
	v_exp_f32_e32 v160, v160
	v_cvt_pk_f32_fp8_e32 v[134:135], v97
	v_add_f32_e32 v68, 1.0, v68
	v_pk_mul_f32 v[92:93], v[146:147], v[92:93]
	v_rcp_f32_e32 v146, v68
	v_add_f32_e32 v68, 1.0, v160
	v_rcp_f32_e32 v147, v68
	v_pk_fma_f32 v[136:137], v[54:55], v[136:137], v[6:7]
	v_pk_fma_f32 v[148:149], v[60:61], v[148:149], v[12:13]
	v_pk_fma_f32 v[136:137], v[38:39], v[128:129], v[136:137]
	v_pk_mul_f32 v[146:147], v[154:155], v[146:147]
	v_pk_fma_f32 v[136:137], v[22:23], v[134:135], v[136:137]
	v_pk_fma_f32 v[148:149], v[44:45], v[140:141], v[148:149]
	v_mul_f32_e32 v68, 0xbfb8aa3b, v136
	v_exp_f32_e32 v68, v68
	v_mul_f32_e32 v154, 0xbfb8aa3b, v137
	v_exp_f32_e32 v154, v154
	v_pk_fma_f32 v[148:149], v[28:29], v[138:139], v[148:149]
	v_cvt_pk_f32_fp8_sdwa v[96:97], v97 src0_sel:WORD_1
	v_pk_mul_f32 v[148:149], v[148:149], 4.0 op_sel_hi:[1,0]
	v_add_f32_e32 v68, 1.0, v68
	v_pk_mul_f32 v[146:147], v[148:149], v[146:147]
	v_rcp_f32_e32 v148, v68
	v_add_f32_e32 v68, 1.0, v154
	v_rcp_f32_e32 v149, v68
	v_pk_fma_f32 v[112:113], v[56:57], v[112:113], v[8:9]
	v_pk_fma_f32 v[132:133], v[46:47], v[132:133], v[2:3]
	v_pk_fma_f32 v[112:113], v[40:41], v[104:105], v[112:113]
	v_pk_mul_f32 v[136:137], v[136:137], v[148:149]
	v_pk_fma_f32 v[112:113], v[24:25], v[96:97], v[112:113]
	v_pk_fma_f32 v[132:133], v[30:31], v[124:125], v[132:133]
	v_mul_f32_e32 v68, 0xbfb8aa3b, v112
	v_exp_f32_e32 v68, v68
	v_mul_f32_e32 v148, 0xbfb8aa3b, v113
	v_exp_f32_e32 v148, v148
	v_pk_fma_f32 v[132:133], v[18:19], v[120:121], v[132:133]
	v_add_f32_e32 v68, 1.0, v68
	v_pk_mul_f32 v[132:133], v[132:133], 4.0 op_sel_hi:[1,0]
	v_pk_fma_f32 v[108:109], v[48:49], v[108:109], v[4:5]
	v_pk_mul_f32 v[132:133], v[132:133], v[136:137]
	v_rcp_f32_e32 v136, v68
	v_add_f32_e32 v68, 1.0, v148
	v_rcp_f32_e32 v137, v68
	v_pk_fma_f32 v[108:109], v[32:33], v[100:101], v[108:109]
	v_med3_f32 v68, v92, s41, v1
	v_pk_fma_f32 v[108:109], v[20:21], v[116:117], v[108:109]
	v_pk_mul_f32 v[112:113], v[112:113], v[136:137]
	v_pk_mul_f32 v[108:109], v[108:109], 4.0 op_sel_hi:[1,0]
	v_med3_f32 v93, v93, s41, v1
	v_mov_b32_e32 v92, v69
	v_pk_mul_f32 v[108:109], v[108:109], v[112:113]
	v_cvt_pk_fp8_f32 v92, v68, v93
	v_med3_f32 v113, v132, s41, v1
	v_med3_f32 v132, v133, s41, v1
	v_mov_b32_e32 v93, v69
	v_cvt_pk_fp8_f32 v93, v113, v132
	v_med3_f32 v68, v146, s41, v1
	v_med3_f32 v112, v147, s41, v1
	v_cvt_pk_fp8_f32 v92, v68, v112 op_sel:[0,0,1]
	v_med3_f32 v68, v108, s41, v1
	v_med3_f32 v108, v109, s41, v1
	v_cvt_pk_fp8_f32 v93, v68, v108 op_sel:[0,0,1]
	v_add_co_u32_e32 v108, vcc, s70, v70
	s_waitcnt vmcnt(32)
	v_cvt_pk_f32_fp8_e32 v[148:149], v88
	v_addc_co_u32_e32 v109, vcc, 0, v71, vcc
	global_store_dwordx2 v[108:109], v[92:93], off offset:1792
	v_pk_fma_f32 v[92:93], v[62:63], v[156:157], v[14:15]
	s_waitcnt vmcnt(32)
	v_cvt_pk_f32_fp8_e32 v[146:147], v84
	v_pk_fma_f32 v[92:93], v[50:51], v[158:159], v[92:93]
	v_cvt_pk_f32_fp8_sdwa v[132:133], v84 src0_sel:WORD_1
	v_pk_fma_f32 v[92:93], v[34:35], v[148:149], v[92:93]
	v_cvt_pk_f32_fp8_sdwa v[136:137], v88 src0_sel:WORD_1
	v_mul_f32_e32 v68, 0xbfb8aa3b, v92
	v_exp_f32_e32 v68, v68
	v_mul_f32_e32 v84, 0xbfb8aa3b, v93
	v_exp_f32_e32 v155, v84
	v_pk_fma_f32 v[144:145], v[64:65], v[144:145], v[16:17]
	v_add_f32_e32 v68, 1.0, v68
	v_rcp_f32_e32 v154, v68
	v_add_f32_e32 v68, 1.0, v155
	v_rcp_f32_e32 v155, v68
	v_pk_fma_f32 v[144:145], v[52:53], v[142:143], v[144:145]
	v_pk_fma_f32 v[152:153], v[58:59], v[152:153], v[10:11]
	v_pk_fma_f32 v[144:145], v[36:37], v[136:137], v[144:145]
	v_pk_mul_f32 v[92:93], v[92:93], v[154:155]
	v_mul_f32_e32 v68, 0xbfb8aa3b, v144
	v_exp_f32_e32 v68, v68
	v_mul_f32_e32 v154, 0xbfb8aa3b, v145
	v_exp_f32_e32 v154, v154
	v_pk_fma_f32 v[152:153], v[42:43], v[150:151], v[152:153]
	v_cvt_pk_f32_fp8_e32 v[112:113], v89
	v_pk_fma_f32 v[152:153], v[26:27], v[146:147], v[152:153]
	v_add_f32_e32 v68, 1.0, v68
	v_pk_mul_f32 v[152:153], v[152:153], 4.0 op_sel_hi:[1,0]
	v_pk_fma_f32 v[128:129], v[54:55], v[128:129], v[6:7]
	v_pk_mul_f32 v[92:93], v[152:153], v[92:93]
	v_rcp_f32_e32 v152, v68
	v_add_f32_e32 v68, 1.0, v154
	v_rcp_f32_e32 v153, v68
	v_pk_fma_f32 v[128:129], v[38:39], v[134:135], v[128:129]
	v_pk_fma_f32 v[140:141], v[60:61], v[140:141], v[12:13]
	v_pk_fma_f32 v[128:129], v[22:23], v[112:113], v[128:129]
	v_pk_mul_f32 v[144:145], v[144:145], v[152:153]
	v_mul_f32_e32 v68, 0xbfb8aa3b, v128
	v_exp_f32_e32 v68, v68
	v_mul_f32_e32 v152, 0xbfb8aa3b, v129
	v_exp_f32_e32 v152, v152
	v_pk_fma_f32 v[140:141], v[44:45], v[138:139], v[140:141]
	v_cvt_pk_f32_fp8_sdwa v[88:89], v89 src0_sel:WORD_1
	v_pk_fma_f32 v[140:141], v[28:29], v[132:133], v[140:141]
	v_add_f32_e32 v68, 1.0, v68
	v_pk_mul_f32 v[140:141], v[140:141], 4.0 op_sel_hi:[1,0]
	v_pk_fma_f32 v[104:105], v[56:57], v[104:105], v[8:9]
	v_pk_mul_f32 v[140:141], v[140:141], v[144:145]
	v_rcp_f32_e32 v144, v68
	v_add_f32_e32 v68, 1.0, v152
	v_rcp_f32_e32 v145, v68
	v_pk_fma_f32 v[104:105], v[40:41], v[96:97], v[104:105]
	v_cvt_pk_f32_fp8_e32 v[108:109], v85
	v_pk_fma_f32 v[104:105], v[24:25], v[88:89], v[104:105]
	v_pk_mul_f32 v[128:129], v[128:129], v[144:145]
	v_mul_f32_e32 v68, 0xbfb8aa3b, v104
	v_exp_f32_e32 v68, v68
	v_mul_f32_e32 v144, 0xbfb8aa3b, v105
	v_pk_fma_f32 v[124:125], v[46:47], v[124:125], v[2:3]
	v_exp_f32_e32 v144, v144
	v_pk_fma_f32 v[124:125], v[30:31], v[120:121], v[124:125]
	v_add_f32_e32 v68, 1.0, v68
	v_pk_fma_f32 v[124:125], v[18:19], v[108:109], v[124:125]
	v_cvt_pk_f32_fp8_sdwa v[84:85], v85 src0_sel:WORD_1
	v_pk_mul_f32 v[124:125], v[124:125], 4.0 op_sel_hi:[1,0]
	v_pk_fma_f32 v[100:101], v[48:49], v[100:101], v[4:5]
	v_pk_mul_f32 v[124:125], v[124:125], v[128:129]
	v_rcp_f32_e32 v128, v68
	v_add_f32_e32 v68, 1.0, v144
	v_rcp_f32_e32 v129, v68
	v_pk_fma_f32 v[100:101], v[32:33], v[116:117], v[100:101]
	v_med3_f32 v68, v92, s41, v1
	v_pk_fma_f32 v[100:101], v[20:21], v[84:85], v[100:101]
	v_pk_mul_f32 v[104:105], v[104:105], v[128:129]
	v_pk_mul_f32 v[100:101], v[100:101], 4.0 op_sel_hi:[1,0]
	v_med3_f32 v93, v93, s41, v1
	v_mov_b32_e32 v92, v69
	v_pk_mul_f32 v[100:101], v[100:101], v[104:105]
	v_cvt_pk_fp8_f32 v92, v68, v93
	v_med3_f32 v105, v124, s41, v1
	v_med3_f32 v124, v125, s41, v1
	v_mov_b32_e32 v93, v69
	v_cvt_pk_fp8_f32 v93, v105, v124
	v_med3_f32 v68, v140, s41, v1
	v_med3_f32 v104, v141, s41, v1
	v_cvt_pk_fp8_f32 v92, v68, v104 op_sel:[0,0,1]
	v_med3_f32 v68, v100, s41, v1
	v_med3_f32 v100, v101, s41, v1
	v_cvt_pk_fp8_f32 v93, v68, v100 op_sel:[0,0,1]
	v_add_co_u32_e32 v100, vcc, s36, v70
	s_waitcnt vmcnt(31)
	v_cvt_pk_f32_fp8_e32 v[152:153], v80
	v_addc_co_u32_e32 v101, vcc, 0, v71, vcc
	global_store_dwordx2 v[100:101], v[92:93], off offset:512
	v_pk_fma_f32 v[92:93], v[62:63], v[158:159], v[14:15]
	s_waitcnt vmcnt(31)
	v_cvt_pk_f32_fp8_e32 v[144:145], v76
	v_pk_fma_f32 v[92:93], v[50:51], v[148:149], v[92:93]
	v_cvt_pk_f32_fp8_sdwa v[128:129], v76 src0_sel:WORD_1
	v_pk_fma_f32 v[104:105], v[34:35], v[152:153], v[92:93]
	v_cvt_pk_f32_fp8_sdwa v[140:141], v80 src0_sel:WORD_1
	v_mul_f32_e32 v68, 0xbfb8aa3b, v104
	v_exp_f32_e32 v68, v68
	v_mul_f32_e32 v76, 0xbfb8aa3b, v105
	v_exp_f32_e32 v154, v76
	v_cvt_pk_f32_fp8_e32 v[100:101], v77
	v_add_f32_e32 v68, 1.0, v68
	v_rcp_f32_e32 v76, v68
	v_add_f32_e32 v68, 1.0, v154
	v_cvt_pk_f32_fp8_sdwa v[92:93], v77 src0_sel:WORD_1
	v_rcp_f32_e32 v77, v68
	v_pk_fma_f32 v[142:143], v[64:65], v[142:143], v[16:17]
	v_pk_fma_f32 v[150:151], v[58:59], v[150:151], v[10:11]
	v_pk_fma_f32 v[142:143], v[52:53], v[136:137], v[142:143]
	v_pk_fma_f32 v[150:151], v[42:43], v[146:147], v[150:151]
	v_pk_fma_f32 v[142:143], v[36:37], v[140:141], v[142:143]
	v_pk_fma_f32 v[150:151], v[26:27], v[144:145], v[150:151]
	v_mul_f32_e32 v68, 0xbfb8aa3b, v142
	v_pk_mul_f32 v[76:77], v[104:105], v[76:77]
	v_pk_mul_f32 v[104:105], v[150:151], 4.0 op_sel_hi:[1,0]
	v_exp_f32_e32 v68, v68
	v_mul_f32_e32 v150, 0xbfb8aa3b, v143
	v_exp_f32_e32 v150, v150
	v_cvt_pk_f32_fp8_e32 v[124:125], v81
	v_add_f32_e32 v68, 1.0, v68
	v_pk_mul_f32 v[76:77], v[104:105], v[76:77]
	v_rcp_f32_e32 v104, v68
	v_add_f32_e32 v68, 1.0, v150
	v_rcp_f32_e32 v105, v68
	v_pk_fma_f32 v[134:135], v[54:55], v[134:135], v[6:7]
	v_pk_fma_f32 v[138:139], v[60:61], v[138:139], v[12:13]
	v_pk_fma_f32 v[134:135], v[38:39], v[112:113], v[134:135]
	v_pk_mul_f32 v[104:105], v[142:143], v[104:105]
	v_pk_fma_f32 v[134:135], v[22:23], v[124:125], v[134:135]
	v_pk_fma_f32 v[138:139], v[44:45], v[132:133], v[138:139]
	v_mul_f32_e32 v68, 0xbfb8aa3b, v134
	v_exp_f32_e32 v68, v68
	v_mul_f32_e32 v142, 0xbfb8aa3b, v135
	v_exp_f32_e32 v142, v142
	v_pk_fma_f32 v[138:139], v[28:29], v[128:129], v[138:139]
	v_cvt_pk_f32_fp8_sdwa v[80:81], v81 src0_sel:WORD_1
	v_pk_mul_f32 v[138:139], v[138:139], 4.0 op_sel_hi:[1,0]
	v_add_f32_e32 v68, 1.0, v68
	v_pk_mul_f32 v[104:105], v[138:139], v[104:105]
	v_rcp_f32_e32 v138, v68
	v_add_f32_e32 v68, 1.0, v142
	v_rcp_f32_e32 v139, v68
	v_pk_fma_f32 v[96:97], v[56:57], v[96:97], v[8:9]
	v_pk_fma_f32 v[120:121], v[46:47], v[120:121], v[2:3]
	v_pk_fma_f32 v[96:97], v[40:41], v[88:89], v[96:97]
	v_pk_mul_f32 v[134:135], v[134:135], v[138:139]
	v_pk_fma_f32 v[96:97], v[24:25], v[80:81], v[96:97]
	v_pk_fma_f32 v[120:121], v[30:31], v[108:109], v[120:121]
	v_mul_f32_e32 v68, 0xbfb8aa3b, v96
	v_exp_f32_e32 v68, v68
	v_mul_f32_e32 v138, 0xbfb8aa3b, v97
	v_exp_f32_e32 v138, v138
	v_pk_fma_f32 v[120:121], v[18:19], v[100:101], v[120:121]
	v_add_f32_e32 v68, 1.0, v68
	v_pk_mul_f32 v[120:121], v[120:121], 4.0 op_sel_hi:[1,0]
	v_pk_fma_f32 v[116:117], v[48:49], v[116:117], v[4:5]
	v_pk_mul_f32 v[120:121], v[120:121], v[134:135]
	v_rcp_f32_e32 v134, v68
	v_add_f32_e32 v68, 1.0, v138
	v_rcp_f32_e32 v135, v68
	v_pk_fma_f32 v[116:117], v[32:33], v[84:85], v[116:117]
	v_med3_f32 v68, v76, s41, v1
	v_pk_fma_f32 v[116:117], v[20:21], v[92:93], v[116:117]
	v_pk_mul_f32 v[96:97], v[96:97], v[134:135]
	v_pk_mul_f32 v[116:117], v[116:117], 4.0 op_sel_hi:[1,0]
	v_med3_f32 v77, v77, s41, v1
	v_mov_b32_e32 v76, v69
	v_pk_mul_f32 v[96:97], v[116:117], v[96:97]
	v_cvt_pk_fp8_f32 v76, v68, v77
	v_med3_f32 v68, v104, s41, v1
	v_med3_f32 v104, v105, s41, v1
	v_med3_f32 v105, v120, s41, v1
	v_med3_f32 v116, v121, s41, v1
	v_mov_b32_e32 v77, v69
	v_cvt_pk_fp8_f32 v77, v105, v116
	v_cvt_pk_fp8_f32 v76, v68, v104 op_sel:[0,0,1]
	v_med3_f32 v68, v96, s41, v1
	v_med3_f32 v96, v97, s41, v1
	v_cvt_pk_fp8_f32 v77, v68, v96 op_sel:[0,0,1]
	v_add_co_u32_e32 v96, vcc, s71, v70
	s_waitcnt vmcnt(22)
	v_cvt_pk_f32_fp8_e32 v[138:139], v130
	v_addc_co_u32_e32 v97, vcc, 0, v71, vcc
	global_store_dwordx2 v[96:97], v[76:77], off offset:3328
	v_pk_fma_f32 v[96:97], v[62:63], v[148:149], v[14:15]
	v_cvt_pk_f32_fp8_sdwa v[134:135], v130 src0_sel:WORD_1
	v_pk_fma_f32 v[96:97], v[50:51], v[152:153], v[96:97]
	v_cvt_pk_f32_fp8_e32 v[116:117], v131
	v_pk_fma_f32 v[142:143], v[34:35], v[138:139], v[96:97]
	v_cvt_pk_f32_fp8_sdwa v[76:77], v131 src0_sel:WORD_1
	v_mul_f32_e32 v68, 0xbfb8aa3b, v142
	v_exp_f32_e32 v68, v68
	v_mul_f32_e32 v96, 0xbfb8aa3b, v143
	v_exp_f32_e32 v148, v96
	s_waitcnt vmcnt(22)
	v_cvt_pk_f32_fp8_e32 v[130:131], v126
	v_add_f32_e32 v68, 1.0, v68
	v_cvt_pk_f32_fp8_sdwa v[120:121], v126 src0_sel:WORD_1
	v_rcp_f32_e32 v126, v68
	v_add_f32_e32 v68, 1.0, v148
	v_cvt_pk_f32_fp8_e32 v[104:105], v127
	v_cvt_pk_f32_fp8_sdwa v[96:97], v127 src0_sel:WORD_1
	v_rcp_f32_e32 v127, v68
	v_pk_fma_f32 v[136:137], v[64:65], v[136:137], v[16:17]
	v_pk_fma_f32 v[146:147], v[58:59], v[146:147], v[10:11]
	v_pk_fma_f32 v[136:137], v[52:53], v[140:141], v[136:137]
	v_pk_fma_f32 v[146:147], v[42:43], v[144:145], v[146:147]
	v_pk_fma_f32 v[136:137], v[36:37], v[134:135], v[136:137]
	v_pk_fma_f32 v[146:147], v[26:27], v[130:131], v[146:147]
	v_mul_f32_e32 v68, 0xbfb8aa3b, v136
	v_pk_mul_f32 v[126:127], v[142:143], v[126:127]
	v_pk_mul_f32 v[142:143], v[146:147], 4.0 op_sel_hi:[1,0]
	v_exp_f32_e32 v68, v68
	v_mul_f32_e32 v146, 0xbfb8aa3b, v137
	v_exp_f32_e32 v146, v146
	v_pk_mul_f32 v[126:127], v[142:143], v[126:127]
	v_add_f32_e32 v68, 1.0, v68
	v_rcp_f32_e32 v142, v68
	v_add_f32_e32 v68, 1.0, v146
	v_rcp_f32_e32 v143, v68
	v_pk_fma_f32 v[112:113], v[54:55], v[112:113], v[6:7]
	v_pk_fma_f32 v[132:133], v[60:61], v[132:133], v[12:13]
	v_pk_fma_f32 v[112:113], v[38:39], v[124:125], v[112:113]
	v_pk_mul_f32 v[136:137], v[136:137], v[142:143]
	v_pk_fma_f32 v[112:113], v[22:23], v[116:117], v[112:113]
	v_pk_fma_f32 v[132:133], v[44:45], v[128:129], v[132:133]
	v_mul_f32_e32 v68, 0xbfb8aa3b, v112
	v_exp_f32_e32 v68, v68
	v_mul_f32_e32 v142, 0xbfb8aa3b, v113
	v_exp_f32_e32 v142, v142
	v_pk_fma_f32 v[132:133], v[28:29], v[120:121], v[132:133]
	v_add_f32_e32 v68, 1.0, v68
	v_pk_mul_f32 v[132:133], v[132:133], 4.0 op_sel_hi:[1,0]
	v_pk_fma_f32 v[88:89], v[56:57], v[88:89], v[8:9]
	v_pk_mul_f32 v[132:133], v[132:133], v[136:137]
	v_rcp_f32_e32 v136, v68
	v_add_f32_e32 v68, 1.0, v142
	v_rcp_f32_e32 v137, v68
	v_pk_fma_f32 v[88:89], v[40:41], v[80:81], v[88:89]
	v_pk_fma_f32 v[108:109], v[46:47], v[108:109], v[2:3]
	v_pk_fma_f32 v[88:89], v[24:25], v[76:77], v[88:89]
	v_pk_mul_f32 v[112:113], v[112:113], v[136:137]
	v_mul_f32_e32 v68, 0xbfb8aa3b, v88
	v_exp_f32_e32 v68, v68
	v_mul_f32_e32 v136, 0xbfb8aa3b, v89
	v_exp_f32_e32 v136, v136
	v_pk_fma_f32 v[108:109], v[30:31], v[100:101], v[108:109]
	v_add_f32_e32 v68, 1.0, v68
	v_pk_fma_f32 v[108:109], v[18:19], v[104:105], v[108:109]
	v_pk_fma_f32 v[84:85], v[48:49], v[84:85], v[4:5]
	v_pk_mul_f32 v[108:109], v[108:109], 4.0 op_sel_hi:[1,0]
	v_pk_fma_f32 v[84:85], v[32:33], v[92:93], v[84:85]
	v_pk_mul_f32 v[108:109], v[108:109], v[112:113]
	v_rcp_f32_e32 v112, v68
	v_add_f32_e32 v68, 1.0, v136
	v_rcp_f32_e32 v113, v68
	v_pk_fma_f32 v[84:85], v[20:21], v[96:97], v[84:85]
	v_med3_f32 v68, v126, s41, v1
	v_pk_mul_f32 v[84:85], v[84:85], 4.0 op_sel_hi:[1,0]
	v_pk_mul_f32 v[88:89], v[88:89], v[112:113]
	v_med3_f32 v108, v108, s41, v1
	v_pk_mul_f32 v[84:85], v[84:85], v[88:89]
	v_med3_f32 v89, v127, s41, v1
	v_mov_b32_e32 v88, v69
	v_cvt_pk_fp8_f32 v88, v68, v89
	v_med3_f32 v109, v109, s41, v1
	v_mov_b32_e32 v89, v69
	v_cvt_pk_fp8_f32 v89, v108, v109
	v_med3_f32 v68, v132, s41, v1
	v_med3_f32 v112, v133, s41, v1
	v_cvt_pk_fp8_f32 v88, v68, v112 op_sel:[0,0,1]
	v_med3_f32 v68, v84, s41, v1
	v_med3_f32 v84, v85, s41, v1
	v_cvt_pk_fp8_f32 v89, v68, v84 op_sel:[0,0,1]
	v_add_co_u32_e32 v84, vcc, s37, v70
	s_waitcnt vmcnt(21)
	v_cvt_pk_f32_fp8_e32 v[136:137], v122
	v_addc_co_u32_e32 v85, vcc, 0, v71, vcc
	global_store_dwordx2 v[84:85], v[88:89], off offset:2048
	v_pk_fma_f32 v[88:89], v[62:63], v[152:153], v[14:15]
	v_cvt_pk_f32_fp8_sdwa v[126:127], v122 src0_sel:WORD_1
	v_pk_fma_f32 v[88:89], v[50:51], v[138:139], v[88:89]
	v_cvt_pk_f32_fp8_e32 v[112:113], v123
	v_pk_fma_f32 v[142:143], v[34:35], v[136:137], v[88:89]
	v_cvt_pk_f32_fp8_sdwa v[84:85], v123 src0_sel:WORD_1
	v_mul_f32_e32 v68, 0xbfb8aa3b, v142
	v_exp_f32_e32 v68, v68
	v_mul_f32_e32 v88, 0xbfb8aa3b, v143
	v_exp_f32_e32 v146, v88
	s_waitcnt vmcnt(21)
	v_cvt_pk_f32_fp8_e32 v[132:133], v118
	v_add_f32_e32 v68, 1.0, v68
	v_cvt_pk_f32_fp8_sdwa v[122:123], v118 src0_sel:WORD_1
	v_rcp_f32_e32 v118, v68
	v_add_f32_e32 v68, 1.0, v146
	v_cvt_pk_f32_fp8_e32 v[108:109], v119
	v_cvt_pk_f32_fp8_sdwa v[88:89], v119 src0_sel:WORD_1
	v_rcp_f32_e32 v119, v68
	v_pk_fma_f32 v[140:141], v[64:65], v[140:141], v[16:17]
	v_pk_fma_f32 v[144:145], v[58:59], v[144:145], v[10:11]
	v_pk_fma_f32 v[140:141], v[52:53], v[134:135], v[140:141]
	v_pk_fma_f32 v[144:145], v[42:43], v[130:131], v[144:145]
	v_pk_fma_f32 v[140:141], v[36:37], v[126:127], v[140:141]
	v_pk_fma_f32 v[144:145], v[26:27], v[132:133], v[144:145]
	v_mul_f32_e32 v68, 0xbfb8aa3b, v140
	v_pk_mul_f32 v[118:119], v[142:143], v[118:119]
	v_pk_mul_f32 v[142:143], v[144:145], 4.0 op_sel_hi:[1,0]
	v_exp_f32_e32 v68, v68
	v_mul_f32_e32 v144, 0xbfb8aa3b, v141
	v_exp_f32_e32 v144, v144
	v_pk_mul_f32 v[118:119], v[142:143], v[118:119]
	v_add_f32_e32 v68, 1.0, v68
	v_rcp_f32_e32 v142, v68
	v_add_f32_e32 v68, 1.0, v144
	v_rcp_f32_e32 v143, v68
	v_pk_fma_f32 v[124:125], v[54:55], v[124:125], v[6:7]
	v_pk_fma_f32 v[128:129], v[60:61], v[128:129], v[12:13]
	v_pk_fma_f32 v[124:125], v[38:39], v[116:117], v[124:125]
	v_pk_mul_f32 v[140:141], v[140:141], v[142:143]
	v_pk_fma_f32 v[124:125], v[22:23], v[112:113], v[124:125]
	v_pk_fma_f32 v[128:129], v[44:45], v[120:121], v[128:129]
	v_mul_f32_e32 v68, 0xbfb8aa3b, v124
	v_exp_f32_e32 v68, v68
	v_mul_f32_e32 v142, 0xbfb8aa3b, v125
	v_exp_f32_e32 v142, v142
	v_pk_fma_f32 v[128:129], v[28:29], v[122:123], v[128:129]
	v_add_f32_e32 v68, 1.0, v68
	v_pk_mul_f32 v[128:129], v[128:129], 4.0 op_sel_hi:[1,0]
	v_pk_fma_f32 v[80:81], v[56:57], v[80:81], v[8:9]
	v_pk_mul_f32 v[128:129], v[128:129], v[140:141]
	v_rcp_f32_e32 v140, v68
	v_add_f32_e32 v68, 1.0, v142
	v_rcp_f32_e32 v141, v68
	v_pk_fma_f32 v[80:81], v[40:41], v[76:77], v[80:81]
	v_pk_fma_f32 v[100:101], v[46:47], v[100:101], v[2:3]
	v_pk_fma_f32 v[80:81], v[24:25], v[84:85], v[80:81]
	v_pk_mul_f32 v[124:125], v[124:125], v[140:141]
	v_mul_f32_e32 v68, 0xbfb8aa3b, v80
	v_exp_f32_e32 v68, v68
	v_mul_f32_e32 v140, 0xbfb8aa3b, v81
	v_exp_f32_e32 v140, v140
	v_pk_fma_f32 v[100:101], v[30:31], v[104:105], v[100:101]
	v_add_f32_e32 v68, 1.0, v68
	v_pk_fma_f32 v[100:101], v[18:19], v[108:109], v[100:101]
	v_pk_fma_f32 v[92:93], v[48:49], v[92:93], v[4:5]
	v_pk_mul_f32 v[100:101], v[100:101], 4.0 op_sel_hi:[1,0]
	v_pk_fma_f32 v[92:93], v[32:33], v[96:97], v[92:93]
	v_pk_mul_f32 v[100:101], v[100:101], v[124:125]
	v_rcp_f32_e32 v124, v68
	v_add_f32_e32 v68, 1.0, v140
	v_rcp_f32_e32 v125, v68
	v_pk_fma_f32 v[92:93], v[20:21], v[88:89], v[92:93]
	v_med3_f32 v68, v118, s41, v1
	v_pk_mul_f32 v[92:93], v[92:93], 4.0 op_sel_hi:[1,0]
	v_pk_mul_f32 v[80:81], v[80:81], v[124:125]
	v_med3_f32 v100, v100, s41, v1
	v_pk_mul_f32 v[80:81], v[92:93], v[80:81]
	v_med3_f32 v93, v119, s41, v1
	v_mov_b32_e32 v92, v69
	v_cvt_pk_fp8_f32 v92, v68, v93
	v_med3_f32 v101, v101, s41, v1
	v_mov_b32_e32 v93, v69
	v_cvt_pk_fp8_f32 v93, v100, v101
	v_med3_f32 v68, v128, s41, v1
	v_med3_f32 v118, v129, s41, v1
	v_cvt_pk_fp8_f32 v92, v68, v118 op_sel:[0,0,1]
	v_med3_f32 v68, v80, s41, v1
	v_med3_f32 v80, v81, s41, v1
	v_cvt_pk_fp8_f32 v93, v68, v80 op_sel:[0,0,1]
	v_add_co_u32_e32 v80, vcc, s72, v70
	s_waitcnt vmcnt(20)
	v_cvt_pk_f32_fp8_e32 v[140:141], v114
	v_addc_co_u32_e32 v81, vcc, 0, v71, vcc
	global_store_dwordx2 v[80:81], v[92:93], off offset:768
	v_pk_fma_f32 v[92:93], v[62:63], v[138:139], v[14:15]
	v_cvt_pk_f32_fp8_sdwa v[124:125], v114 src0_sel:WORD_1
	v_pk_fma_f32 v[92:93], v[50:51], v[136:137], v[92:93]
	v_cvt_pk_f32_fp8_e32 v[118:119], v115
	v_pk_fma_f32 v[138:139], v[34:35], v[140:141], v[92:93]
	v_cvt_pk_f32_fp8_sdwa v[80:81], v115 src0_sel:WORD_1
	v_mul_f32_e32 v68, 0xbfb8aa3b, v138
	v_exp_f32_e32 v68, v68
	v_mul_f32_e32 v92, 0xbfb8aa3b, v139
	v_exp_f32_e32 v142, v92
	s_waitcnt vmcnt(20)
	v_cvt_pk_f32_fp8_e32 v[128:129], v110
	v_add_f32_e32 v68, 1.0, v68
	v_cvt_pk_f32_fp8_sdwa v[114:115], v110 src0_sel:WORD_1
	v_rcp_f32_e32 v110, v68
	v_add_f32_e32 v68, 1.0, v142
	v_cvt_pk_f32_fp8_e32 v[100:101], v111
	v_cvt_pk_f32_fp8_sdwa v[92:93], v111 src0_sel:WORD_1
	v_rcp_f32_e32 v111, v68
	v_pk_fma_f32 v[134:135], v[64:65], v[134:135], v[16:17]
	v_pk_fma_f32 v[130:131], v[58:59], v[130:131], v[10:11]
	v_pk_fma_f32 v[134:135], v[52:53], v[126:127], v[134:135]
	v_pk_mul_f32 v[110:111], v[138:139], v[110:111]
	v_pk_fma_f32 v[134:135], v[36:37], v[124:125], v[134:135]
	v_pk_fma_f32 v[130:131], v[42:43], v[132:133], v[130:131]
	v_mul_f32_e32 v68, 0xbfb8aa3b, v134
	v_exp_f32_e32 v68, v68
	v_mul_f32_e32 v138, 0xbfb8aa3b, v135
	v_exp_f32_e32 v138, v138
	v_pk_fma_f32 v[130:131], v[26:27], v[128:129], v[130:131]
	v_add_f32_e32 v68, 1.0, v68
	v_pk_mul_f32 v[130:131], v[130:131], 4.0 op_sel_hi:[1,0]
	v_pk_fma_f32 v[116:117], v[54:55], v[116:117], v[6:7]
	v_pk_mul_f32 v[110:111], v[130:131], v[110:111]
	v_rcp_f32_e32 v130, v68
	v_add_f32_e32 v68, 1.0, v138
	v_rcp_f32_e32 v131, v68
	v_pk_fma_f32 v[116:117], v[38:39], v[112:113], v[116:117]
	v_pk_fma_f32 v[120:121], v[60:61], v[120:121], v[12:13]
	v_pk_fma_f32 v[116:117], v[22:23], v[118:119], v[116:117]
	v_pk_mul_f32 v[130:131], v[134:135], v[130:131]
	v_mul_f32_e32 v68, 0xbfb8aa3b, v116
	v_exp_f32_e32 v68, v68
	v_mul_f32_e32 v134, 0xbfb8aa3b, v117
	v_exp_f32_e32 v134, v134
	v_pk_fma_f32 v[120:121], v[44:45], v[122:123], v[120:121]
	v_add_f32_e32 v68, 1.0, v68
	v_pk_fma_f32 v[120:121], v[28:29], v[114:115], v[120:121]
	v_pk_fma_f32 v[76:77], v[56:57], v[76:77], v[8:9]
	v_pk_mul_f32 v[120:121], v[120:121], 4.0 op_sel_hi:[1,0]
	v_pk_fma_f32 v[76:77], v[40:41], v[84:85], v[76:77]
	v_pk_mul_f32 v[120:121], v[120:121], v[130:131]
	v_rcp_f32_e32 v130, v68
	v_add_f32_e32 v68, 1.0, v134
	v_rcp_f32_e32 v131, v68
	v_pk_fma_f32 v[76:77], v[24:25], v[80:81], v[76:77]
	v_pk_fma_f32 v[104:105], v[46:47], v[104:105], v[2:3]
	v_mul_f32_e32 v68, 0xbfb8aa3b, v76
	v_pk_mul_f32 v[116:117], v[116:117], v[130:131]
	v_exp_f32_e32 v68, v68
	v_mul_f32_e32 v130, 0xbfb8aa3b, v77
	v_exp_f32_e32 v130, v130
	v_pk_fma_f32 v[104:105], v[30:31], v[108:109], v[104:105]
	v_add_f32_e32 v68, 1.0, v68
	v_pk_fma_f32 v[104:105], v[18:19], v[100:101], v[104:105]
	v_pk_fma_f32 v[96:97], v[48:49], v[96:97], v[4:5]
	v_pk_mul_f32 v[104:105], v[104:105], 4.0 op_sel_hi:[1,0]
	v_pk_fma_f32 v[96:97], v[32:33], v[88:89], v[96:97]
	v_pk_mul_f32 v[104:105], v[104:105], v[116:117]
	v_rcp_f32_e32 v116, v68
	v_add_f32_e32 v68, 1.0, v130
	v_rcp_f32_e32 v117, v68
	v_pk_fma_f32 v[96:97], v[20:21], v[92:93], v[96:97]
	v_med3_f32 v68, v110, s41, v1
	v_pk_mul_f32 v[96:97], v[96:97], 4.0 op_sel_hi:[1,0]
	v_pk_mul_f32 v[76:77], v[76:77], v[116:117]
	v_med3_f32 v104, v104, s41, v1
	v_pk_mul_f32 v[76:77], v[96:97], v[76:77]
	v_med3_f32 v97, v111, s41, v1
	v_mov_b32_e32 v96, v69
	v_cvt_pk_fp8_f32 v96, v68, v97
	v_med3_f32 v105, v105, s41, v1
	v_mov_b32_e32 v97, v69
	v_cvt_pk_fp8_f32 v97, v104, v105
	v_med3_f32 v68, v120, s41, v1
	v_med3_f32 v110, v121, s41, v1
	v_cvt_pk_fp8_f32 v96, v68, v110 op_sel:[0,0,1]
	v_med3_f32 v68, v76, s41, v1
	v_med3_f32 v76, v77, s41, v1
	v_cvt_pk_fp8_f32 v97, v68, v76 op_sel:[0,0,1]
	v_add_co_u32_e32 v76, vcc, s38, v70
	s_waitcnt vmcnt(19)
	v_cvt_pk_f32_fp8_e32 v[130:131], v106
	v_addc_co_u32_e32 v77, vcc, 0, v71, vcc
	global_store_dwordx2 v[76:77], v[96:97], off offset:3584
	v_pk_fma_f32 v[96:97], v[62:63], v[136:137], v[14:15]
	v_cvt_pk_f32_fp8_sdwa v[116:117], v106 src0_sel:WORD_1
	v_pk_fma_f32 v[96:97], v[50:51], v[140:141], v[96:97]
	v_cvt_pk_f32_fp8_e32 v[110:111], v107
	v_pk_fma_f32 v[134:135], v[34:35], v[130:131], v[96:97]
	v_cvt_pk_f32_fp8_sdwa v[76:77], v107 src0_sel:WORD_1
	v_mul_f32_e32 v68, 0xbfb8aa3b, v134
	v_exp_f32_e32 v68, v68
	v_mul_f32_e32 v96, 0xbfb8aa3b, v135
	v_exp_f32_e32 v136, v96
	s_waitcnt vmcnt(19)
	v_cvt_pk_f32_fp8_e32 v[120:121], v102
	v_add_f32_e32 v68, 1.0, v68
	v_cvt_pk_f32_fp8_sdwa v[106:107], v102 src0_sel:WORD_1
	v_rcp_f32_e32 v102, v68
	v_add_f32_e32 v68, 1.0, v136
	v_cvt_pk_f32_fp8_e32 v[104:105], v103
	v_cvt_pk_f32_fp8_sdwa v[96:97], v103 src0_sel:WORD_1
	v_rcp_f32_e32 v103, v68
	v_pk_fma_f32 v[126:127], v[64:65], v[126:127], v[16:17]
	v_pk_fma_f32 v[132:133], v[58:59], v[132:133], v[10:11]
	v_pk_fma_f32 v[126:127], v[52:53], v[124:125], v[126:127]
	v_pk_mul_f32 v[102:103], v[134:135], v[102:103]
	v_pk_fma_f32 v[126:127], v[36:37], v[116:117], v[126:127]
	v_pk_fma_f32 v[132:133], v[42:43], v[128:129], v[132:133]
	v_mul_f32_e32 v68, 0xbfb8aa3b, v126
	v_exp_f32_e32 v68, v68
	v_mul_f32_e32 v134, 0xbfb8aa3b, v127
	v_exp_f32_e32 v134, v134
	v_pk_fma_f32 v[132:133], v[26:27], v[120:121], v[132:133]
	v_add_f32_e32 v68, 1.0, v68
	v_pk_mul_f32 v[132:133], v[132:133], 4.0 op_sel_hi:[1,0]
	v_pk_fma_f32 v[112:113], v[54:55], v[112:113], v[6:7]
	v_pk_mul_f32 v[102:103], v[132:133], v[102:103]
	v_rcp_f32_e32 v132, v68
	v_add_f32_e32 v68, 1.0, v134
	v_rcp_f32_e32 v133, v68
	v_pk_fma_f32 v[112:113], v[38:39], v[118:119], v[112:113]
	v_pk_fma_f32 v[122:123], v[60:61], v[122:123], v[12:13]
	v_pk_fma_f32 v[112:113], v[22:23], v[110:111], v[112:113]
	v_pk_mul_f32 v[126:127], v[126:127], v[132:133]
	v_mul_f32_e32 v68, 0xbfb8aa3b, v112
	v_exp_f32_e32 v68, v68
	v_mul_f32_e32 v132, 0xbfb8aa3b, v113
	v_exp_f32_e32 v132, v132
	v_pk_fma_f32 v[122:123], v[44:45], v[114:115], v[122:123]
	v_add_f32_e32 v68, 1.0, v68
	v_pk_fma_f32 v[122:123], v[28:29], v[106:107], v[122:123]
	v_pk_fma_f32 v[84:85], v[56:57], v[84:85], v[8:9]
	v_pk_mul_f32 v[122:123], v[122:123], 4.0 op_sel_hi:[1,0]
	v_pk_fma_f32 v[84:85], v[40:41], v[80:81], v[84:85]
	v_pk_mul_f32 v[122:123], v[122:123], v[126:127]
	v_rcp_f32_e32 v126, v68
	v_add_f32_e32 v68, 1.0, v132
	v_rcp_f32_e32 v127, v68
	v_pk_fma_f32 v[84:85], v[24:25], v[76:77], v[84:85]
	v_pk_fma_f32 v[108:109], v[46:47], v[108:109], v[2:3]
	v_mul_f32_e32 v68, 0xbfb8aa3b, v84
	v_pk_mul_f32 v[112:113], v[112:113], v[126:127]
	v_exp_f32_e32 v68, v68
	v_mul_f32_e32 v126, 0xbfb8aa3b, v85
	v_exp_f32_e32 v126, v126
	v_pk_fma_f32 v[108:109], v[30:31], v[100:101], v[108:109]
	v_add_f32_e32 v68, 1.0, v68
	v_pk_fma_f32 v[108:109], v[18:19], v[104:105], v[108:109]
	v_pk_fma_f32 v[88:89], v[48:49], v[88:89], v[4:5]
	v_pk_mul_f32 v[108:109], v[108:109], 4.0 op_sel_hi:[1,0]
	v_pk_fma_f32 v[88:89], v[32:33], v[92:93], v[88:89]
	v_pk_mul_f32 v[108:109], v[108:109], v[112:113]
	v_rcp_f32_e32 v112, v68
	v_add_f32_e32 v68, 1.0, v126
	v_rcp_f32_e32 v113, v68
	v_pk_fma_f32 v[88:89], v[20:21], v[96:97], v[88:89]
	v_med3_f32 v68, v102, s41, v1
	v_pk_mul_f32 v[88:89], v[88:89], 4.0 op_sel_hi:[1,0]
	v_pk_mul_f32 v[84:85], v[84:85], v[112:113]
	v_med3_f32 v102, v123, s41, v1
	v_pk_mul_f32 v[84:85], v[88:89], v[84:85]
	v_med3_f32 v89, v103, s41, v1
	v_mov_b32_e32 v88, v69
	v_cvt_pk_fp8_f32 v88, v68, v89
	v_med3_f32 v103, v108, s41, v1
	v_med3_f32 v108, v109, s41, v1
	v_mov_b32_e32 v89, v69
	v_cvt_pk_fp8_f32 v89, v103, v108
	v_med3_f32 v68, v122, s41, v1
	v_cvt_pk_fp8_f32 v88, v68, v102 op_sel:[0,0,1]
	v_med3_f32 v68, v84, s41, v1
	v_med3_f32 v84, v85, s41, v1
	v_cvt_pk_fp8_f32 v89, v68, v84 op_sel:[0,0,1]
	v_add_co_u32_e32 v84, vcc, s73, v70
	s_waitcnt vmcnt(18)
	v_cvt_pk_f32_fp8_e32 v[126:127], v98
	v_addc_co_u32_e32 v85, vcc, 0, v71, vcc
	global_store_dwordx2 v[84:85], v[88:89], off offset:2304
	v_pk_fma_f32 v[88:89], v[62:63], v[140:141], v[14:15]
	v_cvt_pk_f32_fp8_sdwa v[112:113], v98 src0_sel:WORD_1
	v_pk_fma_f32 v[88:89], v[50:51], v[130:131], v[88:89]
	s_waitcnt vmcnt(18)
	v_cvt_pk_f32_fp8_e32 v[122:123], v94
	v_pk_fma_f32 v[132:133], v[34:35], v[126:127], v[88:89]
	v_cvt_pk_f32_fp8_sdwa v[108:109], v94 src0_sel:WORD_1
	v_mul_f32_e32 v68, 0xbfb8aa3b, v132
	v_exp_f32_e32 v68, v68
	v_mul_f32_e32 v88, 0xbfb8aa3b, v133
	v_exp_f32_e32 v134, v88
	v_cvt_pk_f32_fp8_e32 v[102:103], v99
	v_add_f32_e32 v68, 1.0, v68
	v_rcp_f32_e32 v94, v68
	v_add_f32_e32 v68, 1.0, v134
	v_cvt_pk_f32_fp8_sdwa v[84:85], v99 src0_sel:WORD_1
	v_cvt_pk_f32_fp8_e32 v[98:99], v95
	v_cvt_pk_f32_fp8_sdwa v[88:89], v95 src0_sel:WORD_1
	v_rcp_f32_e32 v95, v68
	v_pk_fma_f32 v[124:125], v[64:65], v[124:125], v[16:17]
	v_pk_fma_f32 v[128:129], v[58:59], v[128:129], v[10:11]
	v_pk_fma_f32 v[124:125], v[52:53], v[116:117], v[124:125]
	v_pk_mul_f32 v[94:95], v[132:133], v[94:95]
	v_pk_fma_f32 v[124:125], v[36:37], v[112:113], v[124:125]
	v_pk_fma_f32 v[128:129], v[42:43], v[120:121], v[128:129]
	v_mul_f32_e32 v68, 0xbfb8aa3b, v124
	v_exp_f32_e32 v68, v68
	v_mul_f32_e32 v132, 0xbfb8aa3b, v125
	v_exp_f32_e32 v132, v132
	v_pk_fma_f32 v[128:129], v[26:27], v[122:123], v[128:129]
	v_add_f32_e32 v68, 1.0, v68
	v_pk_mul_f32 v[128:129], v[128:129], 4.0 op_sel_hi:[1,0]
	v_pk_fma_f32 v[118:119], v[54:55], v[118:119], v[6:7]
	v_pk_mul_f32 v[94:95], v[128:129], v[94:95]
	v_rcp_f32_e32 v128, v68
	v_add_f32_e32 v68, 1.0, v132
	v_rcp_f32_e32 v129, v68
	v_pk_fma_f32 v[118:119], v[38:39], v[110:111], v[118:119]
	v_pk_fma_f32 v[114:115], v[60:61], v[114:115], v[12:13]
	v_pk_fma_f32 v[118:119], v[22:23], v[102:103], v[118:119]
	v_pk_mul_f32 v[124:125], v[124:125], v[128:129]
	v_mul_f32_e32 v68, 0xbfb8aa3b, v118
	v_exp_f32_e32 v68, v68
	v_mul_f32_e32 v128, 0xbfb8aa3b, v119
	v_exp_f32_e32 v128, v128
	v_pk_fma_f32 v[114:115], v[44:45], v[106:107], v[114:115]
	v_add_f32_e32 v68, 1.0, v68
	v_pk_fma_f32 v[114:115], v[28:29], v[108:109], v[114:115]
	v_pk_fma_f32 v[80:81], v[56:57], v[80:81], v[8:9]
	v_pk_mul_f32 v[114:115], v[114:115], 4.0 op_sel_hi:[1,0]
	v_pk_fma_f32 v[80:81], v[40:41], v[76:77], v[80:81]
	v_pk_mul_f32 v[114:115], v[114:115], v[124:125]
	v_rcp_f32_e32 v124, v68
	v_add_f32_e32 v68, 1.0, v128
	v_rcp_f32_e32 v125, v68
	v_pk_fma_f32 v[80:81], v[24:25], v[84:85], v[80:81]
	v_pk_fma_f32 v[100:101], v[46:47], v[100:101], v[2:3]
	v_mul_f32_e32 v68, 0xbfb8aa3b, v80
	v_pk_mul_f32 v[118:119], v[118:119], v[124:125]
	v_exp_f32_e32 v68, v68
	v_mul_f32_e32 v124, 0xbfb8aa3b, v81
	v_exp_f32_e32 v124, v124
	v_pk_fma_f32 v[100:101], v[30:31], v[104:105], v[100:101]
	v_add_f32_e32 v68, 1.0, v68
	v_pk_fma_f32 v[100:101], v[18:19], v[98:99], v[100:101]
	v_pk_fma_f32 v[92:93], v[48:49], v[92:93], v[4:5]
	v_pk_mul_f32 v[100:101], v[100:101], 4.0 op_sel_hi:[1,0]
	v_pk_fma_f32 v[92:93], v[32:33], v[96:97], v[92:93]
	v_pk_mul_f32 v[100:101], v[100:101], v[118:119]
	v_rcp_f32_e32 v118, v68
	v_add_f32_e32 v68, 1.0, v124
	v_rcp_f32_e32 v119, v68
	v_pk_fma_f32 v[92:93], v[20:21], v[88:89], v[92:93]
	v_med3_f32 v68, v94, s41, v1
	v_pk_mul_f32 v[92:93], v[92:93], 4.0 op_sel_hi:[1,0]
	v_pk_mul_f32 v[80:81], v[80:81], v[118:119]
	s_waitcnt vmcnt(17)
	v_cvt_pk_f32_fp8_e32 v[118:119], v90
	v_pk_mul_f32 v[80:81], v[92:93], v[80:81]
	v_med3_f32 v93, v95, s41, v1
	v_mov_b32_e32 v92, v69
	v_cvt_pk_fp8_f32 v92, v68, v93
	v_med3_f32 v95, v100, s41, v1
	v_med3_f32 v100, v101, s41, v1
	v_mov_b32_e32 v93, v69
	v_cvt_pk_fp8_f32 v93, v95, v100
	v_pk_fma_f32 v[124:125], v[62:63], v[130:131], v[14:15]
	v_med3_f32 v68, v114, s41, v1
	v_med3_f32 v94, v115, s41, v1
	v_pk_fma_f32 v[124:125], v[50:51], v[126:127], v[124:125]
	v_cvt_pk_fp8_f32 v92, v68, v94 op_sel:[0,0,1]
	v_med3_f32 v68, v80, s41, v1
	v_med3_f32 v80, v81, s41, v1
	v_pk_fma_f32 v[124:125], v[34:35], v[118:119], v[124:125]
	v_cvt_pk_fp8_f32 v93, v68, v80 op_sel:[0,0,1]
	v_mul_f32_e32 v68, 0xbfb8aa3b, v124
	s_waitcnt vmcnt(16)
	v_cvt_pk_f32_fp8_e32 v[114:115], v86
	v_cvt_pk_f32_fp8_sdwa v[94:95], v86 src0_sel:WORD_1
	v_exp_f32_e32 v68, v68
	v_mul_f32_e32 v86, 0xbfb8aa3b, v125
	v_exp_f32_e32 v129, v86
	v_cvt_pk_f32_fp8_sdwa v[100:101], v90 src0_sel:WORD_1
	v_add_f32_e32 v68, 1.0, v68
	v_rcp_f32_e32 v128, v68
	v_add_f32_e32 v68, 1.0, v129
	v_rcp_f32_e32 v129, v68
	v_pk_fma_f32 v[116:117], v[64:65], v[116:117], v[16:17]
	v_pk_fma_f32 v[120:121], v[58:59], v[120:121], v[10:11]
	v_pk_fma_f32 v[116:117], v[52:53], v[112:113], v[116:117]
	v_pk_mul_f32 v[124:125], v[124:125], v[128:129]
	v_pk_fma_f32 v[116:117], v[36:37], v[100:101], v[116:117]
	v_add_co_u32_e32 v80, vcc, s39, v70
	v_mul_f32_e32 v68, 0xbfb8aa3b, v116
	v_exp_f32_e32 v68, v68
	v_mul_f32_e32 v128, 0xbfb8aa3b, v117
	v_exp_f32_e32 v128, v128
	v_pk_fma_f32 v[120:121], v[42:43], v[122:123], v[120:121]
	v_addc_co_u32_e32 v81, vcc, 0, v71, vcc
	v_pk_fma_f32 v[120:121], v[26:27], v[114:115], v[120:121]
	global_store_dwordx2 v[80:81], v[92:93], off offset:1024
	v_cvt_pk_f32_fp8_e32 v[92:93], v91
	v_pk_mul_f32 v[120:121], v[120:121], 4.0 op_sel_hi:[1,0]
	v_add_f32_e32 v68, 1.0, v68
	v_pk_mul_f32 v[120:121], v[120:121], v[124:125]
	v_rcp_f32_e32 v124, v68
	v_add_f32_e32 v68, 1.0, v128
	v_rcp_f32_e32 v125, v68
	v_pk_fma_f32 v[110:111], v[54:55], v[110:111], v[6:7]
	v_pk_fma_f32 v[106:107], v[60:61], v[106:107], v[12:13]
	v_pk_fma_f32 v[110:111], v[38:39], v[102:103], v[110:111]
	v_pk_mul_f32 v[116:117], v[116:117], v[124:125]
	v_pk_fma_f32 v[110:111], v[22:23], v[92:93], v[110:111]
	v_pk_fma_f32 v[106:107], v[44:45], v[108:109], v[106:107]
	v_mul_f32_e32 v68, 0xbfb8aa3b, v110
	v_exp_f32_e32 v68, v68
	v_mul_f32_e32 v124, 0xbfb8aa3b, v111
	v_exp_f32_e32 v124, v124
	v_pk_fma_f32 v[106:107], v[28:29], v[94:95], v[106:107]
	v_cvt_pk_f32_fp8_sdwa v[80:81], v91 src0_sel:WORD_1
	v_pk_mul_f32 v[106:107], v[106:107], 4.0 op_sel_hi:[1,0]
	v_add_f32_e32 v68, 1.0, v68
	v_pk_mul_f32 v[106:107], v[106:107], v[116:117]
	v_rcp_f32_e32 v116, v68
	v_add_f32_e32 v68, 1.0, v124
	v_rcp_f32_e32 v117, v68
	v_pk_fma_f32 v[76:77], v[56:57], v[76:77], v[8:9]
	v_cvt_pk_f32_fp8_e32 v[90:91], v87
	v_pk_fma_f32 v[76:77], v[40:41], v[84:85], v[76:77]
	v_pk_mul_f32 v[110:111], v[110:111], v[116:117]
	v_pk_fma_f32 v[76:77], v[24:25], v[80:81], v[76:77]
	v_pk_fma_f32 v[104:105], v[46:47], v[104:105], v[2:3]
	v_mul_f32_e32 v68, 0xbfb8aa3b, v76
	v_exp_f32_e32 v68, v68
	v_mul_f32_e32 v116, 0xbfb8aa3b, v77
	v_exp_f32_e32 v116, v116
	v_pk_fma_f32 v[104:105], v[30:31], v[98:99], v[104:105]
	v_add_f32_e32 v68, 1.0, v68
	v_pk_fma_f32 v[104:105], v[18:19], v[90:91], v[104:105]
	v_cvt_pk_f32_fp8_sdwa v[86:87], v87 src0_sel:WORD_1
	v_pk_mul_f32 v[104:105], v[104:105], 4.0 op_sel_hi:[1,0]
	v_pk_fma_f32 v[96:97], v[48:49], v[96:97], v[4:5]
	v_pk_mul_f32 v[104:105], v[104:105], v[110:111]
	v_rcp_f32_e32 v110, v68
	v_add_f32_e32 v68, 1.0, v116
	v_rcp_f32_e32 v111, v68
	v_pk_fma_f32 v[96:97], v[32:33], v[88:89], v[96:97]
	v_med3_f32 v68, v120, s41, v1
	v_pk_fma_f32 v[96:97], v[20:21], v[86:87], v[96:97]
	v_pk_mul_f32 v[76:77], v[76:77], v[110:111]
	v_pk_mul_f32 v[96:97], v[96:97], 4.0 op_sel_hi:[1,0]
	v_med3_f32 v104, v104, s41, v1
	v_pk_mul_f32 v[76:77], v[96:97], v[76:77]
	v_med3_f32 v97, v121, s41, v1
	v_mov_b32_e32 v96, v69
	v_cvt_pk_fp8_f32 v96, v68, v97
	v_med3_f32 v105, v105, s41, v1
	v_mov_b32_e32 v97, v69
	v_cvt_pk_fp8_f32 v97, v104, v105
	v_med3_f32 v68, v106, s41, v1
	v_med3_f32 v106, v107, s41, v1
	v_cvt_pk_fp8_f32 v96, v68, v106 op_sel:[0,0,1]
	v_med3_f32 v68, v76, s41, v1
	v_med3_f32 v76, v77, s41, v1
	v_cvt_pk_fp8_f32 v97, v68, v76 op_sel:[0,0,1]
	v_add_co_u32_e32 v76, vcc, s74, v70
	v_pk_fma_f32 v[120:121], v[62:63], v[126:127], v[14:15]
	s_nop 0
	v_addc_co_u32_e32 v77, vcc, 0, v71, vcc
	global_store_dwordx2 v[76:77], v[96:97], off offset:3840
	s_waitcnt vmcnt(17)
	v_cvt_pk_f32_fp8_e32 v[76:77], v82
	v_pk_fma_f32 v[120:121], v[50:51], v[118:119], v[120:121]
	s_waitcnt vmcnt(16)
	v_cvt_pk_f32_fp8_e32 v[106:107], v78
	v_cvt_pk_f32_fp8_sdwa v[110:111], v78 src0_sel:WORD_1
	v_pk_fma_f32 v[120:121], v[34:35], v[76:77], v[120:121]
	v_cvt_pk_f32_fp8_sdwa v[96:97], v82 src0_sel:WORD_1
	v_mul_f32_e32 v68, 0xbfb8aa3b, v120
	v_exp_f32_e32 v68, v68
	v_mul_f32_e32 v78, 0xbfb8aa3b, v121
	v_exp_f32_e32 v125, v78
	v_pk_fma_f32 v[112:113], v[64:65], v[112:113], v[16:17]
	v_add_f32_e32 v68, 1.0, v68
	v_rcp_f32_e32 v124, v68
	v_add_f32_e32 v68, 1.0, v125
	v_rcp_f32_e32 v125, v68
	v_pk_fma_f32 v[112:113], v[52:53], v[100:101], v[112:113]
	v_pk_fma_f32 v[122:123], v[58:59], v[122:123], v[10:11]
	v_pk_fma_f32 v[112:113], v[36:37], v[96:97], v[112:113]
	v_pk_mul_f32 v[120:121], v[120:121], v[124:125]
	v_mul_f32_e32 v68, 0xbfb8aa3b, v112
	v_exp_f32_e32 v68, v68
	v_mul_f32_e32 v124, 0xbfb8aa3b, v113
	v_exp_f32_e32 v124, v124
	v_pk_fma_f32 v[122:123], v[42:43], v[114:115], v[122:123]
	v_cvt_pk_f32_fp8_e32 v[104:105], v83
	v_pk_fma_f32 v[122:123], v[26:27], v[106:107], v[122:123]
	v_add_f32_e32 v68, 1.0, v68
	v_pk_mul_f32 v[122:123], v[122:123], 4.0 op_sel_hi:[1,0]
	v_pk_fma_f32 v[102:103], v[54:55], v[102:103], v[6:7]
	v_pk_mul_f32 v[120:121], v[122:123], v[120:121]
	v_rcp_f32_e32 v122, v68
	v_add_f32_e32 v68, 1.0, v124
	v_rcp_f32_e32 v123, v68
	v_pk_fma_f32 v[102:103], v[38:39], v[92:93], v[102:103]
	v_pk_fma_f32 v[108:109], v[60:61], v[108:109], v[12:13]
	v_pk_fma_f32 v[102:103], v[22:23], v[104:105], v[102:103]
	v_pk_mul_f32 v[112:113], v[112:113], v[122:123]
	v_mul_f32_e32 v68, 0xbfb8aa3b, v102
	v_exp_f32_e32 v68, v68
	v_mul_f32_e32 v122, 0xbfb8aa3b, v103
	v_exp_f32_e32 v122, v122
	v_pk_fma_f32 v[108:109], v[44:45], v[94:95], v[108:109]
	v_cvt_pk_f32_fp8_sdwa v[82:83], v83 src0_sel:WORD_1
; #define CV_LOAD(G_, V_, r0_) do { _Pragma("unroll") for (int i_ = 0; i_ < 8; ++i_) { G_[i_] = *(const GAS v2u*)(ap + (size_t)((r0_) + i_) * F2); V_[i_] = *(const GAS v2u*)(ap + (size_t)((r0_) + i_) * F2 + 128); } } while (0)
; __device__ __forceinline__ void conv_phase(Frame& F) {
;     ...
;     for (size_t idx = (size_t)F.gw * 64 + F.lane; idx < total; idx += (size_t)F.NGW * 64) {
;     ...
;         CV_LOAD(GA, VA, 0); CV_LOAD(GB, VB, 8); CV_COMP(GA, VA, 0); CV_LOAD(GA, VA, 16); CV_COMP(GB, VB, 8); CV_LOAD(GB, VB, 24); CV_COMP(GA, VA, 16); CV_COMP(GB, VB, 24);
	v_pk_fma_f32 v[108:109], v[28:29], v[110:111], v[108:109]
	v_add_f32_e32 v68, 1.0, v68
	v_pk_mul_f32 v[108:109], v[108:109], 4.0 op_sel_hi:[1,0]
	v_pk_fma_f32 v[84:85], v[56:57], v[84:85], v[8:9]
	v_pk_mul_f32 v[108:109], v[108:109], v[112:113]
	v_rcp_f32_e32 v112, v68
	v_add_f32_e32 v68, 1.0, v122
	v_rcp_f32_e32 v113, v68
	v_pk_fma_f32 v[84:85], v[40:41], v[80:81], v[84:85]
	v_cvt_pk_f32_fp8_e32 v[116:117], v79
	v_pk_fma_f32 v[84:85], v[24:25], v[82:83], v[84:85]
	v_pk_mul_f32 v[102:103], v[102:103], v[112:113]
	v_mul_f32_e32 v68, 0xbfb8aa3b, v84
	v_exp_f32_e32 v68, v68
	v_mul_f32_e32 v112, 0xbfb8aa3b, v85
	v_pk_fma_f32 v[98:99], v[46:47], v[98:99], v[2:3]
	v_exp_f32_e32 v112, v112
	v_pk_fma_f32 v[98:99], v[30:31], v[90:91], v[98:99]
	v_add_f32_e32 v68, 1.0, v68
	v_pk_fma_f32 v[98:99], v[18:19], v[116:117], v[98:99]
	v_cvt_pk_f32_fp8_sdwa v[78:79], v79 src0_sel:WORD_1
	v_pk_mul_f32 v[98:99], v[98:99], 4.0 op_sel_hi:[1,0]
	v_pk_fma_f32 v[88:89], v[48:49], v[88:89], v[4:5]
	v_pk_mul_f32 v[98:99], v[98:99], v[102:103]
	v_rcp_f32_e32 v102, v68
	v_add_f32_e32 v68, 1.0, v112
	v_rcp_f32_e32 v103, v68
	v_pk_fma_f32 v[88:89], v[32:33], v[86:87], v[88:89]
	v_med3_f32 v68, v120, s41, v1
	v_pk_fma_f32 v[88:89], v[20:21], v[78:79], v[88:89]
	v_pk_mul_f32 v[84:85], v[84:85], v[102:103]
	v_pk_mul_f32 v[88:89], v[88:89], 4.0 op_sel_hi:[1,0]
	v_med3_f32 v98, v98, s41, v1
	v_pk_mul_f32 v[84:85], v[88:89], v[84:85]
	v_med3_f32 v89, v121, s41, v1
	v_mov_b32_e32 v88, v69
	v_cvt_pk_fp8_f32 v88, v68, v89
	v_med3_f32 v99, v99, s41, v1
	v_mov_b32_e32 v89, v69
	v_cvt_pk_fp8_f32 v89, v98, v99
	v_med3_f32 v68, v108, s41, v1
	v_med3_f32 v102, v109, s41, v1
	v_cvt_pk_fp8_f32 v88, v68, v102 op_sel:[0,0,1]
	v_med3_f32 v68, v84, s41, v1
	v_med3_f32 v84, v85, s41, v1
	v_cvt_pk_fp8_f32 v89, v68, v84 op_sel:[0,0,1]
	v_add_co_u32_e32 v84, vcc, s40, v70
	v_pk_fma_f32 v[14:15], v[62:63], v[118:119], v[14:15]
	s_nop 0
	v_addc_co_u32_e32 v85, vcc, 0, v71, vcc
	global_store_dwordx2 v[84:85], v[88:89], off offset:2560
	s_waitcnt vmcnt(16)
	v_cvt_pk_f32_fp8_e32 v[84:85], v74
	v_pk_fma_f32 v[14:15], v[50:51], v[76:77], v[14:15]
	v_cvt_pk_f32_fp8_sdwa v[88:89], v74 src0_sel:WORD_1
	s_waitcnt vmcnt(15)
	v_cvt_pk_f32_fp8_e32 v[102:103], v72
	v_pk_fma_f32 v[14:15], v[34:35], v[84:85], v[14:15]
	v_pk_fma_f32 v[16:17], v[64:65], v[100:101], v[16:17]
	v_mul_f32_e32 v34, 0xbfb8aa3b, v14
	v_exp_f32_e32 v50, v34
	v_mul_f32_e32 v34, 0xbfb8aa3b, v15
	v_exp_f32_e32 v51, v34
	v_pk_fma_f32 v[10:11], v[58:59], v[114:115], v[10:11]
	v_pk_fma_f32 v[16:17], v[52:53], v[96:97], v[16:17]
	v_add_f32_e32 v50, 1.0, v50
	v_add_f32_e32 v51, 1.0, v51
	v_pk_fma_f32 v[10:11], v[42:43], v[106:107], v[10:11]
	v_pk_fma_f32 v[16:17], v[36:37], v[88:89], v[16:17]
	v_rcp_f32_e32 v50, v50
	v_rcp_f32_e32 v51, v51
	v_pk_fma_f32 v[10:11], v[26:27], v[102:103], v[10:11]
	v_mul_f32_e32 v26, 0xbfb8aa3b, v16
	v_mul_f32_e32 v27, 0xbfb8aa3b, v17
	v_exp_f32_e32 v26, v26
	v_exp_f32_e32 v27, v27
	v_pk_mul_f32 v[14:15], v[14:15], v[50:51]
	v_pk_mul_f32 v[10:11], v[10:11], 4.0 op_sel_hi:[1,0]
	v_cvt_pk_f32_fp8_e32 v[98:99], v75
	v_pk_mul_f32 v[10:11], v[10:11], v[14:15]
	v_add_f32_e32 v14, 1.0, v26
	v_add_f32_e32 v15, 1.0, v27
	v_rcp_f32_e32 v14, v14
	v_rcp_f32_e32 v15, v15
	v_pk_fma_f32 v[6:7], v[54:55], v[92:93], v[6:7]
	v_cvt_pk_f32_fp8_sdwa v[108:109], v72 src0_sel:WORD_1
	v_pk_fma_f32 v[6:7], v[38:39], v[104:105], v[6:7]
	v_pk_mul_f32 v[14:15], v[16:17], v[14:15]
	v_pk_fma_f32 v[6:7], v[22:23], v[98:99], v[6:7]
	v_pk_fma_f32 v[12:13], v[60:61], v[94:95], v[12:13]
	v_mul_f32_e32 v16, 0xbfb8aa3b, v6
	v_mul_f32_e32 v17, 0xbfb8aa3b, v7
	v_exp_f32_e32 v16, v16
	v_exp_f32_e32 v17, v17
	v_pk_fma_f32 v[12:13], v[44:45], v[110:111], v[12:13]
	v_cvt_pk_f32_fp8_sdwa v[74:75], v75 src0_sel:WORD_1
	v_pk_fma_f32 v[12:13], v[28:29], v[108:109], v[12:13]
	v_pk_fma_f32 v[8:9], v[56:57], v[80:81], v[8:9]
	v_pk_mul_f32 v[12:13], v[12:13], 4.0 op_sel_hi:[1,0]
	v_pk_fma_f32 v[8:9], v[40:41], v[82:83], v[8:9]
	v_pk_mul_f32 v[12:13], v[12:13], v[14:15]
	v_add_f32_e32 v14, 1.0, v16
	v_add_f32_e32 v15, 1.0, v17
	v_rcp_f32_e32 v14, v14
	v_rcp_f32_e32 v15, v15
	v_cvt_pk_f32_fp8_e32 v[112:113], v73
	v_pk_fma_f32 v[8:9], v[24:25], v[74:75], v[8:9]
	v_pk_fma_f32 v[2:3], v[46:47], v[90:91], v[2:3]
	v_pk_mul_f32 v[6:7], v[6:7], v[14:15]
	v_mul_f32_e32 v14, 0xbfb8aa3b, v8
	v_mul_f32_e32 v15, 0xbfb8aa3b, v9
	v_exp_f32_e32 v14, v14
	v_exp_f32_e32 v15, v15
	v_pk_fma_f32 v[2:3], v[30:31], v[116:117], v[2:3]
	v_cvt_pk_f32_fp8_sdwa v[34:35], v73 src0_sel:WORD_1
	v_pk_fma_f32 v[2:3], v[18:19], v[112:113], v[2:3]
	v_pk_fma_f32 v[4:5], v[48:49], v[86:87], v[4:5]
	v_pk_mul_f32 v[2:3], v[2:3], 4.0 op_sel_hi:[1,0]
	v_pk_fma_f32 v[4:5], v[32:33], v[78:79], v[4:5]
	v_pk_mul_f32 v[2:3], v[2:3], v[6:7]
	v_add_f32_e32 v6, 1.0, v14
	v_add_f32_e32 v7, 1.0, v15
	v_rcp_f32_e32 v6, v6
	v_rcp_f32_e32 v7, v7
	v_pk_fma_f32 v[4:5], v[20:21], v[34:35], v[4:5]
	v_med3_f32 v2, v2, s41, v1
	v_pk_mul_f32 v[4:5], v[4:5], 4.0 op_sel_hi:[1,0]
	v_pk_mul_f32 v[6:7], v[8:9], v[6:7]
	v_med3_f32 v8, v11, s41, v1
	v_pk_mul_f32 v[4:5], v[4:5], v[6:7]
	v_med3_f32 v7, v10, s41, v1
	v_mov_b32_e32 v6, v69
	v_cvt_pk_fp8_f32 v6, v7, v8
	v_med3_f32 v3, v3, s41, v1
	v_mov_b32_e32 v7, v69
	v_cvt_pk_fp8_f32 v7, v2, v3
	v_med3_f32 v8, v12, s41, v1
	v_med3_f32 v9, v13, s41, v1
	v_med3_f32 v2, v4, s41, v1
	v_med3_f32 v3, v5, s41, v1
	v_cvt_pk_fp8_f32 v6, v8, v9 op_sel:[0,0,1]
	v_cvt_pk_fp8_f32 v7, v2, v3 op_sel:[0,0,1]
	v_add_co_u32_e32 v2, vcc, 0x53000, v70
	v_lshl_add_u64 v[66:67], v[66:67], 0, s[18:19]
	s_nop 0
	v_addc_co_u32_e32 v3, vcc, 0, v71, vcc
	global_store_dwordx2 v[2:3], v[6:7], off offset:1280
	s_mov_b64 s[22:23], 0x55fff
	v_cmp_lt_u64_e32 vcc, s[22:23], v[66:67]
	s_or_b64 s[16:17], vcc, s[16:17]
	s_andn2_b64 exec, exec, s[16:17]
	s_cbranch_execz .LBB0_2571
; #define GAS __attribute__((address_space(1)))
; __device__ __forceinline__ void conv_phase(Frame& F) {
;     ...
;     for (size_t idx = (size_t)F.gw * 64 + F.lane; idx < total; idx += (size_t)F.NGW * 64) {
;         const int c8 = (int)(idx % C8), tb = (int)(idx / C8), ch = 8 * c8, t0 = tb * TB;
;         const int acol = (ch >> 7) * 256 + (ch & 127);
;         f32x2 wg[3][4], wv[3][4], bg[4], bv[4];
; #pragma unroll
;         for (int j = 0; j < 3; ++j) { const f32x4 a = *(const GAS f32x4*)(F.cvw + (size_t)j * F2 + ch) * (1.f / S_A), b = *(const GAS f32x4*)(F.cvw + (size_t)j * F2 + ch + 4) * (1.f / S_A);
;             const f32x4 c = *(const GAS f32x4*)(F.cvw + (size_t)j * F2 + DFF + ch) * (1.f / S_A), d = *(const GAS f32x4*)(F.cvw + (size_t)j * F2 + DFF + ch + 4) * (1.f / S_A);
;             wg[j][0] = (f32x2){a.x, a.y}; wg[j][1] = (f32x2){a.z, a.w}; wg[j][2] = (f32x2){b.x, b.y}; wg[j][3] = (f32x2){b.z, b.w};
;             wv[j][0] = (f32x2){c.x, c.y}; wv[j][1] = (f32x2){c.z, c.w}; wv[j][2] = (f32x2){d.x, d.y}; wv[j][3] = (f32x2){d.z, d.w}; }
;         { const f32x4 a = *(const GAS f32x4*)(F.cvb + ch), b = *(const GAS f32x4*)(F.cvb + ch + 4), c = *(const GAS f32x4*)(F.cvb + DFF + ch), d = *(const GAS f32x4*)(F.cvb + DFF + ch + 4);
;           bg[0] = (f32x2){a.x, a.y}; bg[1] = (f32x2){a.z, a.w}; bg[2] = (f32x2){b.x, b.y}; bg[3] = (f32x2){b.z, b.w}; bv[0] = (f32x2){c.x, c.y}; bv[1] = (f32x2){c.z, c.w}; bv[2] = (f32x2){d.x, d.y}; bv[3] = (f32x2){d.z, d.w}; }
;         f32x2 g1[4], g2[4], v1[4], v2[4];
;         const bool first = (t0 & (SEQ - 1)) == 0;
;         const unsigned char* ap = (const unsigned char*)F.A + (size_t)t0 * F2 + acol;
;         if (first) {
; #pragma unroll
;             for (int e = 0; e < 4; ++e) { g1[e] = g2[e] = v1[e] = v2[e] = (f32x2){0.f, 0.f}; }
;         } else {
;             const v2u ga = *(const GAS v2u*)(ap - F2), gb = *(const GAS v2u*)(ap - 2 * (size_t)F2), va = *(const GAS v2u*)(ap - F2 + 128), vb = *(const GAS v2u*)(ap - 2 * (size_t)F2 + 128);
;             unpack8_fp8(ga, g1); unpack8_fp8(gb, g2); unpack8_fp8(va, v1); unpack8_fp8(vb, v2);
;         }
.LBB0_2569:
	v_mul_hi_u32 v71, v66, s21
	v_lshrrev_b32_e32 v174, 8, v71
	v_mul_u32_u24_e32 v2, 0x560, v174
	v_sub_u32_e32 v70, v66, v2
	v_readlane_b32 s84, v249, 0
	v_lshlrev_b32_e32 v68, 3, v70
	v_readlane_b32 s85, v249, 1
	v_lshlrev_b64 v[2:3], 2, v[68:69]
	v_readlane_b32 s86, v249, 2
	v_readlane_b32 s87, v249, 3
	s_mov_b64 s[76:77], s[84:85]
	v_lshl_add_u64 v[4:5], s[76:77], 0, v[2:3]
	global_load_dwordx4 v[54:57], v[4:5], off offset:16
	global_load_dwordx4 v[62:65], v[4:5], off
	v_lshl_add_u64 v[4:5], s[2:3], 0, v[2:3]
	global_load_dwordx4 v[46:49], v[4:5], off offset:16
	global_load_dwordx4 v[58:61], v[4:5], off
	v_lshl_add_u64 v[4:5], s[6:7], 0, v[2:3]
	global_load_dwordx4 v[38:41], v[4:5], off offset:16
	global_load_dwordx4 v[50:53], v[4:5], off
	v_lshl_add_u64 v[4:5], s[8:9], 0, v[2:3]
	global_load_dwordx4 v[30:33], v[4:5], off offset:16
	global_load_dwordx4 v[42:45], v[4:5], off
	v_lshl_add_u64 v[4:5], s[10:11], 0, v[2:3]
	s_mov_b64 s[78:79], s[86:87]
	global_load_dwordx4 v[22:25], v[4:5], off offset:16
	global_load_dwordx4 v[34:37], v[4:5], off
	v_lshl_add_u64 v[4:5], s[12:13], 0, v[2:3]
	global_load_dwordx4 v[18:21], v[4:5], off offset:16
	global_load_dwordx4 v[26:29], v[4:5], off
	v_lshl_add_u64 v[4:5], s[78:79], 0, v[2:3]
	v_lshl_add_u64 v[10:11], s[14:15], 0, v[2:3]
	global_load_dwordx4 v[6:9], v[4:5], off offset:16
	global_load_dwordx4 v[14:17], v[4:5], off
	s_nop 0
	global_load_dwordx4 v[2:5], v[10:11], off offset:16
	s_nop 0
	global_load_dwordx4 v[10:13], v[10:11], off
	v_lshlrev_b32_e32 v70, 4, v70
	v_and_b32_e32 v72, 0x78, v68
	v_readlane_b32 s22, v248, 12
	v_and_or_b32 v70, v70, s24, v72
	v_bfe_u32 v71, v71, 8, 6
	v_mul_u32_u24_e32 v72, 0xac000, v174
	v_mov_b32_e32 v73, v69
	v_readlane_b32 s23, v248, 13
	v_cmp_ne_u32_e32 vcc, 0, v71
	v_mov_b32_e32 v71, v69
	v_lshl_add_u64 v[72:73], s[22:23], 0, v[72:73]
	v_lshl_add_u64 v[72:73], v[72:73], 0, v[70:71]
	v_mov_b32_e32 v108, v69
	v_mov_b32_e32 v109, v69
	v_mov_b32_e32 v116, v69
	v_mov_b32_e32 v117, v69
	v_mov_b32_e32 v124, v69
	v_mov_b32_e32 v125, v69
	v_mov_b32_e32 v132, v69
	v_mov_b32_e32 v133, v69
	v_mov_b32_e32 v70, v69
	v_mov_b32_e32 v144, v69
	v_mov_b32_e32 v145, v69
	v_mov_b32_e32 v148, v69
	v_mov_b32_e32 v149, v69
	v_mov_b32_e32 v152, v69
	v_mov_b32_e32 v153, v69
	v_mov_b32_e32 v112, v69
	v_mov_b32_e32 v113, v69
	v_mov_b32_e32 v120, v69
	v_mov_b32_e32 v121, v69
	v_mov_b32_e32 v128, v69
	v_mov_b32_e32 v129, v69
	v_mov_b32_e32 v136, v69
	v_mov_b32_e32 v137, v69
	v_mov_b32_e32 v142, v69
	v_mov_b32_e32 v143, v69
	v_mov_b32_e32 v146, v69
	v_mov_b32_e32 v147, v69
	v_mov_b32_e32 v150, v69
	v_mov_b32_e32 v151, v69
	v_mov_b32_e32 v158, v69
	v_mov_b32_e32 v159, v69
	v_readlane_b32 s88, v249, 4
	v_readlane_b32 s89, v249, 5
	v_readlane_b32 s90, v249, 6
	v_readlane_b32 s91, v249, 7
	s_and_saveexec_b64 s[22:23], vcc
	s_cbranch_execz .LBB0_2568
	v_add_co_u32_e32 v70, vcc, 0xffffb000, v72
	s_nop 1
	v_addc_co_u32_e32 v71, vcc, -1, v73, vcc
	v_add_co_u32_e32 v76, vcc, 0xffff6000, v72
	global_load_dwordx2 v[74:75], v[70:71], off offset:-1536 nt
	s_nop 0
	v_addc_co_u32_e32 v77, vcc, -1, v73, vcc
	global_load_dwordx2 v[78:79], v[76:77], off offset:-3072 nt
	s_nop 0
	global_load_dwordx2 v[76:77], v[76:77], off offset:-2944 nt
	s_nop 0
	global_load_dwordx2 v[80:81], v[70:71], off offset:-1408 nt
	s_waitcnt vmcnt(3)
	v_cvt_pk_f32_fp8_e32 v[132:133], v74
	v_cvt_pk_f32_fp8_sdwa v[124:125], v74 src0_sel:WORD_1
	v_cvt_pk_f32_fp8_e32 v[116:117], v75
	v_cvt_pk_f32_fp8_sdwa v[108:109], v75 src0_sel:WORD_1
	s_waitcnt vmcnt(2)
	v_cvt_pk_f32_fp8_e32 v[152:153], v78
	v_cvt_pk_f32_fp8_sdwa v[148:149], v78 src0_sel:WORD_1
	v_cvt_pk_f32_fp8_e32 v[144:145], v79
	v_cvt_pk_f32_fp8_sdwa v[70:71], v79 src0_sel:WORD_1
	s_waitcnt vmcnt(0)
	v_cvt_pk_f32_fp8_e32 v[136:137], v80
	v_cvt_pk_f32_fp8_sdwa v[128:129], v80 src0_sel:WORD_1
	v_cvt_pk_f32_fp8_e32 v[120:121], v81
	v_cvt_pk_f32_fp8_sdwa v[112:113], v81 src0_sel:WORD_1
	v_cvt_pk_f32_fp8_e32 v[158:159], v76
	v_cvt_pk_f32_fp8_sdwa v[150:151], v76 src0_sel:WORD_1
	v_cvt_pk_f32_fp8_e32 v[146:147], v77
	v_cvt_pk_f32_fp8_sdwa v[142:143], v77 src0_sel:WORD_1
	s_branch .LBB0_2568
